# speedup vs baseline: 1.0058x; 1.0058x over previous
.LBB0_15:
.LBB0_16:
	s_mov_b32 s27, s19
	v_mov_b32_e32 v1, 0x42c80000
	v_mov_b32_e32 v0, 0
	s_add_i32 s4, s34, -2
	s_max_i32 s4, s4, 0
	s_mul_i32 s5, s4, 0x804
	s_add_i32 s5, s5, s35
	s_add_i32 s6, s5, 0x101004
	s_add_i32 s7, s5, 0x202008
	s_add_i32 s8, s5, 0x30300c
	s_mul_i32 s9, s4, 0x180c
	s_add_i32 s9, s9, s33
	buffer_load_dword v2, v28, s[16:19], s5 offen nt
	buffer_load_dword v3, v28, s[16:19], s6 offen nt
	buffer_load_dword v4, v28, s[16:19], s7 offen nt
	buffer_load_dword v5, v28, s[16:19], s8 offen nt
	buffer_load_dwordx3 v[8:10], v27, s[24:27], s9 offen nt
	s_add_i32 s4, s34, -1
	s_max_i32 s4, s4, 0
	s_mul_i32 s5, s4, 0x804
	s_add_i32 s5, s5, s35
	s_add_i32 s6, s5, 0x101004
	s_add_i32 s7, s5, 0x202008
	s_add_i32 s8, s5, 0x30300c
	s_mul_i32 s9, s4, 0x180c
	s_add_i32 s9, s9, s33
	buffer_load_dword v6, v28, s[16:19], s5 offen nt
	buffer_load_dword v7, v28, s[16:19], s6 offen nt
	buffer_load_dword v12, v28, s[16:19], s7 offen nt
	buffer_load_dword v13, v28, s[16:19], s8 offen nt
	buffer_load_dwordx3 v[32:34], v27, s[24:27], s9 offen nt
	s_add_i32 s4, s34, 0
	s_min_i32 s4, s4, 0x200
	s_mul_i32 s5, s4, 0x804
	s_add_i32 s5, s5, s35
	s_add_i32 s6, s5, 0x101004
	s_add_i32 s7, s5, 0x202008
	s_add_i32 s8, s5, 0x30300c
	s_mul_i32 s9, s4, 0x180c
	s_add_i32 s9, s9, s33
	buffer_load_dword v14, v28, s[16:19], s5 offen nt
	buffer_load_dword v15, v28, s[16:19], s6 offen nt
	buffer_load_dword v16, v28, s[16:19], s7 offen nt
	buffer_load_dword v17, v28, s[16:19], s8 offen nt
	buffer_load_dwordx3 v[36:38], v27, s[24:27], s9 offen nt
	s_waitcnt vmcnt(10)
	v_pk_mul_f32 v[20:21], v[2:3], v[8:9] op_sel_hi:[1,0]
	v_pk_mul_f32 v[24:25], v[4:5], v[8:9] op_sel_hi:[1,0]
	v_pk_mul_f32 v[30:31], v[2:3], v[8:9] op_sel:[0,1]
	v_pk_mul_f32 v[40:41], v[4:5], v[8:9] op_sel:[0,1]
	v_pk_mul_f32 v[42:43], v[2:3], v[10:11] op_sel_hi:[1,0]
	v_pk_mul_f32 v[44:45], v[4:5], v[10:11] op_sel_hi:[1,0]
	v_add_f32_dpp v46, v2, v2 wave_shr:1 row_mask:0xf bank_mask:0xf bound_ctrl:1
	v_add_f32_dpp v47, v3, v3 wave_shr:1 row_mask:0xf bank_mask:0xf bound_ctrl:1
	v_add_f32_dpp v48, v4, v4 wave_shr:1 row_mask:0xf bank_mask:0xf bound_ctrl:1
	v_add_f32_dpp v49, v5, v5 wave_shr:1 row_mask:0xf bank_mask:0xf bound_ctrl:1
	v_add_f32_dpp v50, v20, v20 wave_shr:1 row_mask:0xf bank_mask:0xf bound_ctrl:1
	v_add_f32_dpp v51, v21, v21 wave_shr:1 row_mask:0xf bank_mask:0xf bound_ctrl:1
	v_add_f32_dpp v52, v24, v24 wave_shr:1 row_mask:0xf bank_mask:0xf bound_ctrl:1
	v_add_f32_dpp v53, v25, v25 wave_shr:1 row_mask:0xf bank_mask:0xf bound_ctrl:1
	v_add_f32_dpp v54, v30, v30 wave_shr:1 row_mask:0xf bank_mask:0xf bound_ctrl:1
	v_add_f32_dpp v55, v31, v31 wave_shr:1 row_mask:0xf bank_mask:0xf bound_ctrl:1
	v_add_f32_dpp v56, v40, v40 wave_shr:1 row_mask:0xf bank_mask:0xf bound_ctrl:1
	v_add_f32_dpp v57, v41, v41 wave_shr:1 row_mask:0xf bank_mask:0xf bound_ctrl:1
	v_add_f32_dpp v58, v42, v42 wave_shr:1 row_mask:0xf bank_mask:0xf bound_ctrl:1
	v_add_f32_dpp v59, v43, v43 wave_shr:1 row_mask:0xf bank_mask:0xf bound_ctrl:1
	v_add_f32_dpp v60, v44, v44 wave_shr:1 row_mask:0xf bank_mask:0xf bound_ctrl:1
	v_add_f32_dpp v61, v45, v45 wave_shr:1 row_mask:0xf bank_mask:0xf bound_ctrl:1
	v_add_f32_dpp v46, v2, v46 wave_shl:1 row_mask:0xf bank_mask:0xf bound_ctrl:1
	v_add_f32_dpp v47, v3, v47 wave_shl:1 row_mask:0xf bank_mask:0xf bound_ctrl:1
	v_add_f32_dpp v48, v4, v48 wave_shl:1 row_mask:0xf bank_mask:0xf bound_ctrl:1
	v_add_f32_dpp v49, v5, v49 wave_shl:1 row_mask:0xf bank_mask:0xf bound_ctrl:1
	v_add_f32_dpp v50, v20, v50 wave_shl:1 row_mask:0xf bank_mask:0xf bound_ctrl:1
	v_add_f32_dpp v51, v21, v51 wave_shl:1 row_mask:0xf bank_mask:0xf bound_ctrl:1
	v_add_f32_dpp v52, v24, v52 wave_shl:1 row_mask:0xf bank_mask:0xf bound_ctrl:1
	v_add_f32_dpp v53, v25, v53 wave_shl:1 row_mask:0xf bank_mask:0xf bound_ctrl:1
	v_add_f32_dpp v54, v30, v54 wave_shl:1 row_mask:0xf bank_mask:0xf bound_ctrl:1
	v_add_f32_dpp v55, v31, v55 wave_shl:1 row_mask:0xf bank_mask:0xf bound_ctrl:1
	v_add_f32_dpp v56, v40, v56 wave_shl:1 row_mask:0xf bank_mask:0xf bound_ctrl:1
	v_add_f32_dpp v57, v41, v57 wave_shl:1 row_mask:0xf bank_mask:0xf bound_ctrl:1
	v_add_f32_dpp v58, v42, v58 wave_shl:1 row_mask:0xf bank_mask:0xf bound_ctrl:1
	v_add_f32_dpp v59, v43, v59 wave_shl:1 row_mask:0xf bank_mask:0xf bound_ctrl:1
	v_add_f32_dpp v60, v44, v60 wave_shl:1 row_mask:0xf bank_mask:0xf bound_ctrl:1
	v_add_f32_dpp v61, v45, v61 wave_shl:1 row_mask:0xf bank_mask:0xf bound_ctrl:1
	s_barrier
	s_add_i32 s4, s34, 1
	s_min_i32 s4, s4, 0x200
	s_mul_i32 s5, s4, 0x804
	s_add_i32 s5, s5, s35
	s_add_i32 s6, s5, 0x101004
	s_add_i32 s7, s5, 0x202008
	s_add_i32 s8, s5, 0x30300c
	s_mul_i32 s9, s4, 0x180c
	s_add_i32 s9, s9, s33
	buffer_load_dword v20, v28, s[16:19], s5 offen nt
	buffer_load_dword v21, v28, s[16:19], s6 offen nt
	buffer_load_dword v24, v28, s[16:19], s7 offen nt
	buffer_load_dword v25, v28, s[16:19], s8 offen nt
	buffer_load_dwordx3 v[40:42], v27, s[24:27], s9 offen nt
	s_waitcnt vmcnt(10)
	v_pk_mul_f32 v[30:31], v[6:7], v[32:33] op_sel_hi:[1,0]
	v_pk_mul_f32 v[44:45], v[12:13], v[32:33] op_sel_hi:[1,0]
	v_pk_mul_f32 v[62:63], v[6:7], v[32:33] op_sel:[0,1]
	v_pk_mul_f32 v[64:65], v[12:13], v[32:33] op_sel:[0,1]
	v_pk_mul_f32 v[66:67], v[6:7], v[34:35] op_sel_hi:[1,0]
	v_pk_mul_f32 v[68:69], v[12:13], v[34:35] op_sel_hi:[1,0]
	v_add_f32_dpp v70, v6, v6 wave_shr:1 row_mask:0xf bank_mask:0xf bound_ctrl:1
	v_add_f32_dpp v71, v7, v7 wave_shr:1 row_mask:0xf bank_mask:0xf bound_ctrl:1
	v_add_f32_dpp v72, v12, v12 wave_shr:1 row_mask:0xf bank_mask:0xf bound_ctrl:1
	v_add_f32_dpp v73, v13, v13 wave_shr:1 row_mask:0xf bank_mask:0xf bound_ctrl:1
	v_add_f32_dpp v74, v30, v30 wave_shr:1 row_mask:0xf bank_mask:0xf bound_ctrl:1
	v_add_f32_dpp v75, v31, v31 wave_shr:1 row_mask:0xf bank_mask:0xf bound_ctrl:1
	v_add_f32_dpp v76, v44, v44 wave_shr:1 row_mask:0xf bank_mask:0xf bound_ctrl:1
	v_add_f32_dpp v77, v45, v45 wave_shr:1 row_mask:0xf bank_mask:0xf bound_ctrl:1
	v_add_f32_dpp v78, v62, v62 wave_shr:1 row_mask:0xf bank_mask:0xf bound_ctrl:1
	v_add_f32_dpp v79, v63, v63 wave_shr:1 row_mask:0xf bank_mask:0xf bound_ctrl:1
	v_add_f32_dpp v80, v64, v64 wave_shr:1 row_mask:0xf bank_mask:0xf bound_ctrl:1
	v_add_f32_dpp v81, v65, v65 wave_shr:1 row_mask:0xf bank_mask:0xf bound_ctrl:1
	v_add_f32_dpp v82, v66, v66 wave_shr:1 row_mask:0xf bank_mask:0xf bound_ctrl:1
	v_add_f32_dpp v83, v67, v67 wave_shr:1 row_mask:0xf bank_mask:0xf bound_ctrl:1
	v_add_f32_dpp v84, v68, v68 wave_shr:1 row_mask:0xf bank_mask:0xf bound_ctrl:1
	v_add_f32_dpp v85, v69, v69 wave_shr:1 row_mask:0xf bank_mask:0xf bound_ctrl:1
	v_add_f32_dpp v70, v6, v70 wave_shl:1 row_mask:0xf bank_mask:0xf bound_ctrl:1
	v_add_f32_dpp v71, v7, v71 wave_shl:1 row_mask:0xf bank_mask:0xf bound_ctrl:1
	v_add_f32_dpp v72, v12, v72 wave_shl:1 row_mask:0xf bank_mask:0xf bound_ctrl:1
	v_add_f32_dpp v73, v13, v73 wave_shl:1 row_mask:0xf bank_mask:0xf bound_ctrl:1
	v_add_f32_dpp v74, v30, v74 wave_shl:1 row_mask:0xf bank_mask:0xf bound_ctrl:1
	v_add_f32_dpp v75, v31, v75 wave_shl:1 row_mask:0xf bank_mask:0xf bound_ctrl:1
	v_add_f32_dpp v76, v44, v76 wave_shl:1 row_mask:0xf bank_mask:0xf bound_ctrl:1
	v_add_f32_dpp v77, v45, v77 wave_shl:1 row_mask:0xf bank_mask:0xf bound_ctrl:1
	v_add_f32_dpp v78, v62, v78 wave_shl:1 row_mask:0xf bank_mask:0xf bound_ctrl:1
	v_add_f32_dpp v79, v63, v79 wave_shl:1 row_mask:0xf bank_mask:0xf bound_ctrl:1
	v_add_f32_dpp v80, v64, v80 wave_shl:1 row_mask:0xf bank_mask:0xf bound_ctrl:1
	v_add_f32_dpp v81, v65, v81 wave_shl:1 row_mask:0xf bank_mask:0xf bound_ctrl:1
	v_add_f32_dpp v82, v66, v82 wave_shl:1 row_mask:0xf bank_mask:0xf bound_ctrl:1
	v_add_f32_dpp v83, v67, v83 wave_shl:1 row_mask:0xf bank_mask:0xf bound_ctrl:1
	v_add_f32_dpp v84, v68, v84 wave_shl:1 row_mask:0xf bank_mask:0xf bound_ctrl:1
	v_add_f32_dpp v85, v69, v85 wave_shl:1 row_mask:0xf bank_mask:0xf bound_ctrl:1
	s_barrier
	s_add_i32 s4, s34, 2
	s_min_i32 s4, s4, 0x200
	s_mul_i32 s5, s4, 0x804
	s_add_i32 s5, s5, s35
	s_add_i32 s6, s5, 0x101004
	s_add_i32 s7, s5, 0x202008
	s_add_i32 s8, s5, 0x30300c
	s_mul_i32 s9, s4, 0x180c
	s_add_i32 s9, s9, s33
	buffer_load_dword v30, v28, s[16:19], s5 offen nt
	buffer_load_dword v31, v28, s[16:19], s6 offen nt
	buffer_load_dword v44, v28, s[16:19], s7 offen nt
	buffer_load_dword v45, v28, s[16:19], s8 offen nt
	buffer_load_dwordx3 v[64:66], v27, s[24:27], s9 offen nt
	s_waitcnt vmcnt(10)
	v_pk_mul_f32 v[62:63], v[14:15], v[36:37] op_sel_hi:[1,0]
	v_pk_mul_f32 v[68:69], v[16:17], v[36:37] op_sel_hi:[1,0]
	v_pk_mul_f32 v[86:87], v[14:15], v[36:37] op_sel:[0,1]
	v_pk_mul_f32 v[88:89], v[16:17], v[36:37] op_sel:[0,1]
	v_pk_mul_f32 v[90:91], v[14:15], v[38:39] op_sel_hi:[1,0]
	v_pk_mul_f32 v[92:93], v[16:17], v[38:39] op_sel_hi:[1,0]
	v_add_f32_dpp v94, v14, v14 wave_shr:1 row_mask:0xf bank_mask:0xf bound_ctrl:1
	v_add_f32_dpp v95, v15, v15 wave_shr:1 row_mask:0xf bank_mask:0xf bound_ctrl:1
	v_add_f32_dpp v96, v16, v16 wave_shr:1 row_mask:0xf bank_mask:0xf bound_ctrl:1
	v_add_f32_dpp v97, v17, v17 wave_shr:1 row_mask:0xf bank_mask:0xf bound_ctrl:1
	v_add_f32_dpp v98, v62, v62 wave_shr:1 row_mask:0xf bank_mask:0xf bound_ctrl:1
	v_add_f32_dpp v99, v63, v63 wave_shr:1 row_mask:0xf bank_mask:0xf bound_ctrl:1
	v_add_f32_dpp v100, v68, v68 wave_shr:1 row_mask:0xf bank_mask:0xf bound_ctrl:1
	v_add_f32_dpp v101, v69, v69 wave_shr:1 row_mask:0xf bank_mask:0xf bound_ctrl:1
	v_add_f32_dpp v102, v86, v86 wave_shr:1 row_mask:0xf bank_mask:0xf bound_ctrl:1
	v_add_f32_dpp v103, v87, v87 wave_shr:1 row_mask:0xf bank_mask:0xf bound_ctrl:1
	v_add_f32_dpp v104, v88, v88 wave_shr:1 row_mask:0xf bank_mask:0xf bound_ctrl:1
	v_add_f32_dpp v105, v89, v89 wave_shr:1 row_mask:0xf bank_mask:0xf bound_ctrl:1
	v_add_f32_dpp v106, v90, v90 wave_shr:1 row_mask:0xf bank_mask:0xf bound_ctrl:1
	v_add_f32_dpp v107, v91, v91 wave_shr:1 row_mask:0xf bank_mask:0xf bound_ctrl:1
	v_add_f32_dpp v108, v92, v92 wave_shr:1 row_mask:0xf bank_mask:0xf bound_ctrl:1
	v_add_f32_dpp v109, v93, v93 wave_shr:1 row_mask:0xf bank_mask:0xf bound_ctrl:1
	v_add_f32_dpp v94, v14, v94 wave_shl:1 row_mask:0xf bank_mask:0xf bound_ctrl:1
	v_add_f32_dpp v95, v15, v95 wave_shl:1 row_mask:0xf bank_mask:0xf bound_ctrl:1
	v_add_f32_dpp v96, v16, v96 wave_shl:1 row_mask:0xf bank_mask:0xf bound_ctrl:1
	v_add_f32_dpp v97, v17, v97 wave_shl:1 row_mask:0xf bank_mask:0xf bound_ctrl:1
	v_add_f32_dpp v98, v62, v98 wave_shl:1 row_mask:0xf bank_mask:0xf bound_ctrl:1
	v_add_f32_dpp v99, v63, v99 wave_shl:1 row_mask:0xf bank_mask:0xf bound_ctrl:1
	v_add_f32_dpp v100, v68, v100 wave_shl:1 row_mask:0xf bank_mask:0xf bound_ctrl:1
	v_add_f32_dpp v101, v69, v101 wave_shl:1 row_mask:0xf bank_mask:0xf bound_ctrl:1
	v_add_f32_dpp v102, v86, v102 wave_shl:1 row_mask:0xf bank_mask:0xf bound_ctrl:1
	v_add_f32_dpp v103, v87, v103 wave_shl:1 row_mask:0xf bank_mask:0xf bound_ctrl:1
	v_add_f32_dpp v104, v88, v104 wave_shl:1 row_mask:0xf bank_mask:0xf bound_ctrl:1
	v_add_f32_dpp v105, v89, v105 wave_shl:1 row_mask:0xf bank_mask:0xf bound_ctrl:1
	v_add_f32_dpp v106, v90, v106 wave_shl:1 row_mask:0xf bank_mask:0xf bound_ctrl:1
	v_add_f32_dpp v107, v91, v107 wave_shl:1 row_mask:0xf bank_mask:0xf bound_ctrl:1
	v_add_f32_dpp v108, v92, v108 wave_shl:1 row_mask:0xf bank_mask:0xf bound_ctrl:1
	v_add_f32_dpp v109, v93, v109 wave_shl:1 row_mask:0xf bank_mask:0xf bound_ctrl:1
	s_barrier
	ds_read_b128 v[88:91], v23 offset:0
	ds_read_b128 v[112:115], v23 offset:1024
	ds_read_b128 v[116:119], v23 offset:2048
	v_pk_add_f32 v[62:63], v[70:71], v[94:95]
	v_pk_add_f32 v[68:69], v[46:47], v[62:63]
	v_pk_add_f32 v[46:47], v[72:73], v[96:97]
	v_pk_add_f32 v[70:71], v[48:49], v[46:47]
	v_pk_add_f32 v[48:49], v[74:75], v[98:99]
	v_pk_add_f32 v[72:73], v[50:51], v[48:49]
	v_pk_add_f32 v[50:51], v[76:77], v[100:101]
	v_pk_add_f32 v[74:75], v[52:53], v[50:51]
	v_pk_add_f32 v[52:53], v[78:79], v[102:103]
	v_pk_add_f32 v[76:77], v[54:55], v[52:53]
	v_pk_add_f32 v[54:55], v[80:81], v[104:105]
	v_pk_add_f32 v[78:79], v[56:57], v[54:55]
	v_pk_add_f32 v[56:57], v[82:83], v[106:107]
	v_pk_add_f32 v[80:81], v[58:59], v[56:57]
	v_pk_add_f32 v[58:59], v[84:85], v[108:109]
	v_pk_add_f32 v[82:83], v[60:61], v[58:59]
	s_waitcnt lgkmcnt(2)
	v_pk_fma_f32 v[72:73], v[88:89], v[68:69], v[72:73] op_sel_hi:[0,1,1] neg_lo:[1,0,0] neg_hi:[1,0,0]
	v_pk_fma_f32 v[74:75], v[88:89], v[70:71], v[74:75] op_sel_hi:[0,1,1] neg_lo:[1,0,0] neg_hi:[1,0,0]
	v_pk_fma_f32 v[76:77], v[88:89], v[68:69], v[76:77] op_sel:[1,0,0] neg_lo:[1,0,0] neg_hi:[1,0,0]
	v_pk_fma_f32 v[78:79], v[88:89], v[70:71], v[78:79] op_sel:[1,0,0] neg_lo:[1,0,0] neg_hi:[1,0,0]
	v_pk_fma_f32 v[80:81], v[90:91], v[68:69], v[80:81] op_sel_hi:[0,1,1] neg_lo:[1,0,0] neg_hi:[1,0,0]
	v_pk_fma_f32 v[82:83], v[90:91], v[70:71], v[82:83] op_sel_hi:[0,1,1] neg_lo:[1,0,0] neg_hi:[1,0,0]
	v_pk_mul_f32 v[60:61], v[90:91], v[72:73] op_sel:[1,0]
	v_pk_mul_f32 v[92:93], v[90:91], v[74:75] op_sel:[1,0]
	s_waitcnt lgkmcnt(1)
	v_pk_mul_f32 v[84:85], v[112:113], v[72:73] op_sel_hi:[0,1]
	v_pk_mul_f32 v[110:111], v[112:113], v[74:75] op_sel_hi:[0,1]
	v_pk_mul_f32 v[86:87], v[112:113], v[72:73] op_sel:[1,0]
	v_pk_mul_f32 v[120:121], v[112:113], v[74:75] op_sel:[1,0]
	v_pk_fma_f32 v[60:61], v[112:113], v[76:77], v[60:61] op_sel_hi:[0,1,1]
	v_pk_fma_f32 v[92:93], v[112:113], v[78:79], v[92:93] op_sel_hi:[0,1,1]
	v_pk_fma_f32 v[84:85], v[114:115], v[76:77], v[84:85] op_sel_hi:[0,1,1]
	v_pk_fma_f32 v[110:111], v[114:115], v[78:79], v[110:111] op_sel_hi:[0,1,1]
	v_pk_fma_f32 v[86:87], v[114:115], v[76:77], v[86:87] op_sel:[1,0,0]
	v_pk_fma_f32 v[120:121], v[114:115], v[78:79], v[120:121] op_sel:[1,0,0]
	v_pk_fma_f32 v[60:61], v[112:113], v[80:81], v[60:61] op_sel:[1,0,0]
	v_pk_fma_f32 v[92:93], v[112:113], v[82:83], v[92:93] op_sel:[1,0,0]
	v_pk_fma_f32 v[84:85], v[114:115], v[80:81], v[84:85] op_sel:[1,0,0]
	v_pk_fma_f32 v[110:111], v[114:115], v[82:83], v[110:111] op_sel:[1,0,0]
	s_waitcnt lgkmcnt(0)
	v_pk_fma_f32 v[86:87], v[116:117], v[80:81], v[86:87] op_sel_hi:[0,1,1]
	v_pk_fma_f32 v[120:121], v[116:117], v[82:83], v[120:121] op_sel_hi:[0,1,1]
	v_pk_mul_f32 v[122:123], v[88:89], v[60:61] op_sel_hi:[0,1]
	v_pk_mul_f32 v[124:125], v[88:89], v[92:93] op_sel_hi:[0,1]
	v_pk_fma_f32 v[122:123], v[88:89], v[84:85], v[122:123] op_sel:[1,0,0]
	v_pk_fma_f32 v[124:125], v[88:89], v[110:111], v[124:125] op_sel:[1,0,0]
	v_pk_fma_f32 v[122:123], v[90:91], v[86:87], v[122:123] op_sel_hi:[0,1,1]
	v_pk_fma_f32 v[124:125], v[90:91], v[120:121], v[124:125] op_sel_hi:[0,1,1]
	v_pk_fma_f32 v[122:123], v[116:117], v[68:69], v[122:123] op_sel:[1,0,0] neg_lo:[0,0,1] neg_hi:[0,0,1]
	v_pk_fma_f32 v[124:125], v[116:117], v[70:71], v[124:125] op_sel:[1,0,0] neg_lo:[0,0,1] neg_hi:[0,0,1]
	v_add_f32_dpp v68, v60, v60 wave_shr:1 row_mask:0xf bank_mask:0xf bound_ctrl:1
	v_add_f32_dpp v69, v61, v61 wave_shr:1 row_mask:0xf bank_mask:0xf bound_ctrl:1
	v_add_f32_dpp v70, v92, v92 wave_shr:1 row_mask:0xf bank_mask:0xf bound_ctrl:1
	v_add_f32_dpp v71, v93, v93 wave_shr:1 row_mask:0xf bank_mask:0xf bound_ctrl:1
	v_add_f32_dpp v72, v84, v84 wave_shr:1 row_mask:0xf bank_mask:0xf bound_ctrl:1
	v_add_f32_dpp v73, v85, v85 wave_shr:1 row_mask:0xf bank_mask:0xf bound_ctrl:1
	v_add_f32_dpp v74, v110, v110 wave_shr:1 row_mask:0xf bank_mask:0xf bound_ctrl:1
	v_add_f32_dpp v75, v111, v111 wave_shr:1 row_mask:0xf bank_mask:0xf bound_ctrl:1
	v_add_f32_dpp v76, v86, v86 wave_shr:1 row_mask:0xf bank_mask:0xf bound_ctrl:1
	v_add_f32_dpp v77, v87, v87 wave_shr:1 row_mask:0xf bank_mask:0xf bound_ctrl:1
	v_add_f32_dpp v78, v120, v120 wave_shr:1 row_mask:0xf bank_mask:0xf bound_ctrl:1
	v_add_f32_dpp v79, v121, v121 wave_shr:1 row_mask:0xf bank_mask:0xf bound_ctrl:1
	v_add_f32_dpp v80, v122, v122 wave_shr:1 row_mask:0xf bank_mask:0xf bound_ctrl:1
	v_add_f32_dpp v81, v123, v123 wave_shr:1 row_mask:0xf bank_mask:0xf bound_ctrl:1
	v_add_f32_dpp v82, v124, v124 wave_shr:1 row_mask:0xf bank_mask:0xf bound_ctrl:1
	v_add_f32_dpp v83, v125, v125 wave_shr:1 row_mask:0xf bank_mask:0xf bound_ctrl:1
	v_add_f32_dpp v68, v60, v68 wave_shl:1 row_mask:0xf bank_mask:0xf bound_ctrl:1
	v_add_f32_dpp v69, v61, v69 wave_shl:1 row_mask:0xf bank_mask:0xf bound_ctrl:1
	v_add_f32_dpp v70, v92, v70 wave_shl:1 row_mask:0xf bank_mask:0xf bound_ctrl:1
	v_add_f32_dpp v71, v93, v71 wave_shl:1 row_mask:0xf bank_mask:0xf bound_ctrl:1
	v_add_f32_dpp v72, v84, v72 wave_shl:1 row_mask:0xf bank_mask:0xf bound_ctrl:1
	v_add_f32_dpp v73, v85, v73 wave_shl:1 row_mask:0xf bank_mask:0xf bound_ctrl:1
	v_add_f32_dpp v74, v110, v74 wave_shl:1 row_mask:0xf bank_mask:0xf bound_ctrl:1
	v_add_f32_dpp v75, v111, v75 wave_shl:1 row_mask:0xf bank_mask:0xf bound_ctrl:1
	v_add_f32_dpp v76, v86, v76 wave_shl:1 row_mask:0xf bank_mask:0xf bound_ctrl:1
	v_add_f32_dpp v77, v87, v77 wave_shl:1 row_mask:0xf bank_mask:0xf bound_ctrl:1
	v_add_f32_dpp v78, v120, v78 wave_shl:1 row_mask:0xf bank_mask:0xf bound_ctrl:1
	v_add_f32_dpp v79, v121, v79 wave_shl:1 row_mask:0xf bank_mask:0xf bound_ctrl:1
	v_add_f32_dpp v80, v122, v80 wave_shl:1 row_mask:0xf bank_mask:0xf bound_ctrl:1
	v_add_f32_dpp v81, v123, v81 wave_shl:1 row_mask:0xf bank_mask:0xf bound_ctrl:1
	v_add_f32_dpp v82, v124, v82 wave_shl:1 row_mask:0xf bank_mask:0xf bound_ctrl:1
	v_add_f32_dpp v83, v125, v83 wave_shl:1 row_mask:0xf bank_mask:0xf bound_ctrl:1
	s_add_i32 s4, s34, 3
	s_min_i32 s4, s4, 0x200
	s_mul_i32 s5, s4, 0x804
	s_add_i32 s5, s5, s35
	s_add_i32 s6, s5, 0x101004
	s_add_i32 s7, s5, 0x202008
	s_add_i32 s8, s5, 0x30300c
	s_mul_i32 s9, s4, 0x180c
	s_add_i32 s9, s9, s33
	buffer_load_dword v2, v28, s[16:19], s5 offen nt
	buffer_load_dword v3, v28, s[16:19], s6 offen nt
	buffer_load_dword v4, v28, s[16:19], s7 offen nt
	buffer_load_dword v5, v28, s[16:19], s8 offen nt
	buffer_load_dwordx3 v[8:10], v27, s[24:27], s9 offen nt
	s_waitcnt vmcnt(10)
	v_pk_mul_f32 v[60:61], v[20:21], v[40:41] op_sel_hi:[1,0]
	v_pk_mul_f32 v[84:85], v[24:25], v[40:41] op_sel_hi:[1,0]
	v_pk_mul_f32 v[86:87], v[20:21], v[40:41] op_sel:[0,1]
	v_pk_mul_f32 v[88:89], v[24:25], v[40:41] op_sel:[0,1]
	v_pk_mul_f32 v[90:91], v[20:21], v[42:43] op_sel_hi:[1,0]
	v_pk_mul_f32 v[92:93], v[24:25], v[42:43] op_sel_hi:[1,0]
	v_add_f32_dpp v110, v20, v20 wave_shr:1 row_mask:0xf bank_mask:0xf bound_ctrl:1
	v_add_f32_dpp v111, v21, v21 wave_shr:1 row_mask:0xf bank_mask:0xf bound_ctrl:1
	v_add_f32_dpp v112, v24, v24 wave_shr:1 row_mask:0xf bank_mask:0xf bound_ctrl:1
	v_add_f32_dpp v113, v25, v25 wave_shr:1 row_mask:0xf bank_mask:0xf bound_ctrl:1
	v_add_f32_dpp v114, v60, v60 wave_shr:1 row_mask:0xf bank_mask:0xf bound_ctrl:1
	v_add_f32_dpp v115, v61, v61 wave_shr:1 row_mask:0xf bank_mask:0xf bound_ctrl:1
	v_add_f32_dpp v116, v84, v84 wave_shr:1 row_mask:0xf bank_mask:0xf bound_ctrl:1
	v_add_f32_dpp v117, v85, v85 wave_shr:1 row_mask:0xf bank_mask:0xf bound_ctrl:1
	v_add_f32_dpp v118, v86, v86 wave_shr:1 row_mask:0xf bank_mask:0xf bound_ctrl:1
	v_add_f32_dpp v119, v87, v87 wave_shr:1 row_mask:0xf bank_mask:0xf bound_ctrl:1
	v_add_f32_dpp v120, v88, v88 wave_shr:1 row_mask:0xf bank_mask:0xf bound_ctrl:1
	v_add_f32_dpp v121, v89, v89 wave_shr:1 row_mask:0xf bank_mask:0xf bound_ctrl:1
	v_add_f32_dpp v122, v90, v90 wave_shr:1 row_mask:0xf bank_mask:0xf bound_ctrl:1
	v_add_f32_dpp v123, v91, v91 wave_shr:1 row_mask:0xf bank_mask:0xf bound_ctrl:1
	v_add_f32_dpp v124, v92, v92 wave_shr:1 row_mask:0xf bank_mask:0xf bound_ctrl:1
	v_add_f32_dpp v125, v93, v93 wave_shr:1 row_mask:0xf bank_mask:0xf bound_ctrl:1
	v_add_f32_dpp v110, v20, v110 wave_shl:1 row_mask:0xf bank_mask:0xf bound_ctrl:1
	v_add_f32_dpp v111, v21, v111 wave_shl:1 row_mask:0xf bank_mask:0xf bound_ctrl:1
	v_add_f32_dpp v112, v24, v112 wave_shl:1 row_mask:0xf bank_mask:0xf bound_ctrl:1
	v_add_f32_dpp v113, v25, v113 wave_shl:1 row_mask:0xf bank_mask:0xf bound_ctrl:1
	v_add_f32_dpp v114, v60, v114 wave_shl:1 row_mask:0xf bank_mask:0xf bound_ctrl:1
	v_add_f32_dpp v115, v61, v115 wave_shl:1 row_mask:0xf bank_mask:0xf bound_ctrl:1
	v_add_f32_dpp v116, v84, v116 wave_shl:1 row_mask:0xf bank_mask:0xf bound_ctrl:1
	v_add_f32_dpp v117, v85, v117 wave_shl:1 row_mask:0xf bank_mask:0xf bound_ctrl:1
	v_add_f32_dpp v118, v86, v118 wave_shl:1 row_mask:0xf bank_mask:0xf bound_ctrl:1
	v_add_f32_dpp v119, v87, v119 wave_shl:1 row_mask:0xf bank_mask:0xf bound_ctrl:1
	v_add_f32_dpp v120, v88, v120 wave_shl:1 row_mask:0xf bank_mask:0xf bound_ctrl:1
	v_add_f32_dpp v121, v89, v121 wave_shl:1 row_mask:0xf bank_mask:0xf bound_ctrl:1
	v_add_f32_dpp v122, v90, v122 wave_shl:1 row_mask:0xf bank_mask:0xf bound_ctrl:1
	v_add_f32_dpp v123, v91, v123 wave_shl:1 row_mask:0xf bank_mask:0xf bound_ctrl:1
	v_add_f32_dpp v124, v92, v124 wave_shl:1 row_mask:0xf bank_mask:0xf bound_ctrl:1
	v_add_f32_dpp v125, v93, v125 wave_shl:1 row_mask:0xf bank_mask:0xf bound_ctrl:1
	s_barrier
	ds_read_b128 v[84:87], v23 offset:3072
	ds_read_b128 v[88:91], v23 offset:4096
	ds_read_b128 v[128:131], v23 offset:5120
	v_pk_add_f32 v[60:61], v[62:63], v[110:111]
	v_pk_add_f32 v[62:63], v[46:47], v[112:113]
	v_pk_add_f32 v[46:47], v[48:49], v[114:115]
	v_pk_add_f32 v[48:49], v[50:51], v[116:117]
	v_pk_add_f32 v[50:51], v[52:53], v[118:119]
	v_pk_add_f32 v[52:53], v[54:55], v[120:121]
	v_pk_add_f32 v[54:55], v[56:57], v[122:123]
	v_pk_add_f32 v[56:57], v[58:59], v[124:125]
	s_waitcnt lgkmcnt(2)
	v_pk_fma_f32 v[46:47], v[84:85], v[60:61], v[46:47] op_sel_hi:[0,1,1] neg_lo:[1,0,0] neg_hi:[1,0,0]
	v_pk_fma_f32 v[48:49], v[84:85], v[62:63], v[48:49] op_sel_hi:[0,1,1] neg_lo:[1,0,0] neg_hi:[1,0,0]
	v_pk_fma_f32 v[50:51], v[84:85], v[60:61], v[50:51] op_sel:[1,0,0] neg_lo:[1,0,0] neg_hi:[1,0,0]
	v_pk_fma_f32 v[52:53], v[84:85], v[62:63], v[52:53] op_sel:[1,0,0] neg_lo:[1,0,0] neg_hi:[1,0,0]
	v_pk_fma_f32 v[54:55], v[86:87], v[60:61], v[54:55] op_sel_hi:[0,1,1] neg_lo:[1,0,0] neg_hi:[1,0,0]
	v_pk_fma_f32 v[56:57], v[86:87], v[62:63], v[56:57] op_sel_hi:[0,1,1] neg_lo:[1,0,0] neg_hi:[1,0,0]
	v_pk_mul_f32 v[58:59], v[86:87], v[46:47] op_sel:[1,0]
	v_pk_mul_f32 v[132:133], v[86:87], v[48:49] op_sel:[1,0]
	s_waitcnt lgkmcnt(1)
	v_pk_mul_f32 v[92:93], v[88:89], v[46:47] op_sel_hi:[0,1]
	v_pk_mul_f32 v[134:135], v[88:89], v[48:49] op_sel_hi:[0,1]
	v_pk_mul_f32 v[126:127], v[88:89], v[46:47] op_sel:[1,0]
	v_pk_mul_f32 v[136:137], v[88:89], v[48:49] op_sel:[1,0]
	v_pk_fma_f32 v[58:59], v[88:89], v[50:51], v[58:59] op_sel_hi:[0,1,1]
	v_pk_fma_f32 v[132:133], v[88:89], v[52:53], v[132:133] op_sel_hi:[0,1,1]
	v_pk_fma_f32 v[92:93], v[90:91], v[50:51], v[92:93] op_sel_hi:[0,1,1]
	v_pk_fma_f32 v[134:135], v[90:91], v[52:53], v[134:135] op_sel_hi:[0,1,1]
	v_pk_fma_f32 v[126:127], v[90:91], v[50:51], v[126:127] op_sel:[1,0,0]
	v_pk_fma_f32 v[136:137], v[90:91], v[52:53], v[136:137] op_sel:[1,0,0]
	v_pk_fma_f32 v[58:59], v[88:89], v[54:55], v[58:59] op_sel:[1,0,0]
	v_pk_fma_f32 v[132:133], v[88:89], v[56:57], v[132:133] op_sel:[1,0,0]
	v_pk_fma_f32 v[92:93], v[90:91], v[54:55], v[92:93] op_sel:[1,0,0]
	v_pk_fma_f32 v[134:135], v[90:91], v[56:57], v[134:135] op_sel:[1,0,0]
	s_waitcnt lgkmcnt(0)
	v_pk_fma_f32 v[126:127], v[128:129], v[54:55], v[126:127] op_sel_hi:[0,1,1]
	v_pk_fma_f32 v[136:137], v[128:129], v[56:57], v[136:137] op_sel_hi:[0,1,1]
	v_pk_mul_f32 v[138:139], v[84:85], v[58:59] op_sel_hi:[0,1]
	v_pk_mul_f32 v[140:141], v[84:85], v[132:133] op_sel_hi:[0,1]
	v_pk_fma_f32 v[138:139], v[84:85], v[92:93], v[138:139] op_sel:[1,0,0]
	v_pk_fma_f32 v[140:141], v[84:85], v[134:135], v[140:141] op_sel:[1,0,0]
	v_pk_fma_f32 v[138:139], v[86:87], v[126:127], v[138:139] op_sel_hi:[0,1,1]
	v_pk_fma_f32 v[140:141], v[86:87], v[136:137], v[140:141] op_sel_hi:[0,1,1]
	v_pk_fma_f32 v[138:139], v[128:129], v[60:61], v[138:139] op_sel:[1,0,0] neg_lo:[0,0,1] neg_hi:[0,0,1]
	v_pk_fma_f32 v[140:141], v[128:129], v[62:63], v[140:141] op_sel:[1,0,0] neg_lo:[0,0,1] neg_hi:[0,0,1]
	v_add_f32_dpp v46, v58, v58 wave_shr:1 row_mask:0xf bank_mask:0xf bound_ctrl:1
	v_add_f32_dpp v47, v59, v59 wave_shr:1 row_mask:0xf bank_mask:0xf bound_ctrl:1
	v_add_f32_dpp v48, v132, v132 wave_shr:1 row_mask:0xf bank_mask:0xf bound_ctrl:1
	v_add_f32_dpp v49, v133, v133 wave_shr:1 row_mask:0xf bank_mask:0xf bound_ctrl:1
	v_add_f32_dpp v50, v92, v92 wave_shr:1 row_mask:0xf bank_mask:0xf bound_ctrl:1
	v_add_f32_dpp v51, v93, v93 wave_shr:1 row_mask:0xf bank_mask:0xf bound_ctrl:1
	v_add_f32_dpp v52, v134, v134 wave_shr:1 row_mask:0xf bank_mask:0xf bound_ctrl:1
	v_add_f32_dpp v53, v135, v135 wave_shr:1 row_mask:0xf bank_mask:0xf bound_ctrl:1
	v_add_f32_dpp v54, v126, v126 wave_shr:1 row_mask:0xf bank_mask:0xf bound_ctrl:1
	v_add_f32_dpp v55, v127, v127 wave_shr:1 row_mask:0xf bank_mask:0xf bound_ctrl:1
	v_add_f32_dpp v56, v136, v136 wave_shr:1 row_mask:0xf bank_mask:0xf bound_ctrl:1
	v_add_f32_dpp v57, v137, v137 wave_shr:1 row_mask:0xf bank_mask:0xf bound_ctrl:1
	v_add_f32_dpp v60, v138, v138 wave_shr:1 row_mask:0xf bank_mask:0xf bound_ctrl:1
	v_add_f32_dpp v61, v139, v139 wave_shr:1 row_mask:0xf bank_mask:0xf bound_ctrl:1
	v_add_f32_dpp v62, v140, v140 wave_shr:1 row_mask:0xf bank_mask:0xf bound_ctrl:1
	v_add_f32_dpp v63, v141, v141 wave_shr:1 row_mask:0xf bank_mask:0xf bound_ctrl:1
	v_add_f32_dpp v46, v58, v46 wave_shl:1 row_mask:0xf bank_mask:0xf bound_ctrl:1
	v_add_f32_dpp v47, v59, v47 wave_shl:1 row_mask:0xf bank_mask:0xf bound_ctrl:1
	v_add_f32_dpp v48, v132, v48 wave_shl:1 row_mask:0xf bank_mask:0xf bound_ctrl:1
	v_add_f32_dpp v49, v133, v49 wave_shl:1 row_mask:0xf bank_mask:0xf bound_ctrl:1
	v_add_f32_dpp v50, v92, v50 wave_shl:1 row_mask:0xf bank_mask:0xf bound_ctrl:1
	v_add_f32_dpp v51, v93, v51 wave_shl:1 row_mask:0xf bank_mask:0xf bound_ctrl:1
	v_add_f32_dpp v52, v134, v52 wave_shl:1 row_mask:0xf bank_mask:0xf bound_ctrl:1
	v_add_f32_dpp v53, v135, v53 wave_shl:1 row_mask:0xf bank_mask:0xf bound_ctrl:1
	v_add_f32_dpp v54, v126, v54 wave_shl:1 row_mask:0xf bank_mask:0xf bound_ctrl:1
	v_add_f32_dpp v55, v127, v55 wave_shl:1 row_mask:0xf bank_mask:0xf bound_ctrl:1
	v_add_f32_dpp v56, v136, v56 wave_shl:1 row_mask:0xf bank_mask:0xf bound_ctrl:1
	v_add_f32_dpp v57, v137, v57 wave_shl:1 row_mask:0xf bank_mask:0xf bound_ctrl:1
	v_add_f32_dpp v60, v138, v60 wave_shl:1 row_mask:0xf bank_mask:0xf bound_ctrl:1
	v_add_f32_dpp v61, v139, v61 wave_shl:1 row_mask:0xf bank_mask:0xf bound_ctrl:1
	v_add_f32_dpp v62, v140, v62 wave_shl:1 row_mask:0xf bank_mask:0xf bound_ctrl:1
	v_add_f32_dpp v63, v141, v63 wave_shl:1 row_mask:0xf bank_mask:0xf bound_ctrl:1
	s_add_i32 s4, s34, 4
	s_min_i32 s4, s4, 0x200
	s_mul_i32 s5, s4, 0x804
	s_add_i32 s5, s5, s35
	s_add_i32 s6, s5, 0x101004
	s_add_i32 s7, s5, 0x202008
	s_add_i32 s8, s5, 0x30300c
	s_mul_i32 s9, s4, 0x180c
	s_add_i32 s9, s9, s33
	buffer_load_dword v6, v28, s[16:19], s5 offen nt
	buffer_load_dword v7, v28, s[16:19], s6 offen nt
	buffer_load_dword v12, v28, s[16:19], s7 offen nt
	buffer_load_dword v13, v28, s[16:19], s8 offen nt
	buffer_load_dwordx3 v[32:34], v27, s[24:27], s9 offen nt
	s_waitcnt vmcnt(10)
	v_pk_mul_f32 v[58:59], v[30:31], v[64:65] op_sel_hi:[1,0]
	v_pk_mul_f32 v[84:85], v[44:45], v[64:65] op_sel_hi:[1,0]
	v_pk_mul_f32 v[86:87], v[30:31], v[64:65] op_sel:[0,1]
	v_pk_mul_f32 v[88:89], v[44:45], v[64:65] op_sel:[0,1]
	v_pk_mul_f32 v[90:91], v[30:31], v[66:67] op_sel_hi:[1,0]
	v_pk_mul_f32 v[92:93], v[44:45], v[66:67] op_sel_hi:[1,0]
	v_add_f32_dpp v126, v30, v30 wave_shr:1 row_mask:0xf bank_mask:0xf bound_ctrl:1
	v_add_f32_dpp v127, v31, v31 wave_shr:1 row_mask:0xf bank_mask:0xf bound_ctrl:1
	v_add_f32_dpp v128, v44, v44 wave_shr:1 row_mask:0xf bank_mask:0xf bound_ctrl:1
	v_add_f32_dpp v129, v45, v45 wave_shr:1 row_mask:0xf bank_mask:0xf bound_ctrl:1
	v_add_f32_dpp v130, v58, v58 wave_shr:1 row_mask:0xf bank_mask:0xf bound_ctrl:1
	v_add_f32_dpp v131, v59, v59 wave_shr:1 row_mask:0xf bank_mask:0xf bound_ctrl:1
	v_add_f32_dpp v132, v84, v84 wave_shr:1 row_mask:0xf bank_mask:0xf bound_ctrl:1
	v_add_f32_dpp v133, v85, v85 wave_shr:1 row_mask:0xf bank_mask:0xf bound_ctrl:1
	v_add_f32_dpp v134, v86, v86 wave_shr:1 row_mask:0xf bank_mask:0xf bound_ctrl:1
	v_add_f32_dpp v135, v87, v87 wave_shr:1 row_mask:0xf bank_mask:0xf bound_ctrl:1
	v_add_f32_dpp v136, v88, v88 wave_shr:1 row_mask:0xf bank_mask:0xf bound_ctrl:1
	v_add_f32_dpp v137, v89, v89 wave_shr:1 row_mask:0xf bank_mask:0xf bound_ctrl:1
	v_add_f32_dpp v138, v90, v90 wave_shr:1 row_mask:0xf bank_mask:0xf bound_ctrl:1
	v_add_f32_dpp v139, v91, v91 wave_shr:1 row_mask:0xf bank_mask:0xf bound_ctrl:1
	v_add_f32_dpp v140, v92, v92 wave_shr:1 row_mask:0xf bank_mask:0xf bound_ctrl:1
	v_add_f32_dpp v141, v93, v93 wave_shr:1 row_mask:0xf bank_mask:0xf bound_ctrl:1
	v_add_f32_dpp v126, v30, v126 wave_shl:1 row_mask:0xf bank_mask:0xf bound_ctrl:1
	v_add_f32_dpp v127, v31, v127 wave_shl:1 row_mask:0xf bank_mask:0xf bound_ctrl:1
	v_add_f32_dpp v128, v44, v128 wave_shl:1 row_mask:0xf bank_mask:0xf bound_ctrl:1
	v_add_f32_dpp v129, v45, v129 wave_shl:1 row_mask:0xf bank_mask:0xf bound_ctrl:1
	v_add_f32_dpp v130, v58, v130 wave_shl:1 row_mask:0xf bank_mask:0xf bound_ctrl:1
	v_add_f32_dpp v131, v59, v131 wave_shl:1 row_mask:0xf bank_mask:0xf bound_ctrl:1
	v_add_f32_dpp v132, v84, v132 wave_shl:1 row_mask:0xf bank_mask:0xf bound_ctrl:1
	v_add_f32_dpp v133, v85, v133 wave_shl:1 row_mask:0xf bank_mask:0xf bound_ctrl:1
	v_add_f32_dpp v134, v86, v134 wave_shl:1 row_mask:0xf bank_mask:0xf bound_ctrl:1
	v_add_f32_dpp v135, v87, v135 wave_shl:1 row_mask:0xf bank_mask:0xf bound_ctrl:1
	v_add_f32_dpp v136, v88, v136 wave_shl:1 row_mask:0xf bank_mask:0xf bound_ctrl:1
	v_add_f32_dpp v137, v89, v137 wave_shl:1 row_mask:0xf bank_mask:0xf bound_ctrl:1
	v_add_f32_dpp v138, v90, v138 wave_shl:1 row_mask:0xf bank_mask:0xf bound_ctrl:1
	v_add_f32_dpp v139, v91, v139 wave_shl:1 row_mask:0xf bank_mask:0xf bound_ctrl:1
	v_add_f32_dpp v140, v92, v140 wave_shl:1 row_mask:0xf bank_mask:0xf bound_ctrl:1
	v_add_f32_dpp v141, v93, v141 wave_shl:1 row_mask:0xf bank_mask:0xf bound_ctrl:1
	s_barrier
	ds_read_b128 v[84:87], v23 offset:0
	ds_read_b128 v[88:91], v23 offset:1024
	ds_read_b128 v[144:147], v23 offset:2048
	v_pk_add_f32 v[58:59], v[110:111], v[126:127]
	v_pk_add_f32 v[92:93], v[94:95], v[58:59]
	v_pk_add_f32 v[94:95], v[112:113], v[128:129]
	v_pk_add_f32 v[110:111], v[96:97], v[94:95]
	v_pk_add_f32 v[96:97], v[114:115], v[130:131]
	v_pk_add_f32 v[112:113], v[98:99], v[96:97]
	v_pk_add_f32 v[98:99], v[116:117], v[132:133]
	v_pk_add_f32 v[114:115], v[100:101], v[98:99]
	v_pk_add_f32 v[100:101], v[118:119], v[134:135]
	v_pk_add_f32 v[116:117], v[102:103], v[100:101]
	v_pk_add_f32 v[102:103], v[120:121], v[136:137]
	v_pk_add_f32 v[118:119], v[104:105], v[102:103]
	v_pk_add_f32 v[104:105], v[122:123], v[138:139]
	v_pk_add_f32 v[120:121], v[106:107], v[104:105]
	v_pk_add_f32 v[106:107], v[124:125], v[140:141]
	v_pk_add_f32 v[122:123], v[108:109], v[106:107]
	s_waitcnt lgkmcnt(2)
	v_pk_fma_f32 v[112:113], v[84:85], v[92:93], v[112:113] op_sel_hi:[0,1,1] neg_lo:[1,0,0] neg_hi:[1,0,0]
	v_pk_fma_f32 v[114:115], v[84:85], v[110:111], v[114:115] op_sel_hi:[0,1,1] neg_lo:[1,0,0] neg_hi:[1,0,0]
	v_pk_fma_f32 v[116:117], v[84:85], v[92:93], v[116:117] op_sel:[1,0,0] neg_lo:[1,0,0] neg_hi:[1,0,0]
	v_pk_fma_f32 v[118:119], v[84:85], v[110:111], v[118:119] op_sel:[1,0,0] neg_lo:[1,0,0] neg_hi:[1,0,0]
	v_pk_fma_f32 v[120:121], v[86:87], v[92:93], v[120:121] op_sel_hi:[0,1,1] neg_lo:[1,0,0] neg_hi:[1,0,0]
	v_pk_fma_f32 v[122:123], v[86:87], v[110:111], v[122:123] op_sel_hi:[0,1,1] neg_lo:[1,0,0] neg_hi:[1,0,0]
	v_pk_mul_f32 v[108:109], v[86:87], v[112:113] op_sel:[1,0]
	v_pk_mul_f32 v[148:149], v[86:87], v[114:115] op_sel:[1,0]
	s_waitcnt lgkmcnt(1)
	v_pk_mul_f32 v[124:125], v[88:89], v[112:113] op_sel_hi:[0,1]
	v_pk_mul_f32 v[150:151], v[88:89], v[114:115] op_sel_hi:[0,1]
	v_pk_mul_f32 v[142:143], v[88:89], v[112:113] op_sel:[1,0]
	v_pk_mul_f32 v[152:153], v[88:89], v[114:115] op_sel:[1,0]
	v_pk_fma_f32 v[108:109], v[88:89], v[116:117], v[108:109] op_sel_hi:[0,1,1]
	v_pk_fma_f32 v[148:149], v[88:89], v[118:119], v[148:149] op_sel_hi:[0,1,1]
	v_pk_fma_f32 v[124:125], v[90:91], v[116:117], v[124:125] op_sel_hi:[0,1,1]
	v_pk_fma_f32 v[150:151], v[90:91], v[118:119], v[150:151] op_sel_hi:[0,1,1]
	v_pk_fma_f32 v[142:143], v[90:91], v[116:117], v[142:143] op_sel:[1,0,0]
	v_pk_fma_f32 v[152:153], v[90:91], v[118:119], v[152:153] op_sel:[1,0,0]
	v_pk_fma_f32 v[108:109], v[88:89], v[120:121], v[108:109] op_sel:[1,0,0]
	v_pk_fma_f32 v[148:149], v[88:89], v[122:123], v[148:149] op_sel:[1,0,0]
	v_pk_fma_f32 v[124:125], v[90:91], v[120:121], v[124:125] op_sel:[1,0,0]
	v_pk_fma_f32 v[150:151], v[90:91], v[122:123], v[150:151] op_sel:[1,0,0]
	s_waitcnt lgkmcnt(0)
	v_pk_fma_f32 v[142:143], v[144:145], v[120:121], v[142:143] op_sel_hi:[0,1,1]
	v_pk_fma_f32 v[152:153], v[144:145], v[122:123], v[152:153] op_sel_hi:[0,1,1]
	v_pk_mul_f32 v[154:155], v[84:85], v[108:109] op_sel_hi:[0,1]
	v_pk_mul_f32 v[156:157], v[84:85], v[148:149] op_sel_hi:[0,1]
	v_pk_fma_f32 v[154:155], v[84:85], v[124:125], v[154:155] op_sel:[1,0,0]
	v_pk_fma_f32 v[156:157], v[84:85], v[150:151], v[156:157] op_sel:[1,0,0]
	v_pk_fma_f32 v[154:155], v[86:87], v[142:143], v[154:155] op_sel_hi:[0,1,1]
	v_pk_fma_f32 v[156:157], v[86:87], v[152:153], v[156:157] op_sel_hi:[0,1,1]
	v_pk_fma_f32 v[154:155], v[144:145], v[92:93], v[154:155] op_sel:[1,0,0] neg_lo:[0,0,1] neg_hi:[0,0,1]
	v_pk_fma_f32 v[156:157], v[144:145], v[110:111], v[156:157] op_sel:[1,0,0] neg_lo:[0,0,1] neg_hi:[0,0,1]
	v_cmp_eq_u32_e64 s[10:11], 1, v147
	v_cmp_eq_u32_e64 s[14:15], 2, v147
	v_cmp_eq_u32_e64 s[20:21], 3, v147
	v_cmp_eq_u32_e64 s[22:23], 4, v147
	v_add_f32_dpp v92, v108, v108 wave_shr:1 row_mask:0xf bank_mask:0xf bound_ctrl:1
	v_add_f32_dpp v93, v109, v109 wave_shr:1 row_mask:0xf bank_mask:0xf bound_ctrl:1
	v_add_f32_dpp v110, v148, v148 wave_shr:1 row_mask:0xf bank_mask:0xf bound_ctrl:1
	v_add_f32_dpp v111, v149, v149 wave_shr:1 row_mask:0xf bank_mask:0xf bound_ctrl:1
	v_add_f32_dpp v112, v124, v124 wave_shr:1 row_mask:0xf bank_mask:0xf bound_ctrl:1
	v_add_f32_dpp v113, v125, v125 wave_shr:1 row_mask:0xf bank_mask:0xf bound_ctrl:1
	v_add_f32_dpp v114, v150, v150 wave_shr:1 row_mask:0xf bank_mask:0xf bound_ctrl:1
	v_add_f32_dpp v115, v151, v151 wave_shr:1 row_mask:0xf bank_mask:0xf bound_ctrl:1
	v_add_f32_dpp v116, v142, v142 wave_shr:1 row_mask:0xf bank_mask:0xf bound_ctrl:1
	v_add_f32_dpp v117, v143, v143 wave_shr:1 row_mask:0xf bank_mask:0xf bound_ctrl:1
	v_add_f32_dpp v118, v152, v152 wave_shr:1 row_mask:0xf bank_mask:0xf bound_ctrl:1
	v_add_f32_dpp v119, v153, v153 wave_shr:1 row_mask:0xf bank_mask:0xf bound_ctrl:1
	v_add_f32_dpp v120, v154, v154 wave_shr:1 row_mask:0xf bank_mask:0xf bound_ctrl:1
	v_add_f32_dpp v121, v155, v155 wave_shr:1 row_mask:0xf bank_mask:0xf bound_ctrl:1
	v_add_f32_dpp v122, v156, v156 wave_shr:1 row_mask:0xf bank_mask:0xf bound_ctrl:1
	v_add_f32_dpp v123, v157, v157 wave_shr:1 row_mask:0xf bank_mask:0xf bound_ctrl:1
	v_add_f32_dpp v92, v108, v92 wave_shl:1 row_mask:0xf bank_mask:0xf bound_ctrl:1
	v_add_f32_dpp v93, v109, v93 wave_shl:1 row_mask:0xf bank_mask:0xf bound_ctrl:1
	v_add_f32_dpp v110, v148, v110 wave_shl:1 row_mask:0xf bank_mask:0xf bound_ctrl:1
	v_add_f32_dpp v111, v149, v111 wave_shl:1 row_mask:0xf bank_mask:0xf bound_ctrl:1
	v_add_f32_dpp v112, v124, v112 wave_shl:1 row_mask:0xf bank_mask:0xf bound_ctrl:1
	v_add_f32_dpp v113, v125, v113 wave_shl:1 row_mask:0xf bank_mask:0xf bound_ctrl:1
	v_add_f32_dpp v114, v150, v114 wave_shl:1 row_mask:0xf bank_mask:0xf bound_ctrl:1
	v_add_f32_dpp v115, v151, v115 wave_shl:1 row_mask:0xf bank_mask:0xf bound_ctrl:1
	v_add_f32_dpp v116, v142, v116 wave_shl:1 row_mask:0xf bank_mask:0xf bound_ctrl:1
	v_add_f32_dpp v117, v143, v117 wave_shl:1 row_mask:0xf bank_mask:0xf bound_ctrl:1
	v_add_f32_dpp v118, v152, v118 wave_shl:1 row_mask:0xf bank_mask:0xf bound_ctrl:1
	v_add_f32_dpp v119, v153, v119 wave_shl:1 row_mask:0xf bank_mask:0xf bound_ctrl:1
	v_add_f32_dpp v120, v154, v120 wave_shl:1 row_mask:0xf bank_mask:0xf bound_ctrl:1
	v_add_f32_dpp v121, v155, v121 wave_shl:1 row_mask:0xf bank_mask:0xf bound_ctrl:1
	v_add_f32_dpp v122, v156, v122 wave_shl:1 row_mask:0xf bank_mask:0xf bound_ctrl:1
	v_add_f32_dpp v123, v157, v123 wave_shl:1 row_mask:0xf bank_mask:0xf bound_ctrl:1
	v_pk_add_f32 v[108:109], v[46:47], v[92:93]
	v_pk_add_f32 v[124:125], v[68:69], v[108:109]
	v_pk_add_f32 v[46:47], v[48:49], v[110:111]
	v_pk_add_f32 v[68:69], v[70:71], v[46:47]
	v_pk_add_f32 v[48:49], v[50:51], v[112:113]
	v_pk_add_f32 v[70:71], v[72:73], v[48:49]
	v_pk_add_f32 v[50:51], v[52:53], v[114:115]
	v_pk_add_f32 v[72:73], v[74:75], v[50:51]
	v_pk_add_f32 v[52:53], v[54:55], v[116:117]
	v_pk_add_f32 v[74:75], v[76:77], v[52:53]
	v_pk_add_f32 v[54:55], v[56:57], v[118:119]
	v_pk_add_f32 v[76:77], v[78:79], v[54:55]
	v_pk_add_f32 v[56:57], v[60:61], v[120:121]
	v_pk_add_f32 v[78:79], v[80:81], v[56:57]
	v_pk_add_f32 v[60:61], v[62:63], v[122:123]
	v_pk_add_f32 v[80:81], v[82:83], v[60:61]
	v_pk_fma_f32 v[78:79], v[36:37], v[124:125], v[78:79] op_sel_hi:[0,1,1]
	v_pk_fma_f32 v[80:81], v[36:37], v[68:69], v[80:81] op_sel_hi:[0,1,1]
	v_pk_fma_f32 v[78:79], v[36:37], v[70:71], v[78:79] op_sel:[1,0,0]
	v_pk_fma_f32 v[80:81], v[36:37], v[72:73], v[80:81] op_sel:[1,0,0]
	v_pk_fma_f32 v[78:79], v[38:39], v[74:75], v[78:79] op_sel_hi:[0,1,1]
	v_pk_fma_f32 v[80:81], v[38:39], v[76:77], v[80:81] op_sel_hi:[0,1,1]
	v_cndmask_b32_e64 v62, 0, v1, s[10:11]
	v_cndmask_b32_e64 v63, 0, v1, s[14:15]
	v_cndmask_b32_e64 v82, 0, v1, s[20:21]
	v_cndmask_b32_e64 v83, 0, v1, s[22:23]
	v_pk_fma_f32 v[78:79], v[14:15], v[146:147], v[78:79] op_sel_hi:[1,0,1] neg_lo:[0,0,1] neg_hi:[0,0,1]
	v_pk_fma_f32 v[80:81], v[16:17], v[146:147], v[80:81] op_sel_hi:[1,0,1] neg_lo:[0,0,1] neg_hi:[0,0,1]
	s_add_i32 s4, s34, 0
	s_cmpk_lt_i32 s4, 0x201
	s_cselect_b64 s[12:13], s[0:1], 0
	v_pk_add_f32 v[78:79], v[78:79], v[62:63] neg_lo:[0,1] neg_hi:[0,1]
	v_pk_add_f32 v[80:81], v[80:81], v[82:83] neg_lo:[0,1] neg_hi:[0,1]
	v_pk_mul_f32 v[142:143], v[78:79], v[78:79]
	v_pk_fma_f32 v[142:143], v[80:81], v[80:81], v[142:143]
	v_add_f32_e32 v142, v142, v143
	v_cndmask_b32_e64 v143, 0, v142, s[12:13]
	v_add_f32_e32 v0, v0, v143
	s_add_i32 s4, s34, 5
	s_min_i32 s4, s4, 0x200
	s_mul_i32 s5, s4, 0x804
	s_add_i32 s5, s5, s35
	s_add_i32 s6, s5, 0x101004
	s_add_i32 s7, s5, 0x202008
	s_add_i32 s8, s5, 0x30300c
	s_mul_i32 s9, s4, 0x180c
	s_add_i32 s9, s9, s33
	buffer_load_dword v14, v28, s[16:19], s5 offen nt
	buffer_load_dword v15, v28, s[16:19], s6 offen nt
	buffer_load_dword v16, v28, s[16:19], s7 offen nt
	buffer_load_dword v17, v28, s[16:19], s8 offen nt
	buffer_load_dwordx3 v[36:38], v27, s[24:27], s9 offen nt
	s_waitcnt vmcnt(10)
	v_pk_mul_f32 v[62:63], v[2:3], v[8:9] op_sel_hi:[1,0]
	v_pk_mul_f32 v[68:69], v[4:5], v[8:9] op_sel_hi:[1,0]
	v_pk_mul_f32 v[70:71], v[2:3], v[8:9] op_sel:[0,1]
	v_pk_mul_f32 v[72:73], v[4:5], v[8:9] op_sel:[0,1]
	v_pk_mul_f32 v[74:75], v[2:3], v[10:11] op_sel_hi:[1,0]
	v_pk_mul_f32 v[76:77], v[4:5], v[10:11] op_sel_hi:[1,0]
	v_add_f32_dpp v78, v2, v2 wave_shr:1 row_mask:0xf bank_mask:0xf bound_ctrl:1
	v_add_f32_dpp v79, v3, v3 wave_shr:1 row_mask:0xf bank_mask:0xf bound_ctrl:1
	v_add_f32_dpp v80, v4, v4 wave_shr:1 row_mask:0xf bank_mask:0xf bound_ctrl:1
	v_add_f32_dpp v81, v5, v5 wave_shr:1 row_mask:0xf bank_mask:0xf bound_ctrl:1
	v_add_f32_dpp v82, v62, v62 wave_shr:1 row_mask:0xf bank_mask:0xf bound_ctrl:1
	v_add_f32_dpp v83, v63, v63 wave_shr:1 row_mask:0xf bank_mask:0xf bound_ctrl:1
	v_add_f32_dpp v84, v68, v68 wave_shr:1 row_mask:0xf bank_mask:0xf bound_ctrl:1
	v_add_f32_dpp v85, v69, v69 wave_shr:1 row_mask:0xf bank_mask:0xf bound_ctrl:1
	v_add_f32_dpp v86, v70, v70 wave_shr:1 row_mask:0xf bank_mask:0xf bound_ctrl:1
	v_add_f32_dpp v87, v71, v71 wave_shr:1 row_mask:0xf bank_mask:0xf bound_ctrl:1
	v_add_f32_dpp v88, v72, v72 wave_shr:1 row_mask:0xf bank_mask:0xf bound_ctrl:1
	v_add_f32_dpp v89, v73, v73 wave_shr:1 row_mask:0xf bank_mask:0xf bound_ctrl:1
	v_add_f32_dpp v90, v74, v74 wave_shr:1 row_mask:0xf bank_mask:0xf bound_ctrl:1
	v_add_f32_dpp v91, v75, v75 wave_shr:1 row_mask:0xf bank_mask:0xf bound_ctrl:1
	v_add_f32_dpp v124, v76, v76 wave_shr:1 row_mask:0xf bank_mask:0xf bound_ctrl:1
	v_add_f32_dpp v125, v77, v77 wave_shr:1 row_mask:0xf bank_mask:0xf bound_ctrl:1
	v_add_f32_dpp v78, v2, v78 wave_shl:1 row_mask:0xf bank_mask:0xf bound_ctrl:1
	v_add_f32_dpp v79, v3, v79 wave_shl:1 row_mask:0xf bank_mask:0xf bound_ctrl:1
	v_add_f32_dpp v80, v4, v80 wave_shl:1 row_mask:0xf bank_mask:0xf bound_ctrl:1
	v_add_f32_dpp v81, v5, v81 wave_shl:1 row_mask:0xf bank_mask:0xf bound_ctrl:1
	v_add_f32_dpp v82, v62, v82 wave_shl:1 row_mask:0xf bank_mask:0xf bound_ctrl:1
	v_add_f32_dpp v83, v63, v83 wave_shl:1 row_mask:0xf bank_mask:0xf bound_ctrl:1
	v_add_f32_dpp v84, v68, v84 wave_shl:1 row_mask:0xf bank_mask:0xf bound_ctrl:1
	v_add_f32_dpp v85, v69, v85 wave_shl:1 row_mask:0xf bank_mask:0xf bound_ctrl:1
	v_add_f32_dpp v86, v70, v86 wave_shl:1 row_mask:0xf bank_mask:0xf bound_ctrl:1
	v_add_f32_dpp v87, v71, v87 wave_shl:1 row_mask:0xf bank_mask:0xf bound_ctrl:1
	v_add_f32_dpp v88, v72, v88 wave_shl:1 row_mask:0xf bank_mask:0xf bound_ctrl:1
	v_add_f32_dpp v89, v73, v89 wave_shl:1 row_mask:0xf bank_mask:0xf bound_ctrl:1
	v_add_f32_dpp v90, v74, v90 wave_shl:1 row_mask:0xf bank_mask:0xf bound_ctrl:1
	v_add_f32_dpp v91, v75, v91 wave_shl:1 row_mask:0xf bank_mask:0xf bound_ctrl:1
	v_add_f32_dpp v124, v76, v124 wave_shl:1 row_mask:0xf bank_mask:0xf bound_ctrl:1
	v_add_f32_dpp v125, v77, v125 wave_shl:1 row_mask:0xf bank_mask:0xf bound_ctrl:1
	s_barrier
	ds_read_b128 v[68:71], v23 offset:3072
	ds_read_b128 v[72:75], v23 offset:4096
	ds_read_b128 v[144:147], v23 offset:5120
	v_pk_add_f32 v[62:63], v[58:59], v[78:79]
	v_pk_add_f32 v[58:59], v[94:95], v[80:81]
	v_pk_add_f32 v[76:77], v[96:97], v[82:83]
	v_pk_add_f32 v[94:95], v[98:99], v[84:85]
	v_pk_add_f32 v[96:97], v[100:101], v[86:87]
	v_pk_add_f32 v[98:99], v[102:103], v[88:89]
	v_pk_add_f32 v[100:101], v[104:105], v[90:91]
	v_pk_add_f32 v[102:103], v[106:107], v[124:125]
	s_waitcnt lgkmcnt(2)
	v_pk_fma_f32 v[76:77], v[68:69], v[62:63], v[76:77] op_sel_hi:[0,1,1] neg_lo:[1,0,0] neg_hi:[1,0,0]
	v_pk_fma_f32 v[94:95], v[68:69], v[58:59], v[94:95] op_sel_hi:[0,1,1] neg_lo:[1,0,0] neg_hi:[1,0,0]
	v_pk_fma_f32 v[96:97], v[68:69], v[62:63], v[96:97] op_sel:[1,0,0] neg_lo:[1,0,0] neg_hi:[1,0,0]
	v_pk_fma_f32 v[98:99], v[68:69], v[58:59], v[98:99] op_sel:[1,0,0] neg_lo:[1,0,0] neg_hi:[1,0,0]
	v_pk_fma_f32 v[100:101], v[70:71], v[62:63], v[100:101] op_sel_hi:[0,1,1] neg_lo:[1,0,0] neg_hi:[1,0,0]
	v_pk_fma_f32 v[102:103], v[70:71], v[58:59], v[102:103] op_sel_hi:[0,1,1] neg_lo:[1,0,0] neg_hi:[1,0,0]
	v_pk_mul_f32 v[104:105], v[70:71], v[76:77] op_sel:[1,0]
	v_pk_mul_f32 v[148:149], v[70:71], v[94:95] op_sel:[1,0]
	s_waitcnt lgkmcnt(1)
	v_pk_mul_f32 v[106:107], v[72:73], v[76:77] op_sel_hi:[0,1]
	v_pk_mul_f32 v[150:151], v[72:73], v[94:95] op_sel_hi:[0,1]
	v_pk_mul_f32 v[142:143], v[72:73], v[76:77] op_sel:[1,0]
	v_pk_mul_f32 v[152:153], v[72:73], v[94:95] op_sel:[1,0]
	v_pk_fma_f32 v[104:105], v[72:73], v[96:97], v[104:105] op_sel_hi:[0,1,1]
	v_pk_fma_f32 v[148:149], v[72:73], v[98:99], v[148:149] op_sel_hi:[0,1,1]
	v_pk_fma_f32 v[106:107], v[74:75], v[96:97], v[106:107] op_sel_hi:[0,1,1]
	v_pk_fma_f32 v[150:151], v[74:75], v[98:99], v[150:151] op_sel_hi:[0,1,1]
	v_pk_fma_f32 v[142:143], v[74:75], v[96:97], v[142:143] op_sel:[1,0,0]
	v_pk_fma_f32 v[152:153], v[74:75], v[98:99], v[152:153] op_sel:[1,0,0]
	v_pk_fma_f32 v[104:105], v[72:73], v[100:101], v[104:105] op_sel:[1,0,0]
	v_pk_fma_f32 v[148:149], v[72:73], v[102:103], v[148:149] op_sel:[1,0,0]
	v_pk_fma_f32 v[106:107], v[74:75], v[100:101], v[106:107] op_sel:[1,0,0]
	v_pk_fma_f32 v[150:151], v[74:75], v[102:103], v[150:151] op_sel:[1,0,0]
	s_waitcnt lgkmcnt(0)
	v_pk_fma_f32 v[142:143], v[144:145], v[100:101], v[142:143] op_sel_hi:[0,1,1]
	v_pk_fma_f32 v[152:153], v[144:145], v[102:103], v[152:153] op_sel_hi:[0,1,1]
	v_pk_mul_f32 v[154:155], v[68:69], v[104:105] op_sel_hi:[0,1]
	v_pk_mul_f32 v[156:157], v[68:69], v[148:149] op_sel_hi:[0,1]
	v_pk_fma_f32 v[154:155], v[68:69], v[106:107], v[154:155] op_sel:[1,0,0]
	v_pk_fma_f32 v[156:157], v[68:69], v[150:151], v[156:157] op_sel:[1,0,0]
	v_pk_fma_f32 v[154:155], v[70:71], v[142:143], v[154:155] op_sel_hi:[0,1,1]
	v_pk_fma_f32 v[156:157], v[70:71], v[152:153], v[156:157] op_sel_hi:[0,1,1]
	v_pk_fma_f32 v[154:155], v[144:145], v[62:63], v[154:155] op_sel:[1,0,0] neg_lo:[0,0,1] neg_hi:[0,0,1]
	v_pk_fma_f32 v[156:157], v[144:145], v[58:59], v[156:157] op_sel:[1,0,0] neg_lo:[0,0,1] neg_hi:[0,0,1]
	v_cmp_eq_u32_e64 s[10:11], 1, v147
	v_cmp_eq_u32_e64 s[14:15], 2, v147
	v_cmp_eq_u32_e64 s[20:21], 3, v147
	v_cmp_eq_u32_e64 s[22:23], 4, v147
	v_add_f32_dpp v58, v104, v104 wave_shr:1 row_mask:0xf bank_mask:0xf bound_ctrl:1
	v_add_f32_dpp v59, v105, v105 wave_shr:1 row_mask:0xf bank_mask:0xf bound_ctrl:1
	v_add_f32_dpp v62, v148, v148 wave_shr:1 row_mask:0xf bank_mask:0xf bound_ctrl:1
	v_add_f32_dpp v63, v149, v149 wave_shr:1 row_mask:0xf bank_mask:0xf bound_ctrl:1
	v_add_f32_dpp v76, v106, v106 wave_shr:1 row_mask:0xf bank_mask:0xf bound_ctrl:1
	v_add_f32_dpp v77, v107, v107 wave_shr:1 row_mask:0xf bank_mask:0xf bound_ctrl:1
	v_add_f32_dpp v94, v150, v150 wave_shr:1 row_mask:0xf bank_mask:0xf bound_ctrl:1
	v_add_f32_dpp v95, v151, v151 wave_shr:1 row_mask:0xf bank_mask:0xf bound_ctrl:1
	v_add_f32_dpp v96, v142, v142 wave_shr:1 row_mask:0xf bank_mask:0xf bound_ctrl:1
	v_add_f32_dpp v97, v143, v143 wave_shr:1 row_mask:0xf bank_mask:0xf bound_ctrl:1
	v_add_f32_dpp v98, v152, v152 wave_shr:1 row_mask:0xf bank_mask:0xf bound_ctrl:1
	v_add_f32_dpp v99, v153, v153 wave_shr:1 row_mask:0xf bank_mask:0xf bound_ctrl:1
	v_add_f32_dpp v100, v154, v154 wave_shr:1 row_mask:0xf bank_mask:0xf bound_ctrl:1
	v_add_f32_dpp v101, v155, v155 wave_shr:1 row_mask:0xf bank_mask:0xf bound_ctrl:1
	v_add_f32_dpp v102, v156, v156 wave_shr:1 row_mask:0xf bank_mask:0xf bound_ctrl:1
	v_add_f32_dpp v103, v157, v157 wave_shr:1 row_mask:0xf bank_mask:0xf bound_ctrl:1
	v_add_f32_dpp v58, v104, v58 wave_shl:1 row_mask:0xf bank_mask:0xf bound_ctrl:1
	v_add_f32_dpp v59, v105, v59 wave_shl:1 row_mask:0xf bank_mask:0xf bound_ctrl:1
	v_add_f32_dpp v62, v148, v62 wave_shl:1 row_mask:0xf bank_mask:0xf bound_ctrl:1
	v_add_f32_dpp v63, v149, v63 wave_shl:1 row_mask:0xf bank_mask:0xf bound_ctrl:1
	v_add_f32_dpp v76, v106, v76 wave_shl:1 row_mask:0xf bank_mask:0xf bound_ctrl:1
	v_add_f32_dpp v77, v107, v77 wave_shl:1 row_mask:0xf bank_mask:0xf bound_ctrl:1
	v_add_f32_dpp v94, v150, v94 wave_shl:1 row_mask:0xf bank_mask:0xf bound_ctrl:1
	v_add_f32_dpp v95, v151, v95 wave_shl:1 row_mask:0xf bank_mask:0xf bound_ctrl:1
	v_add_f32_dpp v96, v142, v96 wave_shl:1 row_mask:0xf bank_mask:0xf bound_ctrl:1
	v_add_f32_dpp v97, v143, v97 wave_shl:1 row_mask:0xf bank_mask:0xf bound_ctrl:1
	v_add_f32_dpp v98, v152, v98 wave_shl:1 row_mask:0xf bank_mask:0xf bound_ctrl:1
	v_add_f32_dpp v99, v153, v99 wave_shl:1 row_mask:0xf bank_mask:0xf bound_ctrl:1
	v_add_f32_dpp v100, v154, v100 wave_shl:1 row_mask:0xf bank_mask:0xf bound_ctrl:1
	v_add_f32_dpp v101, v155, v101 wave_shl:1 row_mask:0xf bank_mask:0xf bound_ctrl:1
	v_add_f32_dpp v102, v156, v102 wave_shl:1 row_mask:0xf bank_mask:0xf bound_ctrl:1
	v_add_f32_dpp v103, v157, v103 wave_shl:1 row_mask:0xf bank_mask:0xf bound_ctrl:1
	v_pk_add_f32 v[104:105], v[108:109], v[58:59]
	v_pk_add_f32 v[106:107], v[46:47], v[62:63]
	v_pk_add_f32 v[46:47], v[48:49], v[76:77]
	v_pk_add_f32 v[48:49], v[50:51], v[94:95]
	v_pk_add_f32 v[50:51], v[52:53], v[96:97]
	v_pk_add_f32 v[52:53], v[54:55], v[98:99]
	v_pk_add_f32 v[54:55], v[56:57], v[100:101]
	v_pk_add_f32 v[56:57], v[60:61], v[102:103]
	v_pk_fma_f32 v[54:55], v[40:41], v[104:105], v[54:55] op_sel_hi:[0,1,1]
	v_pk_fma_f32 v[56:57], v[40:41], v[106:107], v[56:57] op_sel_hi:[0,1,1]
	v_pk_fma_f32 v[54:55], v[40:41], v[46:47], v[54:55] op_sel:[1,0,0]
	v_pk_fma_f32 v[56:57], v[40:41], v[48:49], v[56:57] op_sel:[1,0,0]
	v_pk_fma_f32 v[54:55], v[42:43], v[50:51], v[54:55] op_sel_hi:[0,1,1]
	v_pk_fma_f32 v[56:57], v[42:43], v[52:53], v[56:57] op_sel_hi:[0,1,1]
	v_cndmask_b32_e64 v60, 0, v1, s[10:11]
	v_cndmask_b32_e64 v61, 0, v1, s[14:15]
	v_cndmask_b32_e64 v108, 0, v1, s[20:21]
	v_cndmask_b32_e64 v109, 0, v1, s[22:23]
	v_pk_fma_f32 v[54:55], v[20:21], v[146:147], v[54:55] op_sel_hi:[1,0,1] neg_lo:[0,0,1] neg_hi:[0,0,1]
	v_pk_fma_f32 v[56:57], v[24:25], v[146:147], v[56:57] op_sel_hi:[1,0,1] neg_lo:[0,0,1] neg_hi:[0,0,1]
	s_add_i32 s4, s34, 1
	s_cmpk_lt_i32 s4, 0x201
	s_cselect_b64 s[12:13], s[0:1], 0
	v_pk_add_f32 v[54:55], v[54:55], v[60:61] neg_lo:[0,1] neg_hi:[0,1]
	v_pk_add_f32 v[56:57], v[56:57], v[108:109] neg_lo:[0,1] neg_hi:[0,1]
	v_pk_mul_f32 v[142:143], v[54:55], v[54:55]
	v_pk_fma_f32 v[142:143], v[56:57], v[56:57], v[142:143]
	v_add_f32_e32 v142, v142, v143
	v_cndmask_b32_e64 v143, 0, v142, s[12:13]
	v_add_f32_e32 v0, v0, v143
	s_add_i32 s4, s34, 6
	s_min_i32 s4, s4, 0x200
	s_mul_i32 s5, s4, 0x804
	s_add_i32 s5, s5, s35
	s_add_i32 s6, s5, 0x101004
	s_add_i32 s7, s5, 0x202008
	s_add_i32 s8, s5, 0x30300c
	s_mul_i32 s9, s4, 0x180c
	s_add_i32 s9, s9, s33
	buffer_load_dword v20, v28, s[16:19], s5 offen nt
	buffer_load_dword v21, v28, s[16:19], s6 offen nt
	buffer_load_dword v24, v28, s[16:19], s7 offen nt
	buffer_load_dword v25, v28, s[16:19], s8 offen nt
	buffer_load_dwordx3 v[40:42], v27, s[24:27], s9 offen nt
	s_waitcnt vmcnt(10)
	v_pk_mul_f32 v[46:47], v[6:7], v[32:33] op_sel_hi:[1,0]
	v_pk_mul_f32 v[48:49], v[12:13], v[32:33] op_sel_hi:[1,0]
	v_pk_mul_f32 v[50:51], v[6:7], v[32:33] op_sel:[0,1]
	v_pk_mul_f32 v[52:53], v[12:13], v[32:33] op_sel:[0,1]
	v_pk_mul_f32 v[54:55], v[6:7], v[34:35] op_sel_hi:[1,0]
	v_pk_mul_f32 v[56:57], v[12:13], v[34:35] op_sel_hi:[1,0]
	v_add_f32_dpp v60, v6, v6 wave_shr:1 row_mask:0xf bank_mask:0xf bound_ctrl:1
	v_add_f32_dpp v61, v7, v7 wave_shr:1 row_mask:0xf bank_mask:0xf bound_ctrl:1
	v_add_f32_dpp v68, v12, v12 wave_shr:1 row_mask:0xf bank_mask:0xf bound_ctrl:1
	v_add_f32_dpp v69, v13, v13 wave_shr:1 row_mask:0xf bank_mask:0xf bound_ctrl:1
	v_add_f32_dpp v70, v46, v46 wave_shr:1 row_mask:0xf bank_mask:0xf bound_ctrl:1
	v_add_f32_dpp v71, v47, v47 wave_shr:1 row_mask:0xf bank_mask:0xf bound_ctrl:1
	v_add_f32_dpp v72, v48, v48 wave_shr:1 row_mask:0xf bank_mask:0xf bound_ctrl:1
	v_add_f32_dpp v73, v49, v49 wave_shr:1 row_mask:0xf bank_mask:0xf bound_ctrl:1
	v_add_f32_dpp v74, v50, v50 wave_shr:1 row_mask:0xf bank_mask:0xf bound_ctrl:1
	v_add_f32_dpp v75, v51, v51 wave_shr:1 row_mask:0xf bank_mask:0xf bound_ctrl:1
	v_add_f32_dpp v104, v52, v52 wave_shr:1 row_mask:0xf bank_mask:0xf bound_ctrl:1
	v_add_f32_dpp v105, v53, v53 wave_shr:1 row_mask:0xf bank_mask:0xf bound_ctrl:1
	v_add_f32_dpp v106, v54, v54 wave_shr:1 row_mask:0xf bank_mask:0xf bound_ctrl:1
	v_add_f32_dpp v107, v55, v55 wave_shr:1 row_mask:0xf bank_mask:0xf bound_ctrl:1
	v_add_f32_dpp v108, v56, v56 wave_shr:1 row_mask:0xf bank_mask:0xf bound_ctrl:1
	v_add_f32_dpp v109, v57, v57 wave_shr:1 row_mask:0xf bank_mask:0xf bound_ctrl:1
	v_add_f32_dpp v60, v6, v60 wave_shl:1 row_mask:0xf bank_mask:0xf bound_ctrl:1
	v_add_f32_dpp v61, v7, v61 wave_shl:1 row_mask:0xf bank_mask:0xf bound_ctrl:1
	v_add_f32_dpp v68, v12, v68 wave_shl:1 row_mask:0xf bank_mask:0xf bound_ctrl:1
	v_add_f32_dpp v69, v13, v69 wave_shl:1 row_mask:0xf bank_mask:0xf bound_ctrl:1
	v_add_f32_dpp v70, v46, v70 wave_shl:1 row_mask:0xf bank_mask:0xf bound_ctrl:1
	v_add_f32_dpp v71, v47, v71 wave_shl:1 row_mask:0xf bank_mask:0xf bound_ctrl:1
	v_add_f32_dpp v72, v48, v72 wave_shl:1 row_mask:0xf bank_mask:0xf bound_ctrl:1
	v_add_f32_dpp v73, v49, v73 wave_shl:1 row_mask:0xf bank_mask:0xf bound_ctrl:1
	v_add_f32_dpp v74, v50, v74 wave_shl:1 row_mask:0xf bank_mask:0xf bound_ctrl:1
	v_add_f32_dpp v75, v51, v75 wave_shl:1 row_mask:0xf bank_mask:0xf bound_ctrl:1
	v_add_f32_dpp v104, v52, v104 wave_shl:1 row_mask:0xf bank_mask:0xf bound_ctrl:1
	v_add_f32_dpp v105, v53, v105 wave_shl:1 row_mask:0xf bank_mask:0xf bound_ctrl:1
	v_add_f32_dpp v106, v54, v106 wave_shl:1 row_mask:0xf bank_mask:0xf bound_ctrl:1
	v_add_f32_dpp v107, v55, v107 wave_shl:1 row_mask:0xf bank_mask:0xf bound_ctrl:1
	v_add_f32_dpp v108, v56, v108 wave_shl:1 row_mask:0xf bank_mask:0xf bound_ctrl:1
	v_add_f32_dpp v109, v57, v109 wave_shl:1 row_mask:0xf bank_mask:0xf bound_ctrl:1
	s_barrier
	ds_read_b128 v[48:51], v23 offset:0
	ds_read_b128 v[52:55], v23 offset:1024
	ds_read_b128 v[144:147], v23 offset:2048
	v_pk_add_f32 v[46:47], v[78:79], v[60:61]
	v_pk_add_f32 v[56:57], v[126:127], v[46:47]
	v_pk_add_f32 v[78:79], v[80:81], v[68:69]
	v_pk_add_f32 v[126:127], v[128:129], v[78:79]
	v_pk_add_f32 v[80:81], v[82:83], v[70:71]
	v_pk_add_f32 v[128:129], v[130:131], v[80:81]
	v_pk_add_f32 v[82:83], v[84:85], v[72:73]
	v_pk_add_f32 v[130:131], v[132:133], v[82:83]
	v_pk_add_f32 v[84:85], v[86:87], v[74:75]
	v_pk_add_f32 v[132:133], v[134:135], v[84:85]
	v_pk_add_f32 v[86:87], v[88:89], v[104:105]
	v_pk_add_f32 v[134:135], v[136:137], v[86:87]
	v_pk_add_f32 v[88:89], v[90:91], v[106:107]
	v_pk_add_f32 v[136:137], v[138:139], v[88:89]
	v_pk_add_f32 v[90:91], v[124:125], v[108:109]
	v_pk_add_f32 v[138:139], v[140:141], v[90:91]
	s_waitcnt lgkmcnt(2)
	v_pk_fma_f32 v[128:129], v[48:49], v[56:57], v[128:129] op_sel_hi:[0,1,1] neg_lo:[1,0,0] neg_hi:[1,0,0]
	v_pk_fma_f32 v[130:131], v[48:49], v[126:127], v[130:131] op_sel_hi:[0,1,1] neg_lo:[1,0,0] neg_hi:[1,0,0]
	v_pk_fma_f32 v[132:133], v[48:49], v[56:57], v[132:133] op_sel:[1,0,0] neg_lo:[1,0,0] neg_hi:[1,0,0]
	v_pk_fma_f32 v[134:135], v[48:49], v[126:127], v[134:135] op_sel:[1,0,0] neg_lo:[1,0,0] neg_hi:[1,0,0]
	v_pk_fma_f32 v[136:137], v[50:51], v[56:57], v[136:137] op_sel_hi:[0,1,1] neg_lo:[1,0,0] neg_hi:[1,0,0]
	v_pk_fma_f32 v[138:139], v[50:51], v[126:127], v[138:139] op_sel_hi:[0,1,1] neg_lo:[1,0,0] neg_hi:[1,0,0]
	v_pk_mul_f32 v[124:125], v[50:51], v[128:129] op_sel:[1,0]
	v_pk_mul_f32 v[148:149], v[50:51], v[130:131] op_sel:[1,0]
	s_waitcnt lgkmcnt(1)
	v_pk_mul_f32 v[140:141], v[52:53], v[128:129] op_sel_hi:[0,1]
	v_pk_mul_f32 v[150:151], v[52:53], v[130:131] op_sel_hi:[0,1]
	v_pk_mul_f32 v[142:143], v[52:53], v[128:129] op_sel:[1,0]
	v_pk_mul_f32 v[152:153], v[52:53], v[130:131] op_sel:[1,0]
	v_pk_fma_f32 v[124:125], v[52:53], v[132:133], v[124:125] op_sel_hi:[0,1,1]
	v_pk_fma_f32 v[148:149], v[52:53], v[134:135], v[148:149] op_sel_hi:[0,1,1]
	v_pk_fma_f32 v[140:141], v[54:55], v[132:133], v[140:141] op_sel_hi:[0,1,1]
	v_pk_fma_f32 v[150:151], v[54:55], v[134:135], v[150:151] op_sel_hi:[0,1,1]
	v_pk_fma_f32 v[142:143], v[54:55], v[132:133], v[142:143] op_sel:[1,0,0]
	v_pk_fma_f32 v[152:153], v[54:55], v[134:135], v[152:153] op_sel:[1,0,0]
	v_pk_fma_f32 v[124:125], v[52:53], v[136:137], v[124:125] op_sel:[1,0,0]
	v_pk_fma_f32 v[148:149], v[52:53], v[138:139], v[148:149] op_sel:[1,0,0]
	v_pk_fma_f32 v[140:141], v[54:55], v[136:137], v[140:141] op_sel:[1,0,0]
	v_pk_fma_f32 v[150:151], v[54:55], v[138:139], v[150:151] op_sel:[1,0,0]
	s_waitcnt lgkmcnt(0)
	v_pk_fma_f32 v[142:143], v[144:145], v[136:137], v[142:143] op_sel_hi:[0,1,1]
	v_pk_fma_f32 v[152:153], v[144:145], v[138:139], v[152:153] op_sel_hi:[0,1,1]
	v_pk_mul_f32 v[154:155], v[48:49], v[124:125] op_sel_hi:[0,1]
	v_pk_mul_f32 v[156:157], v[48:49], v[148:149] op_sel_hi:[0,1]
	v_pk_fma_f32 v[154:155], v[48:49], v[140:141], v[154:155] op_sel:[1,0,0]
	v_pk_fma_f32 v[156:157], v[48:49], v[150:151], v[156:157] op_sel:[1,0,0]
	v_pk_fma_f32 v[154:155], v[50:51], v[142:143], v[154:155] op_sel_hi:[0,1,1]
	v_pk_fma_f32 v[156:157], v[50:51], v[152:153], v[156:157] op_sel_hi:[0,1,1]
	v_pk_fma_f32 v[154:155], v[144:145], v[56:57], v[154:155] op_sel:[1,0,0] neg_lo:[0,0,1] neg_hi:[0,0,1]
	v_pk_fma_f32 v[156:157], v[144:145], v[126:127], v[156:157] op_sel:[1,0,0] neg_lo:[0,0,1] neg_hi:[0,0,1]
	v_cmp_eq_u32_e64 s[10:11], 1, v147
	v_cmp_eq_u32_e64 s[14:15], 2, v147
	v_cmp_eq_u32_e64 s[20:21], 3, v147
	v_cmp_eq_u32_e64 s[22:23], 4, v147
	v_add_f32_dpp v56, v124, v124 wave_shr:1 row_mask:0xf bank_mask:0xf bound_ctrl:1
	v_add_f32_dpp v57, v125, v125 wave_shr:1 row_mask:0xf bank_mask:0xf bound_ctrl:1
	v_add_f32_dpp v126, v148, v148 wave_shr:1 row_mask:0xf bank_mask:0xf bound_ctrl:1
	v_add_f32_dpp v127, v149, v149 wave_shr:1 row_mask:0xf bank_mask:0xf bound_ctrl:1
	v_add_f32_dpp v128, v140, v140 wave_shr:1 row_mask:0xf bank_mask:0xf bound_ctrl:1
	v_add_f32_dpp v129, v141, v141 wave_shr:1 row_mask:0xf bank_mask:0xf bound_ctrl:1
	v_add_f32_dpp v130, v150, v150 wave_shr:1 row_mask:0xf bank_mask:0xf bound_ctrl:1
	v_add_f32_dpp v131, v151, v151 wave_shr:1 row_mask:0xf bank_mask:0xf bound_ctrl:1
	v_add_f32_dpp v132, v142, v142 wave_shr:1 row_mask:0xf bank_mask:0xf bound_ctrl:1
	v_add_f32_dpp v133, v143, v143 wave_shr:1 row_mask:0xf bank_mask:0xf bound_ctrl:1
	v_add_f32_dpp v134, v152, v152 wave_shr:1 row_mask:0xf bank_mask:0xf bound_ctrl:1
	v_add_f32_dpp v135, v153, v153 wave_shr:1 row_mask:0xf bank_mask:0xf bound_ctrl:1
	v_add_f32_dpp v136, v154, v154 wave_shr:1 row_mask:0xf bank_mask:0xf bound_ctrl:1
	v_add_f32_dpp v137, v155, v155 wave_shr:1 row_mask:0xf bank_mask:0xf bound_ctrl:1
	v_add_f32_dpp v138, v156, v156 wave_shr:1 row_mask:0xf bank_mask:0xf bound_ctrl:1
	v_add_f32_dpp v139, v157, v157 wave_shr:1 row_mask:0xf bank_mask:0xf bound_ctrl:1
	v_add_f32_dpp v56, v124, v56 wave_shl:1 row_mask:0xf bank_mask:0xf bound_ctrl:1
	v_add_f32_dpp v57, v125, v57 wave_shl:1 row_mask:0xf bank_mask:0xf bound_ctrl:1
	v_add_f32_dpp v126, v148, v126 wave_shl:1 row_mask:0xf bank_mask:0xf bound_ctrl:1
	v_add_f32_dpp v127, v149, v127 wave_shl:1 row_mask:0xf bank_mask:0xf bound_ctrl:1
	v_add_f32_dpp v128, v140, v128 wave_shl:1 row_mask:0xf bank_mask:0xf bound_ctrl:1
	v_add_f32_dpp v129, v141, v129 wave_shl:1 row_mask:0xf bank_mask:0xf bound_ctrl:1
	v_add_f32_dpp v130, v150, v130 wave_shl:1 row_mask:0xf bank_mask:0xf bound_ctrl:1
	v_add_f32_dpp v131, v151, v131 wave_shl:1 row_mask:0xf bank_mask:0xf bound_ctrl:1
	v_add_f32_dpp v132, v142, v132 wave_shl:1 row_mask:0xf bank_mask:0xf bound_ctrl:1
	v_add_f32_dpp v133, v143, v133 wave_shl:1 row_mask:0xf bank_mask:0xf bound_ctrl:1
	v_add_f32_dpp v134, v152, v134 wave_shl:1 row_mask:0xf bank_mask:0xf bound_ctrl:1
	v_add_f32_dpp v135, v153, v135 wave_shl:1 row_mask:0xf bank_mask:0xf bound_ctrl:1
	v_add_f32_dpp v136, v154, v136 wave_shl:1 row_mask:0xf bank_mask:0xf bound_ctrl:1
	v_add_f32_dpp v137, v155, v137 wave_shl:1 row_mask:0xf bank_mask:0xf bound_ctrl:1
	v_add_f32_dpp v138, v156, v138 wave_shl:1 row_mask:0xf bank_mask:0xf bound_ctrl:1
	v_add_f32_dpp v139, v157, v139 wave_shl:1 row_mask:0xf bank_mask:0xf bound_ctrl:1
	v_pk_add_f32 v[124:125], v[58:59], v[56:57]
	v_pk_add_f32 v[140:141], v[92:93], v[124:125]
	v_pk_add_f32 v[58:59], v[62:63], v[126:127]
	v_pk_add_f32 v[92:93], v[110:111], v[58:59]
	v_pk_add_f32 v[62:63], v[76:77], v[128:129]
	v_pk_add_f32 v[110:111], v[112:113], v[62:63]
	v_pk_add_f32 v[76:77], v[94:95], v[130:131]
	v_pk_add_f32 v[112:113], v[114:115], v[76:77]
	v_pk_add_f32 v[94:95], v[96:97], v[132:133]
	v_pk_add_f32 v[114:115], v[116:117], v[94:95]
	v_pk_add_f32 v[96:97], v[98:99], v[134:135]
	v_pk_add_f32 v[116:117], v[118:119], v[96:97]
	v_pk_add_f32 v[98:99], v[100:101], v[136:137]
	v_pk_add_f32 v[118:119], v[120:121], v[98:99]
	v_pk_add_f32 v[100:101], v[102:103], v[138:139]
	v_pk_add_f32 v[120:121], v[122:123], v[100:101]
	v_pk_fma_f32 v[118:119], v[64:65], v[140:141], v[118:119] op_sel_hi:[0,1,1]
	v_pk_fma_f32 v[120:121], v[64:65], v[92:93], v[120:121] op_sel_hi:[0,1,1]
	v_pk_fma_f32 v[118:119], v[64:65], v[110:111], v[118:119] op_sel:[1,0,0]
	v_pk_fma_f32 v[120:121], v[64:65], v[112:113], v[120:121] op_sel:[1,0,0]
	v_pk_fma_f32 v[118:119], v[66:67], v[114:115], v[118:119] op_sel_hi:[0,1,1]
	v_pk_fma_f32 v[120:121], v[66:67], v[116:117], v[120:121] op_sel_hi:[0,1,1]
	v_cndmask_b32_e64 v102, 0, v1, s[10:11]
	v_cndmask_b32_e64 v103, 0, v1, s[14:15]
	v_cndmask_b32_e64 v122, 0, v1, s[20:21]
	v_cndmask_b32_e64 v123, 0, v1, s[22:23]
	v_pk_fma_f32 v[118:119], v[30:31], v[146:147], v[118:119] op_sel_hi:[1,0,1] neg_lo:[0,0,1] neg_hi:[0,0,1]
	v_pk_fma_f32 v[120:121], v[44:45], v[146:147], v[120:121] op_sel_hi:[1,0,1] neg_lo:[0,0,1] neg_hi:[0,0,1]
	s_add_i32 s4, s34, 2
	s_cmpk_lt_i32 s4, 0x201
	s_cselect_b64 s[12:13], s[0:1], 0
	v_pk_add_f32 v[118:119], v[118:119], v[102:103] neg_lo:[0,1] neg_hi:[0,1]
	v_pk_add_f32 v[120:121], v[120:121], v[122:123] neg_lo:[0,1] neg_hi:[0,1]
	v_pk_mul_f32 v[142:143], v[118:119], v[118:119]
	v_pk_fma_f32 v[142:143], v[120:121], v[120:121], v[142:143]
	v_add_f32_e32 v142, v142, v143
	v_cndmask_b32_e64 v143, 0, v142, s[12:13]
	v_add_f32_e32 v0, v0, v143
	s_add_i32 s4, s34, 7
	s_min_i32 s4, s4, 0x200
	s_mul_i32 s5, s4, 0x804
	s_add_i32 s5, s5, s35
	s_add_i32 s6, s5, 0x101004
	s_add_i32 s7, s5, 0x202008
	s_add_i32 s8, s5, 0x30300c
	s_mul_i32 s9, s4, 0x180c
	s_add_i32 s9, s9, s33
	buffer_load_dword v30, v28, s[16:19], s5 offen nt
	buffer_load_dword v31, v28, s[16:19], s6 offen nt
	buffer_load_dword v44, v28, s[16:19], s7 offen nt
	buffer_load_dword v45, v28, s[16:19], s8 offen nt
	buffer_load_dwordx3 v[48:50], v27, s[24:27], s9 offen nt
	s_waitcnt vmcnt(10)
	v_pk_mul_f32 v[52:53], v[14:15], v[36:37] op_sel_hi:[1,0]
	v_pk_mul_f32 v[54:55], v[16:17], v[36:37] op_sel_hi:[1,0]
	v_pk_mul_f32 v[64:65], v[14:15], v[36:37] op_sel:[0,1]
	v_pk_mul_f32 v[66:67], v[16:17], v[36:37] op_sel:[0,1]
	v_pk_mul_f32 v[92:93], v[14:15], v[38:39] op_sel_hi:[1,0]
	v_pk_mul_f32 v[102:103], v[16:17], v[38:39] op_sel_hi:[1,0]
	v_add_f32_dpp v110, v14, v14 wave_shr:1 row_mask:0xf bank_mask:0xf bound_ctrl:1
	v_add_f32_dpp v111, v15, v15 wave_shr:1 row_mask:0xf bank_mask:0xf bound_ctrl:1
	v_add_f32_dpp v112, v16, v16 wave_shr:1 row_mask:0xf bank_mask:0xf bound_ctrl:1
	v_add_f32_dpp v113, v17, v17 wave_shr:1 row_mask:0xf bank_mask:0xf bound_ctrl:1
	v_add_f32_dpp v114, v52, v52 wave_shr:1 row_mask:0xf bank_mask:0xf bound_ctrl:1
	v_add_f32_dpp v115, v53, v53 wave_shr:1 row_mask:0xf bank_mask:0xf bound_ctrl:1
	v_add_f32_dpp v116, v54, v54 wave_shr:1 row_mask:0xf bank_mask:0xf bound_ctrl:1
	v_add_f32_dpp v117, v55, v55 wave_shr:1 row_mask:0xf bank_mask:0xf bound_ctrl:1
	v_add_f32_dpp v118, v64, v64 wave_shr:1 row_mask:0xf bank_mask:0xf bound_ctrl:1
	v_add_f32_dpp v119, v65, v65 wave_shr:1 row_mask:0xf bank_mask:0xf bound_ctrl:1
	v_add_f32_dpp v120, v66, v66 wave_shr:1 row_mask:0xf bank_mask:0xf bound_ctrl:1
	v_add_f32_dpp v121, v67, v67 wave_shr:1 row_mask:0xf bank_mask:0xf bound_ctrl:1
	v_add_f32_dpp v122, v92, v92 wave_shr:1 row_mask:0xf bank_mask:0xf bound_ctrl:1
	v_add_f32_dpp v123, v93, v93 wave_shr:1 row_mask:0xf bank_mask:0xf bound_ctrl:1
	v_add_f32_dpp v140, v102, v102 wave_shr:1 row_mask:0xf bank_mask:0xf bound_ctrl:1
	v_add_f32_dpp v141, v103, v103 wave_shr:1 row_mask:0xf bank_mask:0xf bound_ctrl:1
	v_add_f32_dpp v110, v14, v110 wave_shl:1 row_mask:0xf bank_mask:0xf bound_ctrl:1
	v_add_f32_dpp v111, v15, v111 wave_shl:1 row_mask:0xf bank_mask:0xf bound_ctrl:1
	v_add_f32_dpp v112, v16, v112 wave_shl:1 row_mask:0xf bank_mask:0xf bound_ctrl:1
	v_add_f32_dpp v113, v17, v113 wave_shl:1 row_mask:0xf bank_mask:0xf bound_ctrl:1
	v_add_f32_dpp v114, v52, v114 wave_shl:1 row_mask:0xf bank_mask:0xf bound_ctrl:1
	v_add_f32_dpp v115, v53, v115 wave_shl:1 row_mask:0xf bank_mask:0xf bound_ctrl:1
	v_add_f32_dpp v116, v54, v116 wave_shl:1 row_mask:0xf bank_mask:0xf bound_ctrl:1
	v_add_f32_dpp v117, v55, v117 wave_shl:1 row_mask:0xf bank_mask:0xf bound_ctrl:1
	v_add_f32_dpp v118, v64, v118 wave_shl:1 row_mask:0xf bank_mask:0xf bound_ctrl:1
	v_add_f32_dpp v119, v65, v119 wave_shl:1 row_mask:0xf bank_mask:0xf bound_ctrl:1
	v_add_f32_dpp v120, v66, v120 wave_shl:1 row_mask:0xf bank_mask:0xf bound_ctrl:1
	v_add_f32_dpp v121, v67, v121 wave_shl:1 row_mask:0xf bank_mask:0xf bound_ctrl:1
	v_add_f32_dpp v122, v92, v122 wave_shl:1 row_mask:0xf bank_mask:0xf bound_ctrl:1
	v_add_f32_dpp v123, v93, v123 wave_shl:1 row_mask:0xf bank_mask:0xf bound_ctrl:1
	v_add_f32_dpp v140, v102, v140 wave_shl:1 row_mask:0xf bank_mask:0xf bound_ctrl:1
	v_add_f32_dpp v141, v103, v141 wave_shl:1 row_mask:0xf bank_mask:0xf bound_ctrl:1
	s_barrier
	ds_read_b128 v[52:55], v23 offset:3072
	ds_read_b128 v[64:67], v23 offset:4096
	ds_read_b128 v[144:147], v23 offset:5120
	v_pk_add_f32 v[92:93], v[46:47], v[110:111]
	v_pk_add_f32 v[46:47], v[78:79], v[112:113]
	v_pk_add_f32 v[78:79], v[80:81], v[114:115]
	v_pk_add_f32 v[80:81], v[82:83], v[116:117]
	v_pk_add_f32 v[82:83], v[84:85], v[118:119]
	v_pk_add_f32 v[84:85], v[86:87], v[120:121]
	v_pk_add_f32 v[86:87], v[88:89], v[122:123]
	v_pk_add_f32 v[88:89], v[90:91], v[140:141]
	s_waitcnt lgkmcnt(2)
	v_pk_fma_f32 v[78:79], v[52:53], v[92:93], v[78:79] op_sel_hi:[0,1,1] neg_lo:[1,0,0] neg_hi:[1,0,0]
	v_pk_fma_f32 v[80:81], v[52:53], v[46:47], v[80:81] op_sel_hi:[0,1,1] neg_lo:[1,0,0] neg_hi:[1,0,0]
	v_pk_fma_f32 v[82:83], v[52:53], v[92:93], v[82:83] op_sel:[1,0,0] neg_lo:[1,0,0] neg_hi:[1,0,0]
	v_pk_fma_f32 v[84:85], v[52:53], v[46:47], v[84:85] op_sel:[1,0,0] neg_lo:[1,0,0] neg_hi:[1,0,0]
	v_pk_fma_f32 v[86:87], v[54:55], v[92:93], v[86:87] op_sel_hi:[0,1,1] neg_lo:[1,0,0] neg_hi:[1,0,0]
	v_pk_fma_f32 v[88:89], v[54:55], v[46:47], v[88:89] op_sel_hi:[0,1,1] neg_lo:[1,0,0] neg_hi:[1,0,0]
	v_pk_mul_f32 v[90:91], v[54:55], v[78:79] op_sel:[1,0]
	v_pk_mul_f32 v[148:149], v[54:55], v[80:81] op_sel:[1,0]
	s_waitcnt lgkmcnt(1)
	v_pk_mul_f32 v[102:103], v[64:65], v[78:79] op_sel_hi:[0,1]
	v_pk_mul_f32 v[150:151], v[64:65], v[80:81] op_sel_hi:[0,1]
	v_pk_mul_f32 v[142:143], v[64:65], v[78:79] op_sel:[1,0]
	v_pk_mul_f32 v[152:153], v[64:65], v[80:81] op_sel:[1,0]
	v_pk_fma_f32 v[90:91], v[64:65], v[82:83], v[90:91] op_sel_hi:[0,1,1]
	v_pk_fma_f32 v[148:149], v[64:65], v[84:85], v[148:149] op_sel_hi:[0,1,1]
	v_pk_fma_f32 v[102:103], v[66:67], v[82:83], v[102:103] op_sel_hi:[0,1,1]
	v_pk_fma_f32 v[150:151], v[66:67], v[84:85], v[150:151] op_sel_hi:[0,1,1]
	v_pk_fma_f32 v[142:143], v[66:67], v[82:83], v[142:143] op_sel:[1,0,0]
	v_pk_fma_f32 v[152:153], v[66:67], v[84:85], v[152:153] op_sel:[1,0,0]
	v_pk_fma_f32 v[90:91], v[64:65], v[86:87], v[90:91] op_sel:[1,0,0]
	v_pk_fma_f32 v[148:149], v[64:65], v[88:89], v[148:149] op_sel:[1,0,0]
	v_pk_fma_f32 v[102:103], v[66:67], v[86:87], v[102:103] op_sel:[1,0,0]
	v_pk_fma_f32 v[150:151], v[66:67], v[88:89], v[150:151] op_sel:[1,0,0]
	s_waitcnt lgkmcnt(0)
	v_pk_fma_f32 v[142:143], v[144:145], v[86:87], v[142:143] op_sel_hi:[0,1,1]
	v_pk_fma_f32 v[152:153], v[144:145], v[88:89], v[152:153] op_sel_hi:[0,1,1]
	v_pk_mul_f32 v[154:155], v[52:53], v[90:91] op_sel_hi:[0,1]
	v_pk_mul_f32 v[156:157], v[52:53], v[148:149] op_sel_hi:[0,1]
	v_pk_fma_f32 v[154:155], v[52:53], v[102:103], v[154:155] op_sel:[1,0,0]
	v_pk_fma_f32 v[156:157], v[52:53], v[150:151], v[156:157] op_sel:[1,0,0]
	v_pk_fma_f32 v[154:155], v[54:55], v[142:143], v[154:155] op_sel_hi:[0,1,1]
	v_pk_fma_f32 v[156:157], v[54:55], v[152:153], v[156:157] op_sel_hi:[0,1,1]
	v_pk_fma_f32 v[154:155], v[144:145], v[92:93], v[154:155] op_sel:[1,0,0] neg_lo:[0,0,1] neg_hi:[0,0,1]
	v_pk_fma_f32 v[156:157], v[144:145], v[46:47], v[156:157] op_sel:[1,0,0] neg_lo:[0,0,1] neg_hi:[0,0,1]
	v_cmp_eq_u32_e64 s[10:11], 1, v147
	v_cmp_eq_u32_e64 s[14:15], 2, v147
	v_cmp_eq_u32_e64 s[20:21], 3, v147
	v_cmp_eq_u32_e64 s[22:23], 4, v147
	v_add_f32_dpp v46, v90, v90 wave_shr:1 row_mask:0xf bank_mask:0xf bound_ctrl:1
	v_add_f32_dpp v47, v91, v91 wave_shr:1 row_mask:0xf bank_mask:0xf bound_ctrl:1
	v_add_f32_dpp v78, v148, v148 wave_shr:1 row_mask:0xf bank_mask:0xf bound_ctrl:1
	v_add_f32_dpp v79, v149, v149 wave_shr:1 row_mask:0xf bank_mask:0xf bound_ctrl:1
	v_add_f32_dpp v80, v102, v102 wave_shr:1 row_mask:0xf bank_mask:0xf bound_ctrl:1
	v_add_f32_dpp v81, v103, v103 wave_shr:1 row_mask:0xf bank_mask:0xf bound_ctrl:1
	v_add_f32_dpp v82, v150, v150 wave_shr:1 row_mask:0xf bank_mask:0xf bound_ctrl:1
	v_add_f32_dpp v83, v151, v151 wave_shr:1 row_mask:0xf bank_mask:0xf bound_ctrl:1
	v_add_f32_dpp v84, v142, v142 wave_shr:1 row_mask:0xf bank_mask:0xf bound_ctrl:1
	v_add_f32_dpp v85, v143, v143 wave_shr:1 row_mask:0xf bank_mask:0xf bound_ctrl:1
	v_add_f32_dpp v86, v152, v152 wave_shr:1 row_mask:0xf bank_mask:0xf bound_ctrl:1
	v_add_f32_dpp v87, v153, v153 wave_shr:1 row_mask:0xf bank_mask:0xf bound_ctrl:1
	v_add_f32_dpp v88, v154, v154 wave_shr:1 row_mask:0xf bank_mask:0xf bound_ctrl:1
	v_add_f32_dpp v89, v155, v155 wave_shr:1 row_mask:0xf bank_mask:0xf bound_ctrl:1
	v_add_f32_dpp v92, v156, v156 wave_shr:1 row_mask:0xf bank_mask:0xf bound_ctrl:1
	v_add_f32_dpp v93, v157, v157 wave_shr:1 row_mask:0xf bank_mask:0xf bound_ctrl:1
	v_add_f32_dpp v46, v90, v46 wave_shl:1 row_mask:0xf bank_mask:0xf bound_ctrl:1
	v_add_f32_dpp v47, v91, v47 wave_shl:1 row_mask:0xf bank_mask:0xf bound_ctrl:1
	v_add_f32_dpp v78, v148, v78 wave_shl:1 row_mask:0xf bank_mask:0xf bound_ctrl:1
	v_add_f32_dpp v79, v149, v79 wave_shl:1 row_mask:0xf bank_mask:0xf bound_ctrl:1
	v_add_f32_dpp v80, v102, v80 wave_shl:1 row_mask:0xf bank_mask:0xf bound_ctrl:1
	v_add_f32_dpp v81, v103, v81 wave_shl:1 row_mask:0xf bank_mask:0xf bound_ctrl:1
	v_add_f32_dpp v82, v150, v82 wave_shl:1 row_mask:0xf bank_mask:0xf bound_ctrl:1
	v_add_f32_dpp v83, v151, v83 wave_shl:1 row_mask:0xf bank_mask:0xf bound_ctrl:1
	v_add_f32_dpp v84, v142, v84 wave_shl:1 row_mask:0xf bank_mask:0xf bound_ctrl:1
	v_add_f32_dpp v85, v143, v85 wave_shl:1 row_mask:0xf bank_mask:0xf bound_ctrl:1
	v_add_f32_dpp v86, v152, v86 wave_shl:1 row_mask:0xf bank_mask:0xf bound_ctrl:1
	v_add_f32_dpp v87, v153, v87 wave_shl:1 row_mask:0xf bank_mask:0xf bound_ctrl:1
	v_add_f32_dpp v88, v154, v88 wave_shl:1 row_mask:0xf bank_mask:0xf bound_ctrl:1
	v_add_f32_dpp v89, v155, v89 wave_shl:1 row_mask:0xf bank_mask:0xf bound_ctrl:1
	v_add_f32_dpp v92, v156, v92 wave_shl:1 row_mask:0xf bank_mask:0xf bound_ctrl:1
	v_add_f32_dpp v93, v157, v93 wave_shl:1 row_mask:0xf bank_mask:0xf bound_ctrl:1
	v_pk_add_f32 v[90:91], v[124:125], v[46:47]
	v_pk_add_f32 v[102:103], v[58:59], v[78:79]
	v_pk_add_f32 v[58:59], v[62:63], v[80:81]
	v_pk_add_f32 v[62:63], v[76:77], v[82:83]
	v_pk_add_f32 v[76:77], v[94:95], v[84:85]
	v_pk_add_f32 v[94:95], v[96:97], v[86:87]
	v_pk_add_f32 v[96:97], v[98:99], v[88:89]
	v_pk_add_f32 v[98:99], v[100:101], v[92:93]
	v_pk_fma_f32 v[96:97], v[8:9], v[90:91], v[96:97] op_sel_hi:[0,1,1]
	v_pk_fma_f32 v[98:99], v[8:9], v[102:103], v[98:99] op_sel_hi:[0,1,1]
	v_pk_fma_f32 v[96:97], v[8:9], v[58:59], v[96:97] op_sel:[1,0,0]
	v_pk_fma_f32 v[98:99], v[8:9], v[62:63], v[98:99] op_sel:[1,0,0]
	v_pk_fma_f32 v[96:97], v[10:11], v[76:77], v[96:97] op_sel_hi:[0,1,1]
	v_pk_fma_f32 v[98:99], v[10:11], v[94:95], v[98:99] op_sel_hi:[0,1,1]
	v_cndmask_b32_e64 v100, 0, v1, s[10:11]
	v_cndmask_b32_e64 v101, 0, v1, s[14:15]
	v_cndmask_b32_e64 v124, 0, v1, s[20:21]
	v_cndmask_b32_e64 v125, 0, v1, s[22:23]
	v_pk_fma_f32 v[96:97], v[2:3], v[146:147], v[96:97] op_sel_hi:[1,0,1] neg_lo:[0,0,1] neg_hi:[0,0,1]
	v_pk_fma_f32 v[98:99], v[4:5], v[146:147], v[98:99] op_sel_hi:[1,0,1] neg_lo:[0,0,1] neg_hi:[0,0,1]
	s_add_i32 s4, s34, 3
	s_cmpk_lt_i32 s4, 0x201
	s_cselect_b64 s[12:13], s[0:1], 0
	v_pk_add_f32 v[96:97], v[96:97], v[100:101] neg_lo:[0,1] neg_hi:[0,1]
	v_pk_add_f32 v[98:99], v[98:99], v[124:125] neg_lo:[0,1] neg_hi:[0,1]
	v_pk_mul_f32 v[142:143], v[96:97], v[96:97]
	v_pk_fma_f32 v[142:143], v[98:99], v[98:99], v[142:143]
	v_add_f32_e32 v142, v142, v143
	v_cndmask_b32_e64 v143, 0, v142, s[12:13]
	v_add_f32_e32 v0, v0, v143
	s_add_i32 s4, s34, 8
	s_min_i32 s4, s4, 0x200
	s_mul_i32 s5, s4, 0x804
	s_add_i32 s5, s5, s35
	s_add_i32 s6, s5, 0x101004
	s_add_i32 s7, s5, 0x202008
	s_add_i32 s8, s5, 0x30300c
	s_mul_i32 s9, s4, 0x180c
	s_add_i32 s9, s9, s33
	buffer_load_dword v2, v28, s[16:19], s5 offen nt
	buffer_load_dword v3, v28, s[16:19], s6 offen nt
	buffer_load_dword v4, v28, s[16:19], s7 offen nt
	buffer_load_dword v5, v28, s[16:19], s8 offen nt
	buffer_load_dwordx3 v[8:10], v27, s[24:27], s9 offen nt
	s_waitcnt vmcnt(10)
	v_pk_mul_f32 v[52:53], v[20:21], v[40:41] op_sel_hi:[1,0]
	v_pk_mul_f32 v[54:55], v[24:25], v[40:41] op_sel_hi:[1,0]
	v_pk_mul_f32 v[58:59], v[20:21], v[40:41] op_sel:[0,1]
	v_pk_mul_f32 v[62:63], v[24:25], v[40:41] op_sel:[0,1]
	v_pk_mul_f32 v[64:65], v[20:21], v[42:43] op_sel_hi:[1,0]
	v_pk_mul_f32 v[66:67], v[24:25], v[42:43] op_sel_hi:[1,0]
	v_add_f32_dpp v76, v20, v20 wave_shr:1 row_mask:0xf bank_mask:0xf bound_ctrl:1
	v_add_f32_dpp v77, v21, v21 wave_shr:1 row_mask:0xf bank_mask:0xf bound_ctrl:1
	v_add_f32_dpp v90, v24, v24 wave_shr:1 row_mask:0xf bank_mask:0xf bound_ctrl:1
	v_add_f32_dpp v91, v25, v25 wave_shr:1 row_mask:0xf bank_mask:0xf bound_ctrl:1
	v_add_f32_dpp v94, v52, v52 wave_shr:1 row_mask:0xf bank_mask:0xf bound_ctrl:1
	v_add_f32_dpp v95, v53, v53 wave_shr:1 row_mask:0xf bank_mask:0xf bound_ctrl:1
	v_add_f32_dpp v96, v54, v54 wave_shr:1 row_mask:0xf bank_mask:0xf bound_ctrl:1
	v_add_f32_dpp v97, v55, v55 wave_shr:1 row_mask:0xf bank_mask:0xf bound_ctrl:1
	v_add_f32_dpp v98, v58, v58 wave_shr:1 row_mask:0xf bank_mask:0xf bound_ctrl:1
	v_add_f32_dpp v99, v59, v59 wave_shr:1 row_mask:0xf bank_mask:0xf bound_ctrl:1
	v_add_f32_dpp v100, v62, v62 wave_shr:1 row_mask:0xf bank_mask:0xf bound_ctrl:1
	v_add_f32_dpp v101, v63, v63 wave_shr:1 row_mask:0xf bank_mask:0xf bound_ctrl:1
	v_add_f32_dpp v102, v64, v64 wave_shr:1 row_mask:0xf bank_mask:0xf bound_ctrl:1
	v_add_f32_dpp v103, v65, v65 wave_shr:1 row_mask:0xf bank_mask:0xf bound_ctrl:1
	v_add_f32_dpp v124, v66, v66 wave_shr:1 row_mask:0xf bank_mask:0xf bound_ctrl:1
	v_add_f32_dpp v125, v67, v67 wave_shr:1 row_mask:0xf bank_mask:0xf bound_ctrl:1
	v_add_f32_dpp v76, v20, v76 wave_shl:1 row_mask:0xf bank_mask:0xf bound_ctrl:1
	v_add_f32_dpp v77, v21, v77 wave_shl:1 row_mask:0xf bank_mask:0xf bound_ctrl:1
	v_add_f32_dpp v90, v24, v90 wave_shl:1 row_mask:0xf bank_mask:0xf bound_ctrl:1
	v_add_f32_dpp v91, v25, v91 wave_shl:1 row_mask:0xf bank_mask:0xf bound_ctrl:1
	v_add_f32_dpp v94, v52, v94 wave_shl:1 row_mask:0xf bank_mask:0xf bound_ctrl:1
	v_add_f32_dpp v95, v53, v95 wave_shl:1 row_mask:0xf bank_mask:0xf bound_ctrl:1
	v_add_f32_dpp v96, v54, v96 wave_shl:1 row_mask:0xf bank_mask:0xf bound_ctrl:1
	v_add_f32_dpp v97, v55, v97 wave_shl:1 row_mask:0xf bank_mask:0xf bound_ctrl:1
	v_add_f32_dpp v98, v58, v98 wave_shl:1 row_mask:0xf bank_mask:0xf bound_ctrl:1
	v_add_f32_dpp v99, v59, v99 wave_shl:1 row_mask:0xf bank_mask:0xf bound_ctrl:1
	v_add_f32_dpp v100, v62, v100 wave_shl:1 row_mask:0xf bank_mask:0xf bound_ctrl:1
	v_add_f32_dpp v101, v63, v101 wave_shl:1 row_mask:0xf bank_mask:0xf bound_ctrl:1
	v_add_f32_dpp v102, v64, v102 wave_shl:1 row_mask:0xf bank_mask:0xf bound_ctrl:1
	v_add_f32_dpp v103, v65, v103 wave_shl:1 row_mask:0xf bank_mask:0xf bound_ctrl:1
	v_add_f32_dpp v124, v66, v124 wave_shl:1 row_mask:0xf bank_mask:0xf bound_ctrl:1
	v_add_f32_dpp v125, v67, v125 wave_shl:1 row_mask:0xf bank_mask:0xf bound_ctrl:1
	s_barrier
	ds_read_b128 v[52:55], v23 offset:0
	ds_read_b128 v[64:67], v23 offset:1024
	ds_read_b128 v[144:147], v23 offset:2048
	v_pk_add_f32 v[58:59], v[110:111], v[76:77]
	v_pk_add_f32 v[62:63], v[60:61], v[58:59]
	v_pk_add_f32 v[60:61], v[112:113], v[90:91]
	v_pk_add_f32 v[110:111], v[68:69], v[60:61]
	v_pk_add_f32 v[68:69], v[114:115], v[94:95]
	v_pk_add_f32 v[112:113], v[70:71], v[68:69]
	v_pk_add_f32 v[70:71], v[116:117], v[96:97]
	v_pk_add_f32 v[114:115], v[72:73], v[70:71]
	v_pk_add_f32 v[72:73], v[118:119], v[98:99]
	v_pk_add_f32 v[116:117], v[74:75], v[72:73]
	v_pk_add_f32 v[74:75], v[120:121], v[100:101]
	v_pk_add_f32 v[118:119], v[104:105], v[74:75]
	v_pk_add_f32 v[104:105], v[122:123], v[102:103]
	v_pk_add_f32 v[120:121], v[106:107], v[104:105]
	v_pk_add_f32 v[106:107], v[140:141], v[124:125]
	v_pk_add_f32 v[122:123], v[108:109], v[106:107]
	s_waitcnt lgkmcnt(2)
	v_pk_fma_f32 v[112:113], v[52:53], v[62:63], v[112:113] op_sel_hi:[0,1,1] neg_lo:[1,0,0] neg_hi:[1,0,0]
	v_pk_fma_f32 v[114:115], v[52:53], v[110:111], v[114:115] op_sel_hi:[0,1,1] neg_lo:[1,0,0] neg_hi:[1,0,0]
	v_pk_fma_f32 v[116:117], v[52:53], v[62:63], v[116:117] op_sel:[1,0,0] neg_lo:[1,0,0] neg_hi:[1,0,0]
	v_pk_fma_f32 v[118:119], v[52:53], v[110:111], v[118:119] op_sel:[1,0,0] neg_lo:[1,0,0] neg_hi:[1,0,0]
	v_pk_fma_f32 v[120:121], v[54:55], v[62:63], v[120:121] op_sel_hi:[0,1,1] neg_lo:[1,0,0] neg_hi:[1,0,0]
	v_pk_fma_f32 v[122:123], v[54:55], v[110:111], v[122:123] op_sel_hi:[0,1,1] neg_lo:[1,0,0] neg_hi:[1,0,0]
	v_pk_mul_f32 v[108:109], v[54:55], v[112:113] op_sel:[1,0]
	v_pk_mul_f32 v[148:149], v[54:55], v[114:115] op_sel:[1,0]
	s_waitcnt lgkmcnt(1)
	v_pk_mul_f32 v[140:141], v[64:65], v[112:113] op_sel_hi:[0,1]
	v_pk_mul_f32 v[150:151], v[64:65], v[114:115] op_sel_hi:[0,1]
	v_pk_mul_f32 v[142:143], v[64:65], v[112:113] op_sel:[1,0]
	v_pk_mul_f32 v[152:153], v[64:65], v[114:115] op_sel:[1,0]
	v_pk_fma_f32 v[108:109], v[64:65], v[116:117], v[108:109] op_sel_hi:[0,1,1]
	v_pk_fma_f32 v[148:149], v[64:65], v[118:119], v[148:149] op_sel_hi:[0,1,1]
	v_pk_fma_f32 v[140:141], v[66:67], v[116:117], v[140:141] op_sel_hi:[0,1,1]
	v_pk_fma_f32 v[150:151], v[66:67], v[118:119], v[150:151] op_sel_hi:[0,1,1]
	v_pk_fma_f32 v[142:143], v[66:67], v[116:117], v[142:143] op_sel:[1,0,0]
	v_pk_fma_f32 v[152:153], v[66:67], v[118:119], v[152:153] op_sel:[1,0,0]
	v_pk_fma_f32 v[108:109], v[64:65], v[120:121], v[108:109] op_sel:[1,0,0]
	v_pk_fma_f32 v[148:149], v[64:65], v[122:123], v[148:149] op_sel:[1,0,0]
	v_pk_fma_f32 v[140:141], v[66:67], v[120:121], v[140:141] op_sel:[1,0,0]
	v_pk_fma_f32 v[150:151], v[66:67], v[122:123], v[150:151] op_sel:[1,0,0]
	s_waitcnt lgkmcnt(0)
	v_pk_fma_f32 v[142:143], v[144:145], v[120:121], v[142:143] op_sel_hi:[0,1,1]
	v_pk_fma_f32 v[152:153], v[144:145], v[122:123], v[152:153] op_sel_hi:[0,1,1]
	v_pk_mul_f32 v[154:155], v[52:53], v[108:109] op_sel_hi:[0,1]
	v_pk_mul_f32 v[156:157], v[52:53], v[148:149] op_sel_hi:[0,1]
	v_pk_fma_f32 v[154:155], v[52:53], v[140:141], v[154:155] op_sel:[1,0,0]
	v_pk_fma_f32 v[156:157], v[52:53], v[150:151], v[156:157] op_sel:[1,0,0]
	v_pk_fma_f32 v[154:155], v[54:55], v[142:143], v[154:155] op_sel_hi:[0,1,1]
	v_pk_fma_f32 v[156:157], v[54:55], v[152:153], v[156:157] op_sel_hi:[0,1,1]
	v_pk_fma_f32 v[154:155], v[144:145], v[62:63], v[154:155] op_sel:[1,0,0] neg_lo:[0,0,1] neg_hi:[0,0,1]
	v_pk_fma_f32 v[156:157], v[144:145], v[110:111], v[156:157] op_sel:[1,0,0] neg_lo:[0,0,1] neg_hi:[0,0,1]
	v_cmp_eq_u32_e64 s[10:11], 1, v147
	v_cmp_eq_u32_e64 s[14:15], 2, v147
	v_cmp_eq_u32_e64 s[20:21], 3, v147
	v_cmp_eq_u32_e64 s[22:23], 4, v147
	v_add_f32_dpp v62, v108, v108 wave_shr:1 row_mask:0xf bank_mask:0xf bound_ctrl:1
	v_add_f32_dpp v63, v109, v109 wave_shr:1 row_mask:0xf bank_mask:0xf bound_ctrl:1
	v_add_f32_dpp v110, v148, v148 wave_shr:1 row_mask:0xf bank_mask:0xf bound_ctrl:1
	v_add_f32_dpp v111, v149, v149 wave_shr:1 row_mask:0xf bank_mask:0xf bound_ctrl:1
	v_add_f32_dpp v112, v140, v140 wave_shr:1 row_mask:0xf bank_mask:0xf bound_ctrl:1
	v_add_f32_dpp v113, v141, v141 wave_shr:1 row_mask:0xf bank_mask:0xf bound_ctrl:1
	v_add_f32_dpp v114, v150, v150 wave_shr:1 row_mask:0xf bank_mask:0xf bound_ctrl:1
	v_add_f32_dpp v115, v151, v151 wave_shr:1 row_mask:0xf bank_mask:0xf bound_ctrl:1
	v_add_f32_dpp v116, v142, v142 wave_shr:1 row_mask:0xf bank_mask:0xf bound_ctrl:1
	v_add_f32_dpp v117, v143, v143 wave_shr:1 row_mask:0xf bank_mask:0xf bound_ctrl:1
	v_add_f32_dpp v118, v152, v152 wave_shr:1 row_mask:0xf bank_mask:0xf bound_ctrl:1
	v_add_f32_dpp v119, v153, v153 wave_shr:1 row_mask:0xf bank_mask:0xf bound_ctrl:1
	v_add_f32_dpp v120, v154, v154 wave_shr:1 row_mask:0xf bank_mask:0xf bound_ctrl:1
	v_add_f32_dpp v121, v155, v155 wave_shr:1 row_mask:0xf bank_mask:0xf bound_ctrl:1
	v_add_f32_dpp v122, v156, v156 wave_shr:1 row_mask:0xf bank_mask:0xf bound_ctrl:1
	v_add_f32_dpp v123, v157, v157 wave_shr:1 row_mask:0xf bank_mask:0xf bound_ctrl:1
	v_add_f32_dpp v62, v108, v62 wave_shl:1 row_mask:0xf bank_mask:0xf bound_ctrl:1
	v_add_f32_dpp v63, v109, v63 wave_shl:1 row_mask:0xf bank_mask:0xf bound_ctrl:1
	v_add_f32_dpp v110, v148, v110 wave_shl:1 row_mask:0xf bank_mask:0xf bound_ctrl:1
	v_add_f32_dpp v111, v149, v111 wave_shl:1 row_mask:0xf bank_mask:0xf bound_ctrl:1
	v_add_f32_dpp v112, v140, v112 wave_shl:1 row_mask:0xf bank_mask:0xf bound_ctrl:1
	v_add_f32_dpp v113, v141, v113 wave_shl:1 row_mask:0xf bank_mask:0xf bound_ctrl:1
	v_add_f32_dpp v114, v150, v114 wave_shl:1 row_mask:0xf bank_mask:0xf bound_ctrl:1
	v_add_f32_dpp v115, v151, v115 wave_shl:1 row_mask:0xf bank_mask:0xf bound_ctrl:1
	v_add_f32_dpp v116, v142, v116 wave_shl:1 row_mask:0xf bank_mask:0xf bound_ctrl:1
	v_add_f32_dpp v117, v143, v117 wave_shl:1 row_mask:0xf bank_mask:0xf bound_ctrl:1
	v_add_f32_dpp v118, v152, v118 wave_shl:1 row_mask:0xf bank_mask:0xf bound_ctrl:1
	v_add_f32_dpp v119, v153, v119 wave_shl:1 row_mask:0xf bank_mask:0xf bound_ctrl:1
	v_add_f32_dpp v120, v154, v120 wave_shl:1 row_mask:0xf bank_mask:0xf bound_ctrl:1
	v_add_f32_dpp v121, v155, v121 wave_shl:1 row_mask:0xf bank_mask:0xf bound_ctrl:1
	v_add_f32_dpp v122, v156, v122 wave_shl:1 row_mask:0xf bank_mask:0xf bound_ctrl:1
	v_add_f32_dpp v123, v157, v123 wave_shl:1 row_mask:0xf bank_mask:0xf bound_ctrl:1
	v_pk_add_f32 v[108:109], v[46:47], v[62:63]
	v_pk_add_f32 v[140:141], v[56:57], v[108:109]
	v_pk_add_f32 v[46:47], v[78:79], v[110:111]
	v_pk_add_f32 v[56:57], v[126:127], v[46:47]
	v_pk_add_f32 v[78:79], v[80:81], v[112:113]
	v_pk_add_f32 v[126:127], v[128:129], v[78:79]
	v_pk_add_f32 v[80:81], v[82:83], v[114:115]
	v_pk_add_f32 v[128:129], v[130:131], v[80:81]
	v_pk_add_f32 v[82:83], v[84:85], v[116:117]
	v_pk_add_f32 v[130:131], v[132:133], v[82:83]
	v_pk_add_f32 v[84:85], v[86:87], v[118:119]
	v_pk_add_f32 v[132:133], v[134:135], v[84:85]
	v_pk_add_f32 v[86:87], v[88:89], v[120:121]
	v_pk_add_f32 v[134:135], v[136:137], v[86:87]
	v_pk_add_f32 v[88:89], v[92:93], v[122:123]
	v_pk_add_f32 v[136:137], v[138:139], v[88:89]
	v_pk_fma_f32 v[134:135], v[32:33], v[140:141], v[134:135] op_sel_hi:[0,1,1]
	v_pk_fma_f32 v[136:137], v[32:33], v[56:57], v[136:137] op_sel_hi:[0,1,1]
	v_pk_fma_f32 v[134:135], v[32:33], v[126:127], v[134:135] op_sel:[1,0,0]
	v_pk_fma_f32 v[136:137], v[32:33], v[128:129], v[136:137] op_sel:[1,0,0]
	v_pk_fma_f32 v[134:135], v[34:35], v[130:131], v[134:135] op_sel_hi:[0,1,1]
	v_pk_fma_f32 v[136:137], v[34:35], v[132:133], v[136:137] op_sel_hi:[0,1,1]
	v_cndmask_b32_e64 v92, 0, v1, s[10:11]
	v_cndmask_b32_e64 v93, 0, v1, s[14:15]
	v_cndmask_b32_e64 v138, 0, v1, s[20:21]
	v_cndmask_b32_e64 v139, 0, v1, s[22:23]
	v_pk_fma_f32 v[134:135], v[6:7], v[146:147], v[134:135] op_sel_hi:[1,0,1] neg_lo:[0,0,1] neg_hi:[0,0,1]
	v_pk_fma_f32 v[136:137], v[12:13], v[146:147], v[136:137] op_sel_hi:[1,0,1] neg_lo:[0,0,1] neg_hi:[0,0,1]
	s_add_i32 s4, s34, 4
	s_cmpk_lt_i32 s4, 0x201
	s_cselect_b64 s[12:13], s[0:1], 0
	v_pk_add_f32 v[134:135], v[134:135], v[92:93] neg_lo:[0,1] neg_hi:[0,1]
	v_pk_add_f32 v[136:137], v[136:137], v[138:139] neg_lo:[0,1] neg_hi:[0,1]
	v_pk_mul_f32 v[142:143], v[134:135], v[134:135]
	v_pk_fma_f32 v[142:143], v[136:137], v[136:137], v[142:143]
	v_add_f32_e32 v142, v142, v143
	v_cndmask_b32_e64 v143, 0, v142, s[12:13]
	v_add_f32_e32 v0, v0, v143
	s_add_i32 s4, s34, 9
	s_min_i32 s4, s4, 0x200
	s_mul_i32 s5, s4, 0x804
	s_add_i32 s5, s5, s35
	s_add_i32 s6, s5, 0x101004
	s_add_i32 s7, s5, 0x202008
	s_add_i32 s8, s5, 0x30300c
	s_mul_i32 s9, s4, 0x180c
	s_add_i32 s9, s9, s33
	buffer_load_dword v6, v28, s[16:19], s5 offen nt
	buffer_load_dword v7, v28, s[16:19], s6 offen nt
	buffer_load_dword v12, v28, s[16:19], s7 offen nt
	buffer_load_dword v13, v28, s[16:19], s8 offen nt
	buffer_load_dwordx3 v[32:34], v27, s[24:27], s9 offen nt
	s_waitcnt vmcnt(10)
	v_pk_mul_f32 v[52:53], v[30:31], v[48:49] op_sel_hi:[1,0]
	v_pk_mul_f32 v[54:55], v[44:45], v[48:49] op_sel_hi:[1,0]
	v_pk_mul_f32 v[56:57], v[30:31], v[48:49] op_sel:[0,1]
	v_pk_mul_f32 v[64:65], v[44:45], v[48:49] op_sel:[0,1]
	v_pk_mul_f32 v[66:67], v[30:31], v[50:51] op_sel_hi:[1,0]
	v_pk_mul_f32 v[92:93], v[44:45], v[50:51] op_sel_hi:[1,0]
	v_add_f32_dpp v126, v30, v30 wave_shr:1 row_mask:0xf bank_mask:0xf bound_ctrl:1
	v_add_f32_dpp v127, v31, v31 wave_shr:1 row_mask:0xf bank_mask:0xf bound_ctrl:1
	v_add_f32_dpp v128, v44, v44 wave_shr:1 row_mask:0xf bank_mask:0xf bound_ctrl:1
	v_add_f32_dpp v129, v45, v45 wave_shr:1 row_mask:0xf bank_mask:0xf bound_ctrl:1
	v_add_f32_dpp v130, v52, v52 wave_shr:1 row_mask:0xf bank_mask:0xf bound_ctrl:1
	v_add_f32_dpp v131, v53, v53 wave_shr:1 row_mask:0xf bank_mask:0xf bound_ctrl:1
	v_add_f32_dpp v132, v54, v54 wave_shr:1 row_mask:0xf bank_mask:0xf bound_ctrl:1
	v_add_f32_dpp v133, v55, v55 wave_shr:1 row_mask:0xf bank_mask:0xf bound_ctrl:1
	v_add_f32_dpp v134, v56, v56 wave_shr:1 row_mask:0xf bank_mask:0xf bound_ctrl:1
	v_add_f32_dpp v135, v57, v57 wave_shr:1 row_mask:0xf bank_mask:0xf bound_ctrl:1
	v_add_f32_dpp v136, v64, v64 wave_shr:1 row_mask:0xf bank_mask:0xf bound_ctrl:1
	v_add_f32_dpp v137, v65, v65 wave_shr:1 row_mask:0xf bank_mask:0xf bound_ctrl:1
	v_add_f32_dpp v138, v66, v66 wave_shr:1 row_mask:0xf bank_mask:0xf bound_ctrl:1
	v_add_f32_dpp v139, v67, v67 wave_shr:1 row_mask:0xf bank_mask:0xf bound_ctrl:1
	v_add_f32_dpp v140, v92, v92 wave_shr:1 row_mask:0xf bank_mask:0xf bound_ctrl:1
	v_add_f32_dpp v141, v93, v93 wave_shr:1 row_mask:0xf bank_mask:0xf bound_ctrl:1
	v_add_f32_dpp v126, v30, v126 wave_shl:1 row_mask:0xf bank_mask:0xf bound_ctrl:1
	v_add_f32_dpp v127, v31, v127 wave_shl:1 row_mask:0xf bank_mask:0xf bound_ctrl:1
	v_add_f32_dpp v128, v44, v128 wave_shl:1 row_mask:0xf bank_mask:0xf bound_ctrl:1
	v_add_f32_dpp v129, v45, v129 wave_shl:1 row_mask:0xf bank_mask:0xf bound_ctrl:1
	v_add_f32_dpp v130, v52, v130 wave_shl:1 row_mask:0xf bank_mask:0xf bound_ctrl:1
	v_add_f32_dpp v131, v53, v131 wave_shl:1 row_mask:0xf bank_mask:0xf bound_ctrl:1
	v_add_f32_dpp v132, v54, v132 wave_shl:1 row_mask:0xf bank_mask:0xf bound_ctrl:1
	v_add_f32_dpp v133, v55, v133 wave_shl:1 row_mask:0xf bank_mask:0xf bound_ctrl:1
	v_add_f32_dpp v134, v56, v134 wave_shl:1 row_mask:0xf bank_mask:0xf bound_ctrl:1
	v_add_f32_dpp v135, v57, v135 wave_shl:1 row_mask:0xf bank_mask:0xf bound_ctrl:1
	v_add_f32_dpp v136, v64, v136 wave_shl:1 row_mask:0xf bank_mask:0xf bound_ctrl:1
	v_add_f32_dpp v137, v65, v137 wave_shl:1 row_mask:0xf bank_mask:0xf bound_ctrl:1
	v_add_f32_dpp v138, v66, v138 wave_shl:1 row_mask:0xf bank_mask:0xf bound_ctrl:1
	v_add_f32_dpp v139, v67, v139 wave_shl:1 row_mask:0xf bank_mask:0xf bound_ctrl:1
	v_add_f32_dpp v140, v92, v140 wave_shl:1 row_mask:0xf bank_mask:0xf bound_ctrl:1
	v_add_f32_dpp v141, v93, v141 wave_shl:1 row_mask:0xf bank_mask:0xf bound_ctrl:1
	s_barrier
	ds_read_b128 v[52:55], v23 offset:3072
	ds_read_b128 v[64:67], v23 offset:4096
	ds_read_b128 v[144:147], v23 offset:5120
	v_pk_add_f32 v[56:57], v[58:59], v[126:127]
	v_pk_add_f32 v[58:59], v[60:61], v[128:129]
	v_pk_add_f32 v[60:61], v[68:69], v[130:131]
	v_pk_add_f32 v[68:69], v[70:71], v[132:133]
	v_pk_add_f32 v[70:71], v[72:73], v[134:135]
	v_pk_add_f32 v[72:73], v[74:75], v[136:137]
	v_pk_add_f32 v[74:75], v[104:105], v[138:139]
	v_pk_add_f32 v[92:93], v[106:107], v[140:141]
	s_waitcnt lgkmcnt(2)
	v_pk_fma_f32 v[60:61], v[52:53], v[56:57], v[60:61] op_sel_hi:[0,1,1] neg_lo:[1,0,0] neg_hi:[1,0,0]
	v_pk_fma_f32 v[68:69], v[52:53], v[58:59], v[68:69] op_sel_hi:[0,1,1] neg_lo:[1,0,0] neg_hi:[1,0,0]
	v_pk_fma_f32 v[70:71], v[52:53], v[56:57], v[70:71] op_sel:[1,0,0] neg_lo:[1,0,0] neg_hi:[1,0,0]
	v_pk_fma_f32 v[72:73], v[52:53], v[58:59], v[72:73] op_sel:[1,0,0] neg_lo:[1,0,0] neg_hi:[1,0,0]
	v_pk_fma_f32 v[74:75], v[54:55], v[56:57], v[74:75] op_sel_hi:[0,1,1] neg_lo:[1,0,0] neg_hi:[1,0,0]
	v_pk_fma_f32 v[92:93], v[54:55], v[58:59], v[92:93] op_sel_hi:[0,1,1] neg_lo:[1,0,0] neg_hi:[1,0,0]
	v_pk_mul_f32 v[104:105], v[54:55], v[60:61] op_sel:[1,0]
	v_pk_mul_f32 v[148:149], v[54:55], v[68:69] op_sel:[1,0]
	s_waitcnt lgkmcnt(1)
	v_pk_mul_f32 v[106:107], v[64:65], v[60:61] op_sel_hi:[0,1]
	v_pk_mul_f32 v[150:151], v[64:65], v[68:69] op_sel_hi:[0,1]
	v_pk_mul_f32 v[142:143], v[64:65], v[60:61] op_sel:[1,0]
	v_pk_mul_f32 v[152:153], v[64:65], v[68:69] op_sel:[1,0]
	v_pk_fma_f32 v[104:105], v[64:65], v[70:71], v[104:105] op_sel_hi:[0,1,1]
	v_pk_fma_f32 v[148:149], v[64:65], v[72:73], v[148:149] op_sel_hi:[0,1,1]
	v_pk_fma_f32 v[106:107], v[66:67], v[70:71], v[106:107] op_sel_hi:[0,1,1]
	v_pk_fma_f32 v[150:151], v[66:67], v[72:73], v[150:151] op_sel_hi:[0,1,1]
	v_pk_fma_f32 v[142:143], v[66:67], v[70:71], v[142:143] op_sel:[1,0,0]
	v_pk_fma_f32 v[152:153], v[66:67], v[72:73], v[152:153] op_sel:[1,0,0]
	v_pk_fma_f32 v[104:105], v[64:65], v[74:75], v[104:105] op_sel:[1,0,0]
	v_pk_fma_f32 v[148:149], v[64:65], v[92:93], v[148:149] op_sel:[1,0,0]
	v_pk_fma_f32 v[106:107], v[66:67], v[74:75], v[106:107] op_sel:[1,0,0]
	v_pk_fma_f32 v[150:151], v[66:67], v[92:93], v[150:151] op_sel:[1,0,0]
	s_waitcnt lgkmcnt(0)
	v_pk_fma_f32 v[142:143], v[144:145], v[74:75], v[142:143] op_sel_hi:[0,1,1]
	v_pk_fma_f32 v[152:153], v[144:145], v[92:93], v[152:153] op_sel_hi:[0,1,1]
	v_pk_mul_f32 v[154:155], v[52:53], v[104:105] op_sel_hi:[0,1]
	v_pk_mul_f32 v[156:157], v[52:53], v[148:149] op_sel_hi:[0,1]
	v_pk_fma_f32 v[154:155], v[52:53], v[106:107], v[154:155] op_sel:[1,0,0]
	v_pk_fma_f32 v[156:157], v[52:53], v[150:151], v[156:157] op_sel:[1,0,0]
	v_pk_fma_f32 v[154:155], v[54:55], v[142:143], v[154:155] op_sel_hi:[0,1,1]
	v_pk_fma_f32 v[156:157], v[54:55], v[152:153], v[156:157] op_sel_hi:[0,1,1]
	v_pk_fma_f32 v[154:155], v[144:145], v[56:57], v[154:155] op_sel:[1,0,0] neg_lo:[0,0,1] neg_hi:[0,0,1]
	v_pk_fma_f32 v[156:157], v[144:145], v[58:59], v[156:157] op_sel:[1,0,0] neg_lo:[0,0,1] neg_hi:[0,0,1]
	v_cmp_eq_u32_e64 s[10:11], 1, v147
	v_cmp_eq_u32_e64 s[14:15], 2, v147
	v_cmp_eq_u32_e64 s[20:21], 3, v147
	v_cmp_eq_u32_e64 s[22:23], 4, v147
	v_add_f32_dpp v56, v104, v104 wave_shr:1 row_mask:0xf bank_mask:0xf bound_ctrl:1
	v_add_f32_dpp v57, v105, v105 wave_shr:1 row_mask:0xf bank_mask:0xf bound_ctrl:1
	v_add_f32_dpp v58, v148, v148 wave_shr:1 row_mask:0xf bank_mask:0xf bound_ctrl:1
	v_add_f32_dpp v59, v149, v149 wave_shr:1 row_mask:0xf bank_mask:0xf bound_ctrl:1
	v_add_f32_dpp v60, v106, v106 wave_shr:1 row_mask:0xf bank_mask:0xf bound_ctrl:1
	v_add_f32_dpp v61, v107, v107 wave_shr:1 row_mask:0xf bank_mask:0xf bound_ctrl:1
	v_add_f32_dpp v68, v150, v150 wave_shr:1 row_mask:0xf bank_mask:0xf bound_ctrl:1
	v_add_f32_dpp v69, v151, v151 wave_shr:1 row_mask:0xf bank_mask:0xf bound_ctrl:1
	v_add_f32_dpp v70, v142, v142 wave_shr:1 row_mask:0xf bank_mask:0xf bound_ctrl:1
	v_add_f32_dpp v71, v143, v143 wave_shr:1 row_mask:0xf bank_mask:0xf bound_ctrl:1
	v_add_f32_dpp v72, v152, v152 wave_shr:1 row_mask:0xf bank_mask:0xf bound_ctrl:1
	v_add_f32_dpp v73, v153, v153 wave_shr:1 row_mask:0xf bank_mask:0xf bound_ctrl:1
	v_add_f32_dpp v74, v154, v154 wave_shr:1 row_mask:0xf bank_mask:0xf bound_ctrl:1
	v_add_f32_dpp v75, v155, v155 wave_shr:1 row_mask:0xf bank_mask:0xf bound_ctrl:1
	v_add_f32_dpp v92, v156, v156 wave_shr:1 row_mask:0xf bank_mask:0xf bound_ctrl:1
	v_add_f32_dpp v93, v157, v157 wave_shr:1 row_mask:0xf bank_mask:0xf bound_ctrl:1
	v_add_f32_dpp v56, v104, v56 wave_shl:1 row_mask:0xf bank_mask:0xf bound_ctrl:1
	v_add_f32_dpp v57, v105, v57 wave_shl:1 row_mask:0xf bank_mask:0xf bound_ctrl:1
	v_add_f32_dpp v58, v148, v58 wave_shl:1 row_mask:0xf bank_mask:0xf bound_ctrl:1
	v_add_f32_dpp v59, v149, v59 wave_shl:1 row_mask:0xf bank_mask:0xf bound_ctrl:1
	v_add_f32_dpp v60, v106, v60 wave_shl:1 row_mask:0xf bank_mask:0xf bound_ctrl:1
	v_add_f32_dpp v61, v107, v61 wave_shl:1 row_mask:0xf bank_mask:0xf bound_ctrl:1
	v_add_f32_dpp v68, v150, v68 wave_shl:1 row_mask:0xf bank_mask:0xf bound_ctrl:1
	v_add_f32_dpp v69, v151, v69 wave_shl:1 row_mask:0xf bank_mask:0xf bound_ctrl:1
	v_add_f32_dpp v70, v142, v70 wave_shl:1 row_mask:0xf bank_mask:0xf bound_ctrl:1
	v_add_f32_dpp v71, v143, v71 wave_shl:1 row_mask:0xf bank_mask:0xf bound_ctrl:1
	v_add_f32_dpp v72, v152, v72 wave_shl:1 row_mask:0xf bank_mask:0xf bound_ctrl:1
	v_add_f32_dpp v73, v153, v73 wave_shl:1 row_mask:0xf bank_mask:0xf bound_ctrl:1
	v_add_f32_dpp v74, v154, v74 wave_shl:1 row_mask:0xf bank_mask:0xf bound_ctrl:1
	v_add_f32_dpp v75, v155, v75 wave_shl:1 row_mask:0xf bank_mask:0xf bound_ctrl:1
	v_add_f32_dpp v92, v156, v92 wave_shl:1 row_mask:0xf bank_mask:0xf bound_ctrl:1
	v_add_f32_dpp v93, v157, v93 wave_shl:1 row_mask:0xf bank_mask:0xf bound_ctrl:1
	v_pk_add_f32 v[104:105], v[108:109], v[56:57]
	v_pk_add_f32 v[106:107], v[46:47], v[58:59]
	v_pk_add_f32 v[46:47], v[78:79], v[60:61]
	v_pk_add_f32 v[78:79], v[80:81], v[68:69]
	v_pk_add_f32 v[80:81], v[82:83], v[70:71]
	v_pk_add_f32 v[82:83], v[84:85], v[72:73]
	v_pk_add_f32 v[84:85], v[86:87], v[74:75]
	v_pk_add_f32 v[86:87], v[88:89], v[92:93]
	v_pk_fma_f32 v[84:85], v[36:37], v[104:105], v[84:85] op_sel_hi:[0,1,1]
	v_pk_fma_f32 v[86:87], v[36:37], v[106:107], v[86:87] op_sel_hi:[0,1,1]
	v_pk_fma_f32 v[84:85], v[36:37], v[46:47], v[84:85] op_sel:[1,0,0]
	v_pk_fma_f32 v[86:87], v[36:37], v[78:79], v[86:87] op_sel:[1,0,0]
	v_pk_fma_f32 v[84:85], v[38:39], v[80:81], v[84:85] op_sel_hi:[0,1,1]
	v_pk_fma_f32 v[86:87], v[38:39], v[82:83], v[86:87] op_sel_hi:[0,1,1]
	v_cndmask_b32_e64 v88, 0, v1, s[10:11]
	v_cndmask_b32_e64 v89, 0, v1, s[14:15]
	v_cndmask_b32_e64 v108, 0, v1, s[20:21]
	v_cndmask_b32_e64 v109, 0, v1, s[22:23]
	v_pk_fma_f32 v[84:85], v[14:15], v[146:147], v[84:85] op_sel_hi:[1,0,1] neg_lo:[0,0,1] neg_hi:[0,0,1]
	v_pk_fma_f32 v[86:87], v[16:17], v[146:147], v[86:87] op_sel_hi:[1,0,1] neg_lo:[0,0,1] neg_hi:[0,0,1]
	s_add_i32 s4, s34, 5
	s_cmpk_lt_i32 s4, 0x201
	s_cselect_b64 s[12:13], s[0:1], 0
	v_pk_add_f32 v[84:85], v[84:85], v[88:89] neg_lo:[0,1] neg_hi:[0,1]
	v_pk_add_f32 v[86:87], v[86:87], v[108:109] neg_lo:[0,1] neg_hi:[0,1]
	v_pk_mul_f32 v[142:143], v[84:85], v[84:85]
	v_pk_fma_f32 v[142:143], v[86:87], v[86:87], v[142:143]
	v_add_f32_e32 v142, v142, v143
	v_cndmask_b32_e64 v143, 0, v142, s[12:13]
	v_add_f32_e32 v0, v0, v143
	s_add_i32 s4, s34, 10
	s_min_i32 s4, s4, 0x200
	s_mul_i32 s5, s4, 0x804
	s_add_i32 s5, s5, s35
	s_add_i32 s6, s5, 0x101004
	s_add_i32 s7, s5, 0x202008
	s_add_i32 s8, s5, 0x30300c
	s_mul_i32 s9, s4, 0x180c
	s_add_i32 s9, s9, s33
	buffer_load_dword v14, v28, s[16:19], s5 offen nt
	buffer_load_dword v15, v28, s[16:19], s6 offen nt
	buffer_load_dword v16, v28, s[16:19], s7 offen nt
	buffer_load_dword v17, v28, s[16:19], s8 offen nt
	buffer_load_dwordx3 v[36:38], v27, s[24:27], s9 offen nt
	s_waitcnt vmcnt(10)
	v_pk_mul_f32 v[46:47], v[2:3], v[8:9] op_sel_hi:[1,0]
	v_pk_mul_f32 v[52:53], v[4:5], v[8:9] op_sel_hi:[1,0]
	v_pk_mul_f32 v[54:55], v[2:3], v[8:9] op_sel:[0,1]
	v_pk_mul_f32 v[64:65], v[4:5], v[8:9] op_sel:[0,1]
	v_pk_mul_f32 v[66:67], v[2:3], v[10:11] op_sel_hi:[1,0]
	v_pk_mul_f32 v[78:79], v[4:5], v[10:11] op_sel_hi:[1,0]
	v_add_f32_dpp v80, v2, v2 wave_shr:1 row_mask:0xf bank_mask:0xf bound_ctrl:1
	v_add_f32_dpp v81, v3, v3 wave_shr:1 row_mask:0xf bank_mask:0xf bound_ctrl:1
	v_add_f32_dpp v82, v4, v4 wave_shr:1 row_mask:0xf bank_mask:0xf bound_ctrl:1
	v_add_f32_dpp v83, v5, v5 wave_shr:1 row_mask:0xf bank_mask:0xf bound_ctrl:1
	v_add_f32_dpp v84, v46, v46 wave_shr:1 row_mask:0xf bank_mask:0xf bound_ctrl:1
	v_add_f32_dpp v85, v47, v47 wave_shr:1 row_mask:0xf bank_mask:0xf bound_ctrl:1
	v_add_f32_dpp v86, v52, v52 wave_shr:1 row_mask:0xf bank_mask:0xf bound_ctrl:1
	v_add_f32_dpp v87, v53, v53 wave_shr:1 row_mask:0xf bank_mask:0xf bound_ctrl:1
	v_add_f32_dpp v88, v54, v54 wave_shr:1 row_mask:0xf bank_mask:0xf bound_ctrl:1
	v_add_f32_dpp v89, v55, v55 wave_shr:1 row_mask:0xf bank_mask:0xf bound_ctrl:1
	v_add_f32_dpp v104, v64, v64 wave_shr:1 row_mask:0xf bank_mask:0xf bound_ctrl:1
	v_add_f32_dpp v105, v65, v65 wave_shr:1 row_mask:0xf bank_mask:0xf bound_ctrl:1
	v_add_f32_dpp v106, v66, v66 wave_shr:1 row_mask:0xf bank_mask:0xf bound_ctrl:1
	v_add_f32_dpp v107, v67, v67 wave_shr:1 row_mask:0xf bank_mask:0xf bound_ctrl:1
	v_add_f32_dpp v108, v78, v78 wave_shr:1 row_mask:0xf bank_mask:0xf bound_ctrl:1
	v_add_f32_dpp v109, v79, v79 wave_shr:1 row_mask:0xf bank_mask:0xf bound_ctrl:1
	v_add_f32_dpp v80, v2, v80 wave_shl:1 row_mask:0xf bank_mask:0xf bound_ctrl:1
	v_add_f32_dpp v81, v3, v81 wave_shl:1 row_mask:0xf bank_mask:0xf bound_ctrl:1
	v_add_f32_dpp v82, v4, v82 wave_shl:1 row_mask:0xf bank_mask:0xf bound_ctrl:1
	v_add_f32_dpp v83, v5, v83 wave_shl:1 row_mask:0xf bank_mask:0xf bound_ctrl:1
	v_add_f32_dpp v84, v46, v84 wave_shl:1 row_mask:0xf bank_mask:0xf bound_ctrl:1
	v_add_f32_dpp v85, v47, v85 wave_shl:1 row_mask:0xf bank_mask:0xf bound_ctrl:1
	v_add_f32_dpp v86, v52, v86 wave_shl:1 row_mask:0xf bank_mask:0xf bound_ctrl:1
	v_add_f32_dpp v87, v53, v87 wave_shl:1 row_mask:0xf bank_mask:0xf bound_ctrl:1
	v_add_f32_dpp v88, v54, v88 wave_shl:1 row_mask:0xf bank_mask:0xf bound_ctrl:1
	v_add_f32_dpp v89, v55, v89 wave_shl:1 row_mask:0xf bank_mask:0xf bound_ctrl:1
	v_add_f32_dpp v104, v64, v104 wave_shl:1 row_mask:0xf bank_mask:0xf bound_ctrl:1
	v_add_f32_dpp v105, v65, v105 wave_shl:1 row_mask:0xf bank_mask:0xf bound_ctrl:1
	v_add_f32_dpp v106, v66, v106 wave_shl:1 row_mask:0xf bank_mask:0xf bound_ctrl:1
	v_add_f32_dpp v107, v67, v107 wave_shl:1 row_mask:0xf bank_mask:0xf bound_ctrl:1
	v_add_f32_dpp v108, v78, v108 wave_shl:1 row_mask:0xf bank_mask:0xf bound_ctrl:1
	v_add_f32_dpp v109, v79, v109 wave_shl:1 row_mask:0xf bank_mask:0xf bound_ctrl:1
	s_barrier
	ds_read_b128 v[52:55], v23 offset:0
	ds_read_b128 v[64:67], v23 offset:1024
	ds_read_b128 v[144:147], v23 offset:2048
	v_pk_add_f32 v[46:47], v[126:127], v[80:81]
	v_pk_add_f32 v[78:79], v[76:77], v[46:47]
	v_pk_add_f32 v[76:77], v[128:129], v[82:83]
	v_pk_add_f32 v[126:127], v[90:91], v[76:77]
	v_pk_add_f32 v[90:91], v[130:131], v[84:85]
	v_pk_add_f32 v[128:129], v[94:95], v[90:91]
	v_pk_add_f32 v[94:95], v[132:133], v[86:87]
	v_pk_add_f32 v[130:131], v[96:97], v[94:95]
	v_pk_add_f32 v[96:97], v[134:135], v[88:89]
	v_pk_add_f32 v[132:133], v[98:99], v[96:97]
	v_pk_add_f32 v[98:99], v[136:137], v[104:105]
	v_pk_add_f32 v[134:135], v[100:101], v[98:99]
	v_pk_add_f32 v[100:101], v[138:139], v[106:107]
	v_pk_add_f32 v[136:137], v[102:103], v[100:101]
	v_pk_add_f32 v[102:103], v[140:141], v[108:109]
	v_pk_add_f32 v[138:139], v[124:125], v[102:103]
	s_waitcnt lgkmcnt(2)
	v_pk_fma_f32 v[128:129], v[52:53], v[78:79], v[128:129] op_sel_hi:[0,1,1] neg_lo:[1,0,0] neg_hi:[1,0,0]
	v_pk_fma_f32 v[130:131], v[52:53], v[126:127], v[130:131] op_sel_hi:[0,1,1] neg_lo:[1,0,0] neg_hi:[1,0,0]
	v_pk_fma_f32 v[132:133], v[52:53], v[78:79], v[132:133] op_sel:[1,0,0] neg_lo:[1,0,0] neg_hi:[1,0,0]
	v_pk_fma_f32 v[134:135], v[52:53], v[126:127], v[134:135] op_sel:[1,0,0] neg_lo:[1,0,0] neg_hi:[1,0,0]
	v_pk_fma_f32 v[136:137], v[54:55], v[78:79], v[136:137] op_sel_hi:[0,1,1] neg_lo:[1,0,0] neg_hi:[1,0,0]
	v_pk_fma_f32 v[138:139], v[54:55], v[126:127], v[138:139] op_sel_hi:[0,1,1] neg_lo:[1,0,0] neg_hi:[1,0,0]
	v_pk_mul_f32 v[124:125], v[54:55], v[128:129] op_sel:[1,0]
	v_pk_mul_f32 v[148:149], v[54:55], v[130:131] op_sel:[1,0]
	s_waitcnt lgkmcnt(1)
	v_pk_mul_f32 v[140:141], v[64:65], v[128:129] op_sel_hi:[0,1]
	v_pk_mul_f32 v[150:151], v[64:65], v[130:131] op_sel_hi:[0,1]
	v_pk_mul_f32 v[142:143], v[64:65], v[128:129] op_sel:[1,0]
	v_pk_mul_f32 v[152:153], v[64:65], v[130:131] op_sel:[1,0]
	v_pk_fma_f32 v[124:125], v[64:65], v[132:133], v[124:125] op_sel_hi:[0,1,1]
	v_pk_fma_f32 v[148:149], v[64:65], v[134:135], v[148:149] op_sel_hi:[0,1,1]
	v_pk_fma_f32 v[140:141], v[66:67], v[132:133], v[140:141] op_sel_hi:[0,1,1]
	v_pk_fma_f32 v[150:151], v[66:67], v[134:135], v[150:151] op_sel_hi:[0,1,1]
	v_pk_fma_f32 v[142:143], v[66:67], v[132:133], v[142:143] op_sel:[1,0,0]
	v_pk_fma_f32 v[152:153], v[66:67], v[134:135], v[152:153] op_sel:[1,0,0]
	v_pk_fma_f32 v[124:125], v[64:65], v[136:137], v[124:125] op_sel:[1,0,0]
	v_pk_fma_f32 v[148:149], v[64:65], v[138:139], v[148:149] op_sel:[1,0,0]
	v_pk_fma_f32 v[140:141], v[66:67], v[136:137], v[140:141] op_sel:[1,0,0]
	v_pk_fma_f32 v[150:151], v[66:67], v[138:139], v[150:151] op_sel:[1,0,0]
	s_waitcnt lgkmcnt(0)
	v_pk_fma_f32 v[142:143], v[144:145], v[136:137], v[142:143] op_sel_hi:[0,1,1]
	v_pk_fma_f32 v[152:153], v[144:145], v[138:139], v[152:153] op_sel_hi:[0,1,1]
	v_pk_mul_f32 v[154:155], v[52:53], v[124:125] op_sel_hi:[0,1]
	v_pk_mul_f32 v[156:157], v[52:53], v[148:149] op_sel_hi:[0,1]
	v_pk_fma_f32 v[154:155], v[52:53], v[140:141], v[154:155] op_sel:[1,0,0]
	v_pk_fma_f32 v[156:157], v[52:53], v[150:151], v[156:157] op_sel:[1,0,0]
	v_pk_fma_f32 v[154:155], v[54:55], v[142:143], v[154:155] op_sel_hi:[0,1,1]
	v_pk_fma_f32 v[156:157], v[54:55], v[152:153], v[156:157] op_sel_hi:[0,1,1]
	v_pk_fma_f32 v[154:155], v[144:145], v[78:79], v[154:155] op_sel:[1,0,0] neg_lo:[0,0,1] neg_hi:[0,0,1]
	v_pk_fma_f32 v[156:157], v[144:145], v[126:127], v[156:157] op_sel:[1,0,0] neg_lo:[0,0,1] neg_hi:[0,0,1]
	v_cmp_eq_u32_e64 s[10:11], 1, v147
	v_cmp_eq_u32_e64 s[14:15], 2, v147
	v_cmp_eq_u32_e64 s[20:21], 3, v147
	v_cmp_eq_u32_e64 s[22:23], 4, v147
	v_add_f32_dpp v78, v124, v124 wave_shr:1 row_mask:0xf bank_mask:0xf bound_ctrl:1
	v_add_f32_dpp v79, v125, v125 wave_shr:1 row_mask:0xf bank_mask:0xf bound_ctrl:1
	v_add_f32_dpp v126, v148, v148 wave_shr:1 row_mask:0xf bank_mask:0xf bound_ctrl:1
	v_add_f32_dpp v127, v149, v149 wave_shr:1 row_mask:0xf bank_mask:0xf bound_ctrl:1
	v_add_f32_dpp v128, v140, v140 wave_shr:1 row_mask:0xf bank_mask:0xf bound_ctrl:1
	v_add_f32_dpp v129, v141, v141 wave_shr:1 row_mask:0xf bank_mask:0xf bound_ctrl:1
	v_add_f32_dpp v130, v150, v150 wave_shr:1 row_mask:0xf bank_mask:0xf bound_ctrl:1
	v_add_f32_dpp v131, v151, v151 wave_shr:1 row_mask:0xf bank_mask:0xf bound_ctrl:1
	v_add_f32_dpp v132, v142, v142 wave_shr:1 row_mask:0xf bank_mask:0xf bound_ctrl:1
	v_add_f32_dpp v133, v143, v143 wave_shr:1 row_mask:0xf bank_mask:0xf bound_ctrl:1
	v_add_f32_dpp v134, v152, v152 wave_shr:1 row_mask:0xf bank_mask:0xf bound_ctrl:1
	v_add_f32_dpp v135, v153, v153 wave_shr:1 row_mask:0xf bank_mask:0xf bound_ctrl:1
	v_add_f32_dpp v136, v154, v154 wave_shr:1 row_mask:0xf bank_mask:0xf bound_ctrl:1
	v_add_f32_dpp v137, v155, v155 wave_shr:1 row_mask:0xf bank_mask:0xf bound_ctrl:1
	v_add_f32_dpp v138, v156, v156 wave_shr:1 row_mask:0xf bank_mask:0xf bound_ctrl:1
	v_add_f32_dpp v139, v157, v157 wave_shr:1 row_mask:0xf bank_mask:0xf bound_ctrl:1
	v_add_f32_dpp v78, v124, v78 wave_shl:1 row_mask:0xf bank_mask:0xf bound_ctrl:1
	v_add_f32_dpp v79, v125, v79 wave_shl:1 row_mask:0xf bank_mask:0xf bound_ctrl:1
	v_add_f32_dpp v126, v148, v126 wave_shl:1 row_mask:0xf bank_mask:0xf bound_ctrl:1
	v_add_f32_dpp v127, v149, v127 wave_shl:1 row_mask:0xf bank_mask:0xf bound_ctrl:1
	v_add_f32_dpp v128, v140, v128 wave_shl:1 row_mask:0xf bank_mask:0xf bound_ctrl:1
	v_add_f32_dpp v129, v141, v129 wave_shl:1 row_mask:0xf bank_mask:0xf bound_ctrl:1
	v_add_f32_dpp v130, v150, v130 wave_shl:1 row_mask:0xf bank_mask:0xf bound_ctrl:1
	v_add_f32_dpp v131, v151, v131 wave_shl:1 row_mask:0xf bank_mask:0xf bound_ctrl:1
	v_add_f32_dpp v132, v142, v132 wave_shl:1 row_mask:0xf bank_mask:0xf bound_ctrl:1
	v_add_f32_dpp v133, v143, v133 wave_shl:1 row_mask:0xf bank_mask:0xf bound_ctrl:1
	v_add_f32_dpp v134, v152, v134 wave_shl:1 row_mask:0xf bank_mask:0xf bound_ctrl:1
	v_add_f32_dpp v135, v153, v135 wave_shl:1 row_mask:0xf bank_mask:0xf bound_ctrl:1
	v_add_f32_dpp v136, v154, v136 wave_shl:1 row_mask:0xf bank_mask:0xf bound_ctrl:1
	v_add_f32_dpp v137, v155, v137 wave_shl:1 row_mask:0xf bank_mask:0xf bound_ctrl:1
	v_add_f32_dpp v138, v156, v138 wave_shl:1 row_mask:0xf bank_mask:0xf bound_ctrl:1
	v_add_f32_dpp v139, v157, v139 wave_shl:1 row_mask:0xf bank_mask:0xf bound_ctrl:1
	v_pk_add_f32 v[124:125], v[56:57], v[78:79]
	v_pk_add_f32 v[140:141], v[62:63], v[124:125]
	v_pk_add_f32 v[56:57], v[58:59], v[126:127]
	v_pk_add_f32 v[62:63], v[110:111], v[56:57]
	v_pk_add_f32 v[58:59], v[60:61], v[128:129]
	v_pk_add_f32 v[110:111], v[112:113], v[58:59]
	v_pk_add_f32 v[60:61], v[68:69], v[130:131]
	v_pk_add_f32 v[112:113], v[114:115], v[60:61]
	v_pk_add_f32 v[68:69], v[70:71], v[132:133]
	v_pk_add_f32 v[114:115], v[116:117], v[68:69]
	v_pk_add_f32 v[70:71], v[72:73], v[134:135]
	v_pk_add_f32 v[116:117], v[118:119], v[70:71]
	v_pk_add_f32 v[72:73], v[74:75], v[136:137]
	v_pk_add_f32 v[118:119], v[120:121], v[72:73]
	v_pk_add_f32 v[74:75], v[92:93], v[138:139]
	v_pk_add_f32 v[120:121], v[122:123], v[74:75]
	v_pk_fma_f32 v[118:119], v[40:41], v[140:141], v[118:119] op_sel_hi:[0,1,1]
	v_pk_fma_f32 v[120:121], v[40:41], v[62:63], v[120:121] op_sel_hi:[0,1,1]
	v_pk_fma_f32 v[118:119], v[40:41], v[110:111], v[118:119] op_sel:[1,0,0]
	v_pk_fma_f32 v[120:121], v[40:41], v[112:113], v[120:121] op_sel:[1,0,0]
	v_pk_fma_f32 v[118:119], v[42:43], v[114:115], v[118:119] op_sel_hi:[0,1,1]
	v_pk_fma_f32 v[120:121], v[42:43], v[116:117], v[120:121] op_sel_hi:[0,1,1]
	v_cndmask_b32_e64 v92, 0, v1, s[10:11]
	v_cndmask_b32_e64 v93, 0, v1, s[14:15]
	v_cndmask_b32_e64 v122, 0, v1, s[20:21]
	v_cndmask_b32_e64 v123, 0, v1, s[22:23]
	v_pk_fma_f32 v[118:119], v[20:21], v[146:147], v[118:119] op_sel_hi:[1,0,1] neg_lo:[0,0,1] neg_hi:[0,0,1]
	v_pk_fma_f32 v[120:121], v[24:25], v[146:147], v[120:121] op_sel_hi:[1,0,1] neg_lo:[0,0,1] neg_hi:[0,0,1]
	s_add_i32 s4, s34, 6
	s_cmpk_lt_i32 s4, 0x201
	s_cselect_b64 s[12:13], s[0:1], 0
	v_pk_add_f32 v[118:119], v[118:119], v[92:93] neg_lo:[0,1] neg_hi:[0,1]
	v_pk_add_f32 v[120:121], v[120:121], v[122:123] neg_lo:[0,1] neg_hi:[0,1]
	v_pk_mul_f32 v[142:143], v[118:119], v[118:119]
	v_pk_fma_f32 v[142:143], v[120:121], v[120:121], v[142:143]
	v_add_f32_e32 v142, v142, v143
	v_cndmask_b32_e64 v143, 0, v142, s[12:13]
	v_add_f32_e32 v0, v0, v143
	s_add_i32 s4, s34, 11
	s_min_i32 s4, s4, 0x200
	s_mul_i32 s5, s4, 0x804
	s_add_i32 s5, s5, s35
	s_add_i32 s6, s5, 0x101004
	s_add_i32 s7, s5, 0x202008
	s_add_i32 s8, s5, 0x30300c
	s_mul_i32 s9, s4, 0x180c
	s_add_i32 s9, s9, s33
	buffer_load_dword v20, v28, s[16:19], s5 offen nt
	buffer_load_dword v21, v28, s[16:19], s6 offen nt
	buffer_load_dword v24, v28, s[16:19], s7 offen nt
	buffer_load_dword v25, v28, s[16:19], s8 offen nt
	buffer_load_dwordx3 v[40:42], v27, s[24:27], s9 offen nt
	s_waitcnt vmcnt(10)
	v_pk_mul_f32 v[52:53], v[6:7], v[32:33] op_sel_hi:[1,0]
	v_pk_mul_f32 v[54:55], v[12:13], v[32:33] op_sel_hi:[1,0]
	v_pk_mul_f32 v[62:63], v[6:7], v[32:33] op_sel:[0,1]
	v_pk_mul_f32 v[64:65], v[12:13], v[32:33] op_sel:[0,1]
	v_pk_mul_f32 v[66:67], v[6:7], v[34:35] op_sel_hi:[1,0]
	v_pk_mul_f32 v[92:93], v[12:13], v[34:35] op_sel_hi:[1,0]
	v_add_f32_dpp v110, v6, v6 wave_shr:1 row_mask:0xf bank_mask:0xf bound_ctrl:1
	v_add_f32_dpp v111, v7, v7 wave_shr:1 row_mask:0xf bank_mask:0xf bound_ctrl:1
	v_add_f32_dpp v112, v12, v12 wave_shr:1 row_mask:0xf bank_mask:0xf bound_ctrl:1
	v_add_f32_dpp v113, v13, v13 wave_shr:1 row_mask:0xf bank_mask:0xf bound_ctrl:1
	v_add_f32_dpp v114, v52, v52 wave_shr:1 row_mask:0xf bank_mask:0xf bound_ctrl:1
	v_add_f32_dpp v115, v53, v53 wave_shr:1 row_mask:0xf bank_mask:0xf bound_ctrl:1
	v_add_f32_dpp v116, v54, v54 wave_shr:1 row_mask:0xf bank_mask:0xf bound_ctrl:1
	v_add_f32_dpp v117, v55, v55 wave_shr:1 row_mask:0xf bank_mask:0xf bound_ctrl:1
	v_add_f32_dpp v118, v62, v62 wave_shr:1 row_mask:0xf bank_mask:0xf bound_ctrl:1
	v_add_f32_dpp v119, v63, v63 wave_shr:1 row_mask:0xf bank_mask:0xf bound_ctrl:1
	v_add_f32_dpp v120, v64, v64 wave_shr:1 row_mask:0xf bank_mask:0xf bound_ctrl:1
	v_add_f32_dpp v121, v65, v65 wave_shr:1 row_mask:0xf bank_mask:0xf bound_ctrl:1
	v_add_f32_dpp v122, v66, v66 wave_shr:1 row_mask:0xf bank_mask:0xf bound_ctrl:1
	v_add_f32_dpp v123, v67, v67 wave_shr:1 row_mask:0xf bank_mask:0xf bound_ctrl:1
	v_add_f32_dpp v140, v92, v92 wave_shr:1 row_mask:0xf bank_mask:0xf bound_ctrl:1
	v_add_f32_dpp v141, v93, v93 wave_shr:1 row_mask:0xf bank_mask:0xf bound_ctrl:1
	v_add_f32_dpp v110, v6, v110 wave_shl:1 row_mask:0xf bank_mask:0xf bound_ctrl:1
	v_add_f32_dpp v111, v7, v111 wave_shl:1 row_mask:0xf bank_mask:0xf bound_ctrl:1
	v_add_f32_dpp v112, v12, v112 wave_shl:1 row_mask:0xf bank_mask:0xf bound_ctrl:1
	v_add_f32_dpp v113, v13, v113 wave_shl:1 row_mask:0xf bank_mask:0xf bound_ctrl:1
	v_add_f32_dpp v114, v52, v114 wave_shl:1 row_mask:0xf bank_mask:0xf bound_ctrl:1
	v_add_f32_dpp v115, v53, v115 wave_shl:1 row_mask:0xf bank_mask:0xf bound_ctrl:1
	v_add_f32_dpp v116, v54, v116 wave_shl:1 row_mask:0xf bank_mask:0xf bound_ctrl:1
	v_add_f32_dpp v117, v55, v117 wave_shl:1 row_mask:0xf bank_mask:0xf bound_ctrl:1
	v_add_f32_dpp v118, v62, v118 wave_shl:1 row_mask:0xf bank_mask:0xf bound_ctrl:1
	v_add_f32_dpp v119, v63, v119 wave_shl:1 row_mask:0xf bank_mask:0xf bound_ctrl:1
	v_add_f32_dpp v120, v64, v120 wave_shl:1 row_mask:0xf bank_mask:0xf bound_ctrl:1
	v_add_f32_dpp v121, v65, v121 wave_shl:1 row_mask:0xf bank_mask:0xf bound_ctrl:1
	v_add_f32_dpp v122, v66, v122 wave_shl:1 row_mask:0xf bank_mask:0xf bound_ctrl:1
	v_add_f32_dpp v123, v67, v123 wave_shl:1 row_mask:0xf bank_mask:0xf bound_ctrl:1
	v_add_f32_dpp v140, v92, v140 wave_shl:1 row_mask:0xf bank_mask:0xf bound_ctrl:1
	v_add_f32_dpp v141, v93, v141 wave_shl:1 row_mask:0xf bank_mask:0xf bound_ctrl:1
	s_barrier
	ds_read_b128 v[52:55], v23 offset:3072
	ds_read_b128 v[64:67], v23 offset:4096
	ds_read_b128 v[144:147], v23 offset:5120
	v_pk_add_f32 v[62:63], v[46:47], v[110:111]
	v_pk_add_f32 v[46:47], v[76:77], v[112:113]
	v_pk_add_f32 v[76:77], v[90:91], v[114:115]
	v_pk_add_f32 v[90:91], v[94:95], v[116:117]
	v_pk_add_f32 v[92:93], v[96:97], v[118:119]
	v_pk_add_f32 v[94:95], v[98:99], v[120:121]
	v_pk_add_f32 v[96:97], v[100:101], v[122:123]
	v_pk_add_f32 v[98:99], v[102:103], v[140:141]
	s_waitcnt lgkmcnt(2)
	v_pk_fma_f32 v[76:77], v[52:53], v[62:63], v[76:77] op_sel_hi:[0,1,1] neg_lo:[1,0,0] neg_hi:[1,0,0]
	v_pk_fma_f32 v[90:91], v[52:53], v[46:47], v[90:91] op_sel_hi:[0,1,1] neg_lo:[1,0,0] neg_hi:[1,0,0]
	v_pk_fma_f32 v[92:93], v[52:53], v[62:63], v[92:93] op_sel:[1,0,0] neg_lo:[1,0,0] neg_hi:[1,0,0]
	v_pk_fma_f32 v[94:95], v[52:53], v[46:47], v[94:95] op_sel:[1,0,0] neg_lo:[1,0,0] neg_hi:[1,0,0]
	v_pk_fma_f32 v[96:97], v[54:55], v[62:63], v[96:97] op_sel_hi:[0,1,1] neg_lo:[1,0,0] neg_hi:[1,0,0]
	v_pk_fma_f32 v[98:99], v[54:55], v[46:47], v[98:99] op_sel_hi:[0,1,1] neg_lo:[1,0,0] neg_hi:[1,0,0]
	v_pk_mul_f32 v[100:101], v[54:55], v[76:77] op_sel:[1,0]
	v_pk_mul_f32 v[148:149], v[54:55], v[90:91] op_sel:[1,0]
	s_waitcnt lgkmcnt(1)
	v_pk_mul_f32 v[102:103], v[64:65], v[76:77] op_sel_hi:[0,1]
	v_pk_mul_f32 v[150:151], v[64:65], v[90:91] op_sel_hi:[0,1]
	v_pk_mul_f32 v[142:143], v[64:65], v[76:77] op_sel:[1,0]
	v_pk_mul_f32 v[152:153], v[64:65], v[90:91] op_sel:[1,0]
	v_pk_fma_f32 v[100:101], v[64:65], v[92:93], v[100:101] op_sel_hi:[0,1,1]
	v_pk_fma_f32 v[148:149], v[64:65], v[94:95], v[148:149] op_sel_hi:[0,1,1]
	v_pk_fma_f32 v[102:103], v[66:67], v[92:93], v[102:103] op_sel_hi:[0,1,1]
	v_pk_fma_f32 v[150:151], v[66:67], v[94:95], v[150:151] op_sel_hi:[0,1,1]
	v_pk_fma_f32 v[142:143], v[66:67], v[92:93], v[142:143] op_sel:[1,0,0]
	v_pk_fma_f32 v[152:153], v[66:67], v[94:95], v[152:153] op_sel:[1,0,0]
	v_pk_fma_f32 v[100:101], v[64:65], v[96:97], v[100:101] op_sel:[1,0,0]
	v_pk_fma_f32 v[148:149], v[64:65], v[98:99], v[148:149] op_sel:[1,0,0]
	v_pk_fma_f32 v[102:103], v[66:67], v[96:97], v[102:103] op_sel:[1,0,0]
	v_pk_fma_f32 v[150:151], v[66:67], v[98:99], v[150:151] op_sel:[1,0,0]
	s_waitcnt lgkmcnt(0)
	v_pk_fma_f32 v[142:143], v[144:145], v[96:97], v[142:143] op_sel_hi:[0,1,1]
	v_pk_fma_f32 v[152:153], v[144:145], v[98:99], v[152:153] op_sel_hi:[0,1,1]
	v_pk_mul_f32 v[154:155], v[52:53], v[100:101] op_sel_hi:[0,1]
	v_pk_mul_f32 v[156:157], v[52:53], v[148:149] op_sel_hi:[0,1]
	v_pk_fma_f32 v[154:155], v[52:53], v[102:103], v[154:155] op_sel:[1,0,0]
	v_pk_fma_f32 v[156:157], v[52:53], v[150:151], v[156:157] op_sel:[1,0,0]
	v_pk_fma_f32 v[154:155], v[54:55], v[142:143], v[154:155] op_sel_hi:[0,1,1]
	v_pk_fma_f32 v[156:157], v[54:55], v[152:153], v[156:157] op_sel_hi:[0,1,1]
	v_pk_fma_f32 v[154:155], v[144:145], v[62:63], v[154:155] op_sel:[1,0,0] neg_lo:[0,0,1] neg_hi:[0,0,1]
	v_pk_fma_f32 v[156:157], v[144:145], v[46:47], v[156:157] op_sel:[1,0,0] neg_lo:[0,0,1] neg_hi:[0,0,1]
	v_cmp_eq_u32_e64 s[10:11], 1, v147
	v_cmp_eq_u32_e64 s[14:15], 2, v147
	v_cmp_eq_u32_e64 s[20:21], 3, v147
	v_cmp_eq_u32_e64 s[22:23], 4, v147
	v_add_f32_dpp v46, v100, v100 wave_shr:1 row_mask:0xf bank_mask:0xf bound_ctrl:1
	v_add_f32_dpp v47, v101, v101 wave_shr:1 row_mask:0xf bank_mask:0xf bound_ctrl:1
	v_add_f32_dpp v62, v148, v148 wave_shr:1 row_mask:0xf bank_mask:0xf bound_ctrl:1
	v_add_f32_dpp v63, v149, v149 wave_shr:1 row_mask:0xf bank_mask:0xf bound_ctrl:1
	v_add_f32_dpp v76, v102, v102 wave_shr:1 row_mask:0xf bank_mask:0xf bound_ctrl:1
	v_add_f32_dpp v77, v103, v103 wave_shr:1 row_mask:0xf bank_mask:0xf bound_ctrl:1
	v_add_f32_dpp v90, v150, v150 wave_shr:1 row_mask:0xf bank_mask:0xf bound_ctrl:1
	v_add_f32_dpp v91, v151, v151 wave_shr:1 row_mask:0xf bank_mask:0xf bound_ctrl:1
	v_add_f32_dpp v92, v142, v142 wave_shr:1 row_mask:0xf bank_mask:0xf bound_ctrl:1
	v_add_f32_dpp v93, v143, v143 wave_shr:1 row_mask:0xf bank_mask:0xf bound_ctrl:1
	v_add_f32_dpp v94, v152, v152 wave_shr:1 row_mask:0xf bank_mask:0xf bound_ctrl:1
	v_add_f32_dpp v95, v153, v153 wave_shr:1 row_mask:0xf bank_mask:0xf bound_ctrl:1
	v_add_f32_dpp v96, v154, v154 wave_shr:1 row_mask:0xf bank_mask:0xf bound_ctrl:1
	v_add_f32_dpp v97, v155, v155 wave_shr:1 row_mask:0xf bank_mask:0xf bound_ctrl:1
	v_add_f32_dpp v98, v156, v156 wave_shr:1 row_mask:0xf bank_mask:0xf bound_ctrl:1
	v_add_f32_dpp v99, v157, v157 wave_shr:1 row_mask:0xf bank_mask:0xf bound_ctrl:1
	v_add_f32_dpp v46, v100, v46 wave_shl:1 row_mask:0xf bank_mask:0xf bound_ctrl:1
	v_add_f32_dpp v47, v101, v47 wave_shl:1 row_mask:0xf bank_mask:0xf bound_ctrl:1
	v_add_f32_dpp v62, v148, v62 wave_shl:1 row_mask:0xf bank_mask:0xf bound_ctrl:1
	v_add_f32_dpp v63, v149, v63 wave_shl:1 row_mask:0xf bank_mask:0xf bound_ctrl:1
	v_add_f32_dpp v76, v102, v76 wave_shl:1 row_mask:0xf bank_mask:0xf bound_ctrl:1
	v_add_f32_dpp v77, v103, v77 wave_shl:1 row_mask:0xf bank_mask:0xf bound_ctrl:1
	v_add_f32_dpp v90, v150, v90 wave_shl:1 row_mask:0xf bank_mask:0xf bound_ctrl:1
	v_add_f32_dpp v91, v151, v91 wave_shl:1 row_mask:0xf bank_mask:0xf bound_ctrl:1
	v_add_f32_dpp v92, v142, v92 wave_shl:1 row_mask:0xf bank_mask:0xf bound_ctrl:1
	v_add_f32_dpp v93, v143, v93 wave_shl:1 row_mask:0xf bank_mask:0xf bound_ctrl:1
	v_add_f32_dpp v94, v152, v94 wave_shl:1 row_mask:0xf bank_mask:0xf bound_ctrl:1
	v_add_f32_dpp v95, v153, v95 wave_shl:1 row_mask:0xf bank_mask:0xf bound_ctrl:1
	v_add_f32_dpp v96, v154, v96 wave_shl:1 row_mask:0xf bank_mask:0xf bound_ctrl:1
	v_add_f32_dpp v97, v155, v97 wave_shl:1 row_mask:0xf bank_mask:0xf bound_ctrl:1
	v_add_f32_dpp v98, v156, v98 wave_shl:1 row_mask:0xf bank_mask:0xf bound_ctrl:1
	v_add_f32_dpp v99, v157, v99 wave_shl:1 row_mask:0xf bank_mask:0xf bound_ctrl:1
	v_pk_add_f32 v[100:101], v[124:125], v[46:47]
	v_pk_add_f32 v[102:103], v[56:57], v[62:63]
	v_pk_add_f32 v[56:57], v[58:59], v[76:77]
	v_pk_add_f32 v[58:59], v[60:61], v[90:91]
	v_pk_add_f32 v[60:61], v[68:69], v[92:93]
	v_pk_add_f32 v[68:69], v[70:71], v[94:95]
	v_pk_add_f32 v[70:71], v[72:73], v[96:97]
	v_pk_add_f32 v[72:73], v[74:75], v[98:99]
	v_pk_fma_f32 v[70:71], v[48:49], v[100:101], v[70:71] op_sel_hi:[0,1,1]
	v_pk_fma_f32 v[72:73], v[48:49], v[102:103], v[72:73] op_sel_hi:[0,1,1]
	v_pk_fma_f32 v[70:71], v[48:49], v[56:57], v[70:71] op_sel:[1,0,0]
	v_pk_fma_f32 v[72:73], v[48:49], v[58:59], v[72:73] op_sel:[1,0,0]
	v_pk_fma_f32 v[70:71], v[50:51], v[60:61], v[70:71] op_sel_hi:[0,1,1]
	v_pk_fma_f32 v[72:73], v[50:51], v[68:69], v[72:73] op_sel_hi:[0,1,1]
	v_cndmask_b32_e64 v74, 0, v1, s[10:11]
	v_cndmask_b32_e64 v75, 0, v1, s[14:15]
	v_cndmask_b32_e64 v124, 0, v1, s[20:21]
	v_cndmask_b32_e64 v125, 0, v1, s[22:23]
	v_pk_fma_f32 v[70:71], v[30:31], v[146:147], v[70:71] op_sel_hi:[1,0,1] neg_lo:[0,0,1] neg_hi:[0,0,1]
	v_pk_fma_f32 v[72:73], v[44:45], v[146:147], v[72:73] op_sel_hi:[1,0,1] neg_lo:[0,0,1] neg_hi:[0,0,1]
	s_add_i32 s4, s34, 7
	s_cmpk_lt_i32 s4, 0x201
	s_cselect_b64 s[12:13], s[0:1], 0
	v_pk_add_f32 v[70:71], v[70:71], v[74:75] neg_lo:[0,1] neg_hi:[0,1]
	v_pk_add_f32 v[72:73], v[72:73], v[124:125] neg_lo:[0,1] neg_hi:[0,1]
	v_pk_mul_f32 v[142:143], v[70:71], v[70:71]
	v_pk_fma_f32 v[142:143], v[72:73], v[72:73], v[142:143]
	v_add_f32_e32 v142, v142, v143
	v_cndmask_b32_e64 v143, 0, v142, s[12:13]
	v_add_f32_e32 v0, v0, v143
	s_waitcnt vmcnt(5)
	v_pk_mul_f32 v[30:31], v[14:15], v[36:37] op_sel_hi:[1,0]
	v_pk_mul_f32 v[44:45], v[16:17], v[36:37] op_sel_hi:[1,0]
	v_pk_mul_f32 v[48:49], v[14:15], v[36:37] op_sel:[0,1]
	v_pk_mul_f32 v[50:51], v[16:17], v[36:37] op_sel:[0,1]
	v_pk_mul_f32 v[52:53], v[14:15], v[38:39] op_sel_hi:[1,0]
	v_pk_mul_f32 v[54:55], v[16:17], v[38:39] op_sel_hi:[1,0]
	v_add_f32_dpp v56, v14, v14 wave_shr:1 row_mask:0xf bank_mask:0xf bound_ctrl:1
	v_add_f32_dpp v57, v15, v15 wave_shr:1 row_mask:0xf bank_mask:0xf bound_ctrl:1
	v_add_f32_dpp v58, v16, v16 wave_shr:1 row_mask:0xf bank_mask:0xf bound_ctrl:1
	v_add_f32_dpp v59, v17, v17 wave_shr:1 row_mask:0xf bank_mask:0xf bound_ctrl:1
	v_add_f32_dpp v60, v30, v30 wave_shr:1 row_mask:0xf bank_mask:0xf bound_ctrl:1
	v_add_f32_dpp v61, v31, v31 wave_shr:1 row_mask:0xf bank_mask:0xf bound_ctrl:1
	v_add_f32_dpp v64, v44, v44 wave_shr:1 row_mask:0xf bank_mask:0xf bound_ctrl:1
	v_add_f32_dpp v65, v45, v45 wave_shr:1 row_mask:0xf bank_mask:0xf bound_ctrl:1
	v_add_f32_dpp v66, v48, v48 wave_shr:1 row_mask:0xf bank_mask:0xf bound_ctrl:1
	v_add_f32_dpp v67, v49, v49 wave_shr:1 row_mask:0xf bank_mask:0xf bound_ctrl:1
	v_add_f32_dpp v68, v50, v50 wave_shr:1 row_mask:0xf bank_mask:0xf bound_ctrl:1
	v_add_f32_dpp v69, v51, v51 wave_shr:1 row_mask:0xf bank_mask:0xf bound_ctrl:1
	v_add_f32_dpp v70, v52, v52 wave_shr:1 row_mask:0xf bank_mask:0xf bound_ctrl:1
	v_add_f32_dpp v71, v53, v53 wave_shr:1 row_mask:0xf bank_mask:0xf bound_ctrl:1
	v_add_f32_dpp v72, v54, v54 wave_shr:1 row_mask:0xf bank_mask:0xf bound_ctrl:1
	v_add_f32_dpp v73, v55, v55 wave_shr:1 row_mask:0xf bank_mask:0xf bound_ctrl:1
	v_add_f32_dpp v56, v14, v56 wave_shl:1 row_mask:0xf bank_mask:0xf bound_ctrl:1
	v_add_f32_dpp v57, v15, v57 wave_shl:1 row_mask:0xf bank_mask:0xf bound_ctrl:1
	v_add_f32_dpp v58, v16, v58 wave_shl:1 row_mask:0xf bank_mask:0xf bound_ctrl:1
	v_add_f32_dpp v59, v17, v59 wave_shl:1 row_mask:0xf bank_mask:0xf bound_ctrl:1
	v_add_f32_dpp v60, v30, v60 wave_shl:1 row_mask:0xf bank_mask:0xf bound_ctrl:1
	v_add_f32_dpp v61, v31, v61 wave_shl:1 row_mask:0xf bank_mask:0xf bound_ctrl:1
	v_add_f32_dpp v64, v44, v64 wave_shl:1 row_mask:0xf bank_mask:0xf bound_ctrl:1
	v_add_f32_dpp v65, v45, v65 wave_shl:1 row_mask:0xf bank_mask:0xf bound_ctrl:1
	v_add_f32_dpp v66, v48, v66 wave_shl:1 row_mask:0xf bank_mask:0xf bound_ctrl:1
	v_add_f32_dpp v67, v49, v67 wave_shl:1 row_mask:0xf bank_mask:0xf bound_ctrl:1
	v_add_f32_dpp v68, v50, v68 wave_shl:1 row_mask:0xf bank_mask:0xf bound_ctrl:1
	v_add_f32_dpp v69, v51, v69 wave_shl:1 row_mask:0xf bank_mask:0xf bound_ctrl:1
	v_add_f32_dpp v70, v52, v70 wave_shl:1 row_mask:0xf bank_mask:0xf bound_ctrl:1
	v_add_f32_dpp v71, v53, v71 wave_shl:1 row_mask:0xf bank_mask:0xf bound_ctrl:1
	v_add_f32_dpp v72, v54, v72 wave_shl:1 row_mask:0xf bank_mask:0xf bound_ctrl:1
	v_add_f32_dpp v73, v55, v73 wave_shl:1 row_mask:0xf bank_mask:0xf bound_ctrl:1
	s_barrier
	ds_read_b128 v[48:51], v23 offset:0
	ds_read_b128 v[52:55], v23 offset:1024
	ds_read_b128 v[100:103], v23 offset:2048
	v_pk_add_f32 v[30:31], v[110:111], v[56:57]
	v_pk_add_f32 v[44:45], v[80:81], v[30:31]
	v_pk_add_f32 v[74:75], v[112:113], v[58:59]
	v_pk_add_f32 v[80:81], v[82:83], v[74:75]
	v_pk_add_f32 v[82:83], v[114:115], v[60:61]
	v_pk_add_f32 v[110:111], v[84:85], v[82:83]
	v_pk_add_f32 v[84:85], v[116:117], v[64:65]
	v_pk_add_f32 v[112:113], v[86:87], v[84:85]
	v_pk_add_f32 v[86:87], v[118:119], v[66:67]
	v_pk_add_f32 v[114:115], v[88:89], v[86:87]
	v_pk_add_f32 v[88:89], v[120:121], v[68:69]
	v_pk_add_f32 v[116:117], v[104:105], v[88:89]
	v_pk_add_f32 v[104:105], v[122:123], v[70:71]
	v_pk_add_f32 v[118:119], v[106:107], v[104:105]
	v_pk_add_f32 v[106:107], v[140:141], v[72:73]
	v_pk_add_f32 v[120:121], v[108:109], v[106:107]
	s_waitcnt lgkmcnt(2)
	v_pk_fma_f32 v[110:111], v[48:49], v[44:45], v[110:111] op_sel_hi:[0,1,1] neg_lo:[1,0,0] neg_hi:[1,0,0]
	v_pk_fma_f32 v[112:113], v[48:49], v[80:81], v[112:113] op_sel_hi:[0,1,1] neg_lo:[1,0,0] neg_hi:[1,0,0]
	v_pk_fma_f32 v[114:115], v[48:49], v[44:45], v[114:115] op_sel:[1,0,0] neg_lo:[1,0,0] neg_hi:[1,0,0]
	v_pk_fma_f32 v[116:117], v[48:49], v[80:81], v[116:117] op_sel:[1,0,0] neg_lo:[1,0,0] neg_hi:[1,0,0]
	v_pk_fma_f32 v[118:119], v[50:51], v[44:45], v[118:119] op_sel_hi:[0,1,1] neg_lo:[1,0,0] neg_hi:[1,0,0]
	v_pk_fma_f32 v[120:121], v[50:51], v[80:81], v[120:121] op_sel_hi:[0,1,1] neg_lo:[1,0,0] neg_hi:[1,0,0]
	v_pk_mul_f32 v[108:109], v[50:51], v[110:111] op_sel:[1,0]
	v_pk_mul_f32 v[140:141], v[50:51], v[112:113] op_sel:[1,0]
	s_waitcnt lgkmcnt(1)
	v_pk_mul_f32 v[122:123], v[52:53], v[110:111] op_sel_hi:[0,1]
	v_pk_mul_f32 v[142:143], v[52:53], v[112:113] op_sel_hi:[0,1]
	v_pk_mul_f32 v[124:125], v[52:53], v[110:111] op_sel:[1,0]
	v_pk_mul_f32 v[144:145], v[52:53], v[112:113] op_sel:[1,0]
	v_pk_fma_f32 v[108:109], v[52:53], v[114:115], v[108:109] op_sel_hi:[0,1,1]
	v_pk_fma_f32 v[140:141], v[52:53], v[116:117], v[140:141] op_sel_hi:[0,1,1]
	v_pk_fma_f32 v[122:123], v[54:55], v[114:115], v[122:123] op_sel_hi:[0,1,1]
	v_pk_fma_f32 v[142:143], v[54:55], v[116:117], v[142:143] op_sel_hi:[0,1,1]
	v_pk_fma_f32 v[124:125], v[54:55], v[114:115], v[124:125] op_sel:[1,0,0]
	v_pk_fma_f32 v[144:145], v[54:55], v[116:117], v[144:145] op_sel:[1,0,0]
	v_pk_fma_f32 v[108:109], v[52:53], v[118:119], v[108:109] op_sel:[1,0,0]
	v_pk_fma_f32 v[140:141], v[52:53], v[120:121], v[140:141] op_sel:[1,0,0]
	v_pk_fma_f32 v[122:123], v[54:55], v[118:119], v[122:123] op_sel:[1,0,0]
	v_pk_fma_f32 v[142:143], v[54:55], v[120:121], v[142:143] op_sel:[1,0,0]
	s_waitcnt lgkmcnt(0)
	v_pk_fma_f32 v[124:125], v[100:101], v[118:119], v[124:125] op_sel_hi:[0,1,1]
	v_pk_fma_f32 v[144:145], v[100:101], v[120:121], v[144:145] op_sel_hi:[0,1,1]
	v_pk_mul_f32 v[146:147], v[48:49], v[108:109] op_sel_hi:[0,1]
	v_pk_mul_f32 v[148:149], v[48:49], v[140:141] op_sel_hi:[0,1]
	v_pk_fma_f32 v[146:147], v[48:49], v[122:123], v[146:147] op_sel:[1,0,0]
	v_pk_fma_f32 v[148:149], v[48:49], v[142:143], v[148:149] op_sel:[1,0,0]
	v_pk_fma_f32 v[146:147], v[50:51], v[124:125], v[146:147] op_sel_hi:[0,1,1]
	v_pk_fma_f32 v[148:149], v[50:51], v[144:145], v[148:149] op_sel_hi:[0,1,1]
	v_pk_fma_f32 v[146:147], v[100:101], v[44:45], v[146:147] op_sel:[1,0,0] neg_lo:[0,0,1] neg_hi:[0,0,1]
	v_pk_fma_f32 v[148:149], v[100:101], v[80:81], v[148:149] op_sel:[1,0,0] neg_lo:[0,0,1] neg_hi:[0,0,1]
	v_cmp_eq_u32_e64 s[10:11], 1, v103
	v_cmp_eq_u32_e64 s[14:15], 2, v103
	v_cmp_eq_u32_e64 s[20:21], 3, v103
	v_cmp_eq_u32_e64 s[22:23], 4, v103
	v_add_f32_dpp v44, v108, v108 wave_shr:1 row_mask:0xf bank_mask:0xf bound_ctrl:1
	v_add_f32_dpp v45, v109, v109 wave_shr:1 row_mask:0xf bank_mask:0xf bound_ctrl:1
	v_add_f32_dpp v80, v140, v140 wave_shr:1 row_mask:0xf bank_mask:0xf bound_ctrl:1
	v_add_f32_dpp v81, v141, v141 wave_shr:1 row_mask:0xf bank_mask:0xf bound_ctrl:1
	v_add_f32_dpp v110, v122, v122 wave_shr:1 row_mask:0xf bank_mask:0xf bound_ctrl:1
	v_add_f32_dpp v111, v123, v123 wave_shr:1 row_mask:0xf bank_mask:0xf bound_ctrl:1
	v_add_f32_dpp v112, v142, v142 wave_shr:1 row_mask:0xf bank_mask:0xf bound_ctrl:1
	v_add_f32_dpp v113, v143, v143 wave_shr:1 row_mask:0xf bank_mask:0xf bound_ctrl:1
	v_add_f32_dpp v114, v124, v124 wave_shr:1 row_mask:0xf bank_mask:0xf bound_ctrl:1
	v_add_f32_dpp v115, v125, v125 wave_shr:1 row_mask:0xf bank_mask:0xf bound_ctrl:1
	v_add_f32_dpp v116, v144, v144 wave_shr:1 row_mask:0xf bank_mask:0xf bound_ctrl:1
	v_add_f32_dpp v117, v145, v145 wave_shr:1 row_mask:0xf bank_mask:0xf bound_ctrl:1
	v_add_f32_dpp v118, v146, v146 wave_shr:1 row_mask:0xf bank_mask:0xf bound_ctrl:1
	v_add_f32_dpp v119, v147, v147 wave_shr:1 row_mask:0xf bank_mask:0xf bound_ctrl:1
	v_add_f32_dpp v120, v148, v148 wave_shr:1 row_mask:0xf bank_mask:0xf bound_ctrl:1
	v_add_f32_dpp v121, v149, v149 wave_shr:1 row_mask:0xf bank_mask:0xf bound_ctrl:1
	v_add_f32_dpp v44, v108, v44 wave_shl:1 row_mask:0xf bank_mask:0xf bound_ctrl:1
	v_add_f32_dpp v45, v109, v45 wave_shl:1 row_mask:0xf bank_mask:0xf bound_ctrl:1
	v_add_f32_dpp v80, v140, v80 wave_shl:1 row_mask:0xf bank_mask:0xf bound_ctrl:1
	v_add_f32_dpp v81, v141, v81 wave_shl:1 row_mask:0xf bank_mask:0xf bound_ctrl:1
	v_add_f32_dpp v110, v122, v110 wave_shl:1 row_mask:0xf bank_mask:0xf bound_ctrl:1
	v_add_f32_dpp v111, v123, v111 wave_shl:1 row_mask:0xf bank_mask:0xf bound_ctrl:1
	v_add_f32_dpp v112, v142, v112 wave_shl:1 row_mask:0xf bank_mask:0xf bound_ctrl:1
	v_add_f32_dpp v113, v143, v113 wave_shl:1 row_mask:0xf bank_mask:0xf bound_ctrl:1
	v_add_f32_dpp v114, v124, v114 wave_shl:1 row_mask:0xf bank_mask:0xf bound_ctrl:1
	v_add_f32_dpp v115, v125, v115 wave_shl:1 row_mask:0xf bank_mask:0xf bound_ctrl:1
	v_add_f32_dpp v116, v144, v116 wave_shl:1 row_mask:0xf bank_mask:0xf bound_ctrl:1
	v_add_f32_dpp v117, v145, v117 wave_shl:1 row_mask:0xf bank_mask:0xf bound_ctrl:1
	v_add_f32_dpp v118, v146, v118 wave_shl:1 row_mask:0xf bank_mask:0xf bound_ctrl:1
	v_add_f32_dpp v119, v147, v119 wave_shl:1 row_mask:0xf bank_mask:0xf bound_ctrl:1
	v_add_f32_dpp v120, v148, v120 wave_shl:1 row_mask:0xf bank_mask:0xf bound_ctrl:1
	v_add_f32_dpp v121, v149, v121 wave_shl:1 row_mask:0xf bank_mask:0xf bound_ctrl:1
	v_pk_add_f32 v[108:109], v[46:47], v[44:45]
	v_pk_add_f32 v[122:123], v[78:79], v[108:109]
	v_pk_add_f32 v[46:47], v[62:63], v[80:81]
	v_pk_add_f32 v[78:79], v[126:127], v[46:47]
	v_pk_add_f32 v[62:63], v[76:77], v[110:111]
	v_pk_add_f32 v[124:125], v[128:129], v[62:63]
	v_pk_add_f32 v[76:77], v[90:91], v[112:113]
	v_pk_add_f32 v[126:127], v[130:131], v[76:77]
	v_pk_add_f32 v[90:91], v[92:93], v[114:115]
	v_pk_add_f32 v[128:129], v[132:133], v[90:91]
	v_pk_add_f32 v[92:93], v[94:95], v[116:117]
	v_pk_add_f32 v[130:131], v[134:135], v[92:93]
	v_pk_add_f32 v[94:95], v[96:97], v[118:119]
	v_pk_add_f32 v[132:133], v[136:137], v[94:95]
	v_pk_add_f32 v[96:97], v[98:99], v[120:121]
	v_pk_add_f32 v[134:135], v[138:139], v[96:97]
	v_pk_fma_f32 v[132:133], v[8:9], v[122:123], v[132:133] op_sel_hi:[0,1,1]
	v_pk_fma_f32 v[134:135], v[8:9], v[78:79], v[134:135] op_sel_hi:[0,1,1]
	v_pk_fma_f32 v[132:133], v[8:9], v[124:125], v[132:133] op_sel:[1,0,0]
	v_pk_fma_f32 v[134:135], v[8:9], v[126:127], v[134:135] op_sel:[1,0,0]
	v_pk_fma_f32 v[132:133], v[10:11], v[128:129], v[132:133] op_sel_hi:[0,1,1]
	v_pk_fma_f32 v[134:135], v[10:11], v[130:131], v[134:135] op_sel_hi:[0,1,1]
	v_cndmask_b32_e64 v98, 0, v1, s[10:11]
	v_cndmask_b32_e64 v99, 0, v1, s[14:15]
	v_cndmask_b32_e64 v136, 0, v1, s[20:21]
	v_cndmask_b32_e64 v137, 0, v1, s[22:23]
	v_pk_fma_f32 v[132:133], v[2:3], v[102:103], v[132:133] op_sel_hi:[1,0,1] neg_lo:[0,0,1] neg_hi:[0,0,1]
	v_pk_fma_f32 v[134:135], v[4:5], v[102:103], v[134:135] op_sel_hi:[1,0,1] neg_lo:[0,0,1] neg_hi:[0,0,1]
	s_add_i32 s4, s34, 8
	s_cmpk_lt_i32 s4, 0x201
	s_cselect_b64 s[12:13], s[0:1], 0
	v_pk_add_f32 v[132:133], v[132:133], v[98:99] neg_lo:[0,1] neg_hi:[0,1]
	v_pk_add_f32 v[134:135], v[134:135], v[136:137] neg_lo:[0,1] neg_hi:[0,1]
	v_pk_mul_f32 v[138:139], v[132:133], v[132:133]
	v_pk_fma_f32 v[138:139], v[134:135], v[134:135], v[138:139]
	v_add_f32_e32 v138, v138, v139
	v_cndmask_b32_e64 v139, 0, v138, s[12:13]
	v_add_f32_e32 v0, v0, v139
	s_waitcnt vmcnt(0)
	v_pk_mul_f32 v[2:3], v[20:21], v[40:41] op_sel_hi:[1,0]
	v_pk_mul_f32 v[4:5], v[24:25], v[40:41] op_sel_hi:[1,0]
	v_pk_mul_f32 v[8:9], v[20:21], v[40:41] op_sel:[0,1]
	v_pk_mul_f32 v[10:11], v[24:25], v[40:41] op_sel:[0,1]
	v_pk_mul_f32 v[48:49], v[20:21], v[42:43] op_sel_hi:[1,0]
	v_pk_mul_f32 v[50:51], v[24:25], v[42:43] op_sel_hi:[1,0]
	v_add_f32_dpp v52, v20, v20 wave_shr:1 row_mask:0xf bank_mask:0xf bound_ctrl:1
	v_add_f32_dpp v53, v21, v21 wave_shr:1 row_mask:0xf bank_mask:0xf bound_ctrl:1
	v_add_f32_dpp v54, v24, v24 wave_shr:1 row_mask:0xf bank_mask:0xf bound_ctrl:1
	v_add_f32_dpp v55, v25, v25 wave_shr:1 row_mask:0xf bank_mask:0xf bound_ctrl:1
	v_add_f32_dpp v78, v2, v2 wave_shr:1 row_mask:0xf bank_mask:0xf bound_ctrl:1
	v_add_f32_dpp v79, v3, v3 wave_shr:1 row_mask:0xf bank_mask:0xf bound_ctrl:1
	v_add_f32_dpp v98, v4, v4 wave_shr:1 row_mask:0xf bank_mask:0xf bound_ctrl:1
	v_add_f32_dpp v99, v5, v5 wave_shr:1 row_mask:0xf bank_mask:0xf bound_ctrl:1
	v_add_f32_dpp v100, v8, v8 wave_shr:1 row_mask:0xf bank_mask:0xf bound_ctrl:1
	v_add_f32_dpp v101, v9, v9 wave_shr:1 row_mask:0xf bank_mask:0xf bound_ctrl:1
	v_add_f32_dpp v102, v10, v10 wave_shr:1 row_mask:0xf bank_mask:0xf bound_ctrl:1
	v_add_f32_dpp v103, v11, v11 wave_shr:1 row_mask:0xf bank_mask:0xf bound_ctrl:1
	v_add_f32_dpp v122, v48, v48 wave_shr:1 row_mask:0xf bank_mask:0xf bound_ctrl:1
	v_add_f32_dpp v123, v49, v49 wave_shr:1 row_mask:0xf bank_mask:0xf bound_ctrl:1
	v_add_f32_dpp v124, v50, v50 wave_shr:1 row_mask:0xf bank_mask:0xf bound_ctrl:1
	v_add_f32_dpp v125, v51, v51 wave_shr:1 row_mask:0xf bank_mask:0xf bound_ctrl:1
	v_add_f32_dpp v52, v20, v52 wave_shl:1 row_mask:0xf bank_mask:0xf bound_ctrl:1
	v_add_f32_dpp v53, v21, v53 wave_shl:1 row_mask:0xf bank_mask:0xf bound_ctrl:1
	v_add_f32_dpp v54, v24, v54 wave_shl:1 row_mask:0xf bank_mask:0xf bound_ctrl:1
	v_add_f32_dpp v55, v25, v55 wave_shl:1 row_mask:0xf bank_mask:0xf bound_ctrl:1
	v_add_f32_dpp v78, v2, v78 wave_shl:1 row_mask:0xf bank_mask:0xf bound_ctrl:1
	v_add_f32_dpp v79, v3, v79 wave_shl:1 row_mask:0xf bank_mask:0xf bound_ctrl:1
	v_add_f32_dpp v98, v4, v98 wave_shl:1 row_mask:0xf bank_mask:0xf bound_ctrl:1
	v_add_f32_dpp v99, v5, v99 wave_shl:1 row_mask:0xf bank_mask:0xf bound_ctrl:1
	v_add_f32_dpp v100, v8, v100 wave_shl:1 row_mask:0xf bank_mask:0xf bound_ctrl:1
	v_add_f32_dpp v101, v9, v101 wave_shl:1 row_mask:0xf bank_mask:0xf bound_ctrl:1
	v_add_f32_dpp v102, v10, v102 wave_shl:1 row_mask:0xf bank_mask:0xf bound_ctrl:1
	v_add_f32_dpp v103, v11, v103 wave_shl:1 row_mask:0xf bank_mask:0xf bound_ctrl:1
	v_add_f32_dpp v122, v48, v122 wave_shl:1 row_mask:0xf bank_mask:0xf bound_ctrl:1
	v_add_f32_dpp v123, v49, v123 wave_shl:1 row_mask:0xf bank_mask:0xf bound_ctrl:1
	v_add_f32_dpp v124, v50, v124 wave_shl:1 row_mask:0xf bank_mask:0xf bound_ctrl:1
	v_add_f32_dpp v125, v51, v125 wave_shl:1 row_mask:0xf bank_mask:0xf bound_ctrl:1
	s_barrier
	ds_read_b128 v[8:11], v23 offset:3072
	ds_read_b128 v[48:51], v23 offset:4096
	ds_read_b128 v[128:131], v23 offset:5120
	v_pk_add_f32 v[2:3], v[30:31], v[52:53]
	v_pk_add_f32 v[4:5], v[74:75], v[54:55]
	v_pk_add_f32 v[30:31], v[82:83], v[78:79]
	v_pk_add_f32 v[74:75], v[84:85], v[98:99]
	v_pk_add_f32 v[82:83], v[86:87], v[100:101]
	v_pk_add_f32 v[84:85], v[88:89], v[102:103]
	v_pk_add_f32 v[86:87], v[104:105], v[122:123]
	v_pk_add_f32 v[88:89], v[106:107], v[124:125]
	s_waitcnt lgkmcnt(2)
	v_pk_fma_f32 v[30:31], v[8:9], v[2:3], v[30:31] op_sel_hi:[0,1,1] neg_lo:[1,0,0] neg_hi:[1,0,0]
	v_pk_fma_f32 v[74:75], v[8:9], v[4:5], v[74:75] op_sel_hi:[0,1,1] neg_lo:[1,0,0] neg_hi:[1,0,0]
	v_pk_fma_f32 v[82:83], v[8:9], v[2:3], v[82:83] op_sel:[1,0,0] neg_lo:[1,0,0] neg_hi:[1,0,0]
	v_pk_fma_f32 v[84:85], v[8:9], v[4:5], v[84:85] op_sel:[1,0,0] neg_lo:[1,0,0] neg_hi:[1,0,0]
	v_pk_fma_f32 v[86:87], v[10:11], v[2:3], v[86:87] op_sel_hi:[0,1,1] neg_lo:[1,0,0] neg_hi:[1,0,0]
	v_pk_fma_f32 v[88:89], v[10:11], v[4:5], v[88:89] op_sel_hi:[0,1,1] neg_lo:[1,0,0] neg_hi:[1,0,0]
	v_pk_mul_f32 v[104:105], v[10:11], v[30:31] op_sel:[1,0]
	v_pk_mul_f32 v[132:133], v[10:11], v[74:75] op_sel:[1,0]
	s_waitcnt lgkmcnt(1)
	v_pk_mul_f32 v[106:107], v[48:49], v[30:31] op_sel_hi:[0,1]
	v_pk_mul_f32 v[134:135], v[48:49], v[74:75] op_sel_hi:[0,1]
	v_pk_mul_f32 v[126:127], v[48:49], v[30:31] op_sel:[1,0]
	v_pk_mul_f32 v[136:137], v[48:49], v[74:75] op_sel:[1,0]
	v_pk_fma_f32 v[104:105], v[48:49], v[82:83], v[104:105] op_sel_hi:[0,1,1]
	v_pk_fma_f32 v[132:133], v[48:49], v[84:85], v[132:133] op_sel_hi:[0,1,1]
	v_pk_fma_f32 v[106:107], v[50:51], v[82:83], v[106:107] op_sel_hi:[0,1,1]
	v_pk_fma_f32 v[134:135], v[50:51], v[84:85], v[134:135] op_sel_hi:[0,1,1]
	v_pk_fma_f32 v[126:127], v[50:51], v[82:83], v[126:127] op_sel:[1,0,0]
	v_pk_fma_f32 v[136:137], v[50:51], v[84:85], v[136:137] op_sel:[1,0,0]
	v_pk_fma_f32 v[104:105], v[48:49], v[86:87], v[104:105] op_sel:[1,0,0]
	v_pk_fma_f32 v[132:133], v[48:49], v[88:89], v[132:133] op_sel:[1,0,0]
	v_pk_fma_f32 v[106:107], v[50:51], v[86:87], v[106:107] op_sel:[1,0,0]
	v_pk_fma_f32 v[134:135], v[50:51], v[88:89], v[134:135] op_sel:[1,0,0]
	s_waitcnt lgkmcnt(0)
	v_pk_fma_f32 v[126:127], v[128:129], v[86:87], v[126:127] op_sel_hi:[0,1,1]
	v_pk_fma_f32 v[136:137], v[128:129], v[88:89], v[136:137] op_sel_hi:[0,1,1]
	v_pk_mul_f32 v[138:139], v[8:9], v[104:105] op_sel_hi:[0,1]
	v_pk_mul_f32 v[140:141], v[8:9], v[132:133] op_sel_hi:[0,1]
	v_pk_fma_f32 v[138:139], v[8:9], v[106:107], v[138:139] op_sel:[1,0,0]
	v_pk_fma_f32 v[140:141], v[8:9], v[134:135], v[140:141] op_sel:[1,0,0]
	v_pk_fma_f32 v[138:139], v[10:11], v[126:127], v[138:139] op_sel_hi:[0,1,1]
	v_pk_fma_f32 v[140:141], v[10:11], v[136:137], v[140:141] op_sel_hi:[0,1,1]
	v_pk_fma_f32 v[138:139], v[128:129], v[2:3], v[138:139] op_sel:[1,0,0] neg_lo:[0,0,1] neg_hi:[0,0,1]
	v_pk_fma_f32 v[140:141], v[128:129], v[4:5], v[140:141] op_sel:[1,0,0] neg_lo:[0,0,1] neg_hi:[0,0,1]
	v_cmp_eq_u32_e64 s[10:11], 1, v131
	v_cmp_eq_u32_e64 s[14:15], 2, v131
	v_cmp_eq_u32_e64 s[20:21], 3, v131
	v_cmp_eq_u32_e64 s[22:23], 4, v131
	v_add_f32_dpp v2, v104, v104 wave_shr:1 row_mask:0xf bank_mask:0xf bound_ctrl:1
	v_add_f32_dpp v3, v105, v105 wave_shr:1 row_mask:0xf bank_mask:0xf bound_ctrl:1
	v_add_f32_dpp v4, v132, v132 wave_shr:1 row_mask:0xf bank_mask:0xf bound_ctrl:1
	v_add_f32_dpp v5, v133, v133 wave_shr:1 row_mask:0xf bank_mask:0xf bound_ctrl:1
	v_add_f32_dpp v30, v106, v106 wave_shr:1 row_mask:0xf bank_mask:0xf bound_ctrl:1
	v_add_f32_dpp v31, v107, v107 wave_shr:1 row_mask:0xf bank_mask:0xf bound_ctrl:1
	v_add_f32_dpp v74, v134, v134 wave_shr:1 row_mask:0xf bank_mask:0xf bound_ctrl:1
	v_add_f32_dpp v75, v135, v135 wave_shr:1 row_mask:0xf bank_mask:0xf bound_ctrl:1
	v_add_f32_dpp v82, v126, v126 wave_shr:1 row_mask:0xf bank_mask:0xf bound_ctrl:1
	v_add_f32_dpp v83, v127, v127 wave_shr:1 row_mask:0xf bank_mask:0xf bound_ctrl:1
	v_add_f32_dpp v84, v136, v136 wave_shr:1 row_mask:0xf bank_mask:0xf bound_ctrl:1
	v_add_f32_dpp v85, v137, v137 wave_shr:1 row_mask:0xf bank_mask:0xf bound_ctrl:1
	v_add_f32_dpp v86, v138, v138 wave_shr:1 row_mask:0xf bank_mask:0xf bound_ctrl:1
	v_add_f32_dpp v87, v139, v139 wave_shr:1 row_mask:0xf bank_mask:0xf bound_ctrl:1
	v_add_f32_dpp v88, v140, v140 wave_shr:1 row_mask:0xf bank_mask:0xf bound_ctrl:1
	v_add_f32_dpp v89, v141, v141 wave_shr:1 row_mask:0xf bank_mask:0xf bound_ctrl:1
	v_add_f32_dpp v2, v104, v2 wave_shl:1 row_mask:0xf bank_mask:0xf bound_ctrl:1
	v_add_f32_dpp v3, v105, v3 wave_shl:1 row_mask:0xf bank_mask:0xf bound_ctrl:1
	v_add_f32_dpp v4, v132, v4 wave_shl:1 row_mask:0xf bank_mask:0xf bound_ctrl:1
	v_add_f32_dpp v5, v133, v5 wave_shl:1 row_mask:0xf bank_mask:0xf bound_ctrl:1
	v_add_f32_dpp v30, v106, v30 wave_shl:1 row_mask:0xf bank_mask:0xf bound_ctrl:1
	v_add_f32_dpp v31, v107, v31 wave_shl:1 row_mask:0xf bank_mask:0xf bound_ctrl:1
	v_add_f32_dpp v74, v134, v74 wave_shl:1 row_mask:0xf bank_mask:0xf bound_ctrl:1
	v_add_f32_dpp v75, v135, v75 wave_shl:1 row_mask:0xf bank_mask:0xf bound_ctrl:1
	v_add_f32_dpp v82, v126, v82 wave_shl:1 row_mask:0xf bank_mask:0xf bound_ctrl:1
	v_add_f32_dpp v83, v127, v83 wave_shl:1 row_mask:0xf bank_mask:0xf bound_ctrl:1
	v_add_f32_dpp v84, v136, v84 wave_shl:1 row_mask:0xf bank_mask:0xf bound_ctrl:1
	v_add_f32_dpp v85, v137, v85 wave_shl:1 row_mask:0xf bank_mask:0xf bound_ctrl:1
	v_add_f32_dpp v86, v138, v86 wave_shl:1 row_mask:0xf bank_mask:0xf bound_ctrl:1
	v_add_f32_dpp v87, v139, v87 wave_shl:1 row_mask:0xf bank_mask:0xf bound_ctrl:1
	v_add_f32_dpp v88, v140, v88 wave_shl:1 row_mask:0xf bank_mask:0xf bound_ctrl:1
	v_add_f32_dpp v89, v141, v89 wave_shl:1 row_mask:0xf bank_mask:0xf bound_ctrl:1
	v_pk_add_f32 v[104:105], v[108:109], v[2:3]
	v_pk_add_f32 v[106:107], v[46:47], v[4:5]
	v_pk_add_f32 v[46:47], v[62:63], v[30:31]
	v_pk_add_f32 v[62:63], v[76:77], v[74:75]
	v_pk_add_f32 v[76:77], v[90:91], v[82:83]
	v_pk_add_f32 v[90:91], v[92:93], v[84:85]
	v_pk_add_f32 v[92:93], v[94:95], v[86:87]
	v_pk_add_f32 v[94:95], v[96:97], v[88:89]
	v_pk_fma_f32 v[92:93], v[32:33], v[104:105], v[92:93] op_sel_hi:[0,1,1]
	v_pk_fma_f32 v[94:95], v[32:33], v[106:107], v[94:95] op_sel_hi:[0,1,1]
	v_pk_fma_f32 v[92:93], v[32:33], v[46:47], v[92:93] op_sel:[1,0,0]
	v_pk_fma_f32 v[94:95], v[32:33], v[62:63], v[94:95] op_sel:[1,0,0]
	v_pk_fma_f32 v[92:93], v[34:35], v[76:77], v[92:93] op_sel_hi:[0,1,1]
	v_pk_fma_f32 v[94:95], v[34:35], v[90:91], v[94:95] op_sel_hi:[0,1,1]
	v_cndmask_b32_e64 v96, 0, v1, s[10:11]
	v_cndmask_b32_e64 v97, 0, v1, s[14:15]
	v_cndmask_b32_e64 v108, 0, v1, s[20:21]
	v_cndmask_b32_e64 v109, 0, v1, s[22:23]
	v_pk_fma_f32 v[92:93], v[6:7], v[130:131], v[92:93] op_sel_hi:[1,0,1] neg_lo:[0,0,1] neg_hi:[0,0,1]
	v_pk_fma_f32 v[94:95], v[12:13], v[130:131], v[94:95] op_sel_hi:[1,0,1] neg_lo:[0,0,1] neg_hi:[0,0,1]
	s_add_i32 s4, s34, 9
	s_cmpk_lt_i32 s4, 0x201
	s_cselect_b64 s[12:13], s[0:1], 0
	v_pk_add_f32 v[92:93], v[92:93], v[96:97] neg_lo:[0,1] neg_hi:[0,1]
	v_pk_add_f32 v[94:95], v[94:95], v[108:109] neg_lo:[0,1] neg_hi:[0,1]
	v_pk_mul_f32 v[126:127], v[92:93], v[92:93]
	v_pk_fma_f32 v[126:127], v[94:95], v[94:95], v[126:127]
	v_add_f32_e32 v126, v126, v127
	v_cndmask_b32_e64 v127, 0, v126, s[12:13]
	v_add_f32_e32 v0, v0, v127

	.amdhsa_kernel _Z16closed_form_mainPKfS0_PKiPf
		.amdhsa_group_segment_fixed_size 6144
		.amdhsa_private_segment_fixed_size 0
		.amdhsa_kernarg_size 32
		.amdhsa_user_sgpr_count 2
		.amdhsa_user_sgpr_dispatch_ptr 0
		.amdhsa_user_sgpr_queue_ptr 0
		.amdhsa_user_sgpr_kernarg_segment_ptr 1
		.amdhsa_user_sgpr_dispatch_id 0
		.amdhsa_user_sgpr_kernarg_preload_length 0
		.amdhsa_user_sgpr_kernarg_preload_offset 0
		.amdhsa_user_sgpr_private_segment_size 0
		.amdhsa_uses_dynamic_stack 0
		.amdhsa_enable_private_segment 0
		.amdhsa_system_sgpr_workgroup_id_x 1
		.amdhsa_system_sgpr_workgroup_id_y 0
		.amdhsa_system_sgpr_workgroup_id_z 0
		.amdhsa_system_sgpr_workgroup_info 0
		.amdhsa_system_vgpr_workitem_id 0
		.amdhsa_next_free_vgpr 158
		.amdhsa_next_free_sgpr 44
		.amdhsa_accum_offset 160
		.amdhsa_reserve_vcc 1
		.amdhsa_float_round_mode_32 0
		.amdhsa_float_round_mode_16_64 0
		.amdhsa_float_denorm_mode_32 3
		.amdhsa_float_denorm_mode_16_64 3
		.amdhsa_dx10_clamp 1
		.amdhsa_ieee_mode 1
		.amdhsa_fp16_overflow 0
		.amdhsa_tg_split 0
		.amdhsa_exception_fp_ieee_invalid_op 0
		.amdhsa_exception_fp_denorm_src 0
		.amdhsa_exception_fp_ieee_div_zero 0
		.amdhsa_exception_fp_ieee_overflow 0
		.amdhsa_exception_fp_ieee_underflow 0
		.amdhsa_exception_fp_ieee_inexact 0
		.amdhsa_exception_int_div_zero 0
	.end_amdhsa_kernel

amdhsa.kernels:
  - .agpr_count:     0
    .args:
      - .address_space:  global
        .offset:         0
        .size:           8
        .value_kind:     global_buffer
      - .address_space:  global
        .offset:         8
        .size:           8
        .value_kind:     global_buffer
      - .address_space:  global
        .offset:         16
        .size:           8
        .value_kind:     global_buffer
      - .address_space:  global
        .offset:         24
        .size:           8
        .value_kind:     global_buffer
    .group_segment_fixed_size: 6144
    .kernarg_segment_align: 8
    .kernarg_segment_size: 32
    .language:       OpenCL C
    .language_version:
      - 2
      - 0
    .max_flat_workgroup_size: 128
    .name:           _Z16closed_form_mainPKfS0_PKiPf
    .private_segment_fixed_size: 0
    .sgpr_count:     50
    .sgpr_spill_count: 0
    .symbol:         _Z16closed_form_mainPKfS0_PKiPf.kd
    .uniform_work_group_size: 1
    .uses_dynamic_stack: false
    .vgpr_count:     158
    .vgpr_spill_count: 0
    .wavefront_size: 64
  - .agpr_count:     0
    .args:
      - .actual_access:  read_only
        .address_space:  global
        .offset:         0
        .size:           8
        .value_kind:     global_buffer
      - .actual_access:  write_only
        .address_space:  global
        .offset:         8
        .size:           8
        .value_kind:     global_buffer
    .group_segment_fixed_size: 0
    .kernarg_segment_align: 8
    .kernarg_segment_size: 16
    .language:       OpenCL C
    .language_version:
      - 2
      - 0
    .max_flat_workgroup_size: 64
    .name:           _Z17closed_form_finalPK15HIP_vector_typeIfLj4EEPf
    .private_segment_fixed_size: 0
    .sgpr_count:     10
    .sgpr_spill_count: 0
    .symbol:         _Z17closed_form_finalPK15HIP_vector_typeIfLj4EEPf.kd
    .uniform_work_group_size: 1
    .uses_dynamic_stack: false
    .vgpr_count:     36
    .vgpr_spill_count: 0
    .wavefront_size: 64
